# load width: the hand-written post phases use dwordx4 loads and stores (each lane owns 8 consecutive elements per 512-element chunk) instead of dwordx2; otherwise e1
# baseline (speedup 1.0000x reference)
.Lmp_entry:
	v_mbcnt_lo_u32_b32 v162, -1, 0
	v_mbcnt_hi_u32_b32 v162, -1, v162
	v_lshlrev_b32_e32 v163, 4, v162
	v_lshlrev_b32_e32 v162, 5, v162
	v_readlane_b32 s4, v252, 0
	v_readlane_b32 s5, v252, 1
	v_readlane_b32 s6, v252, 2
	v_readlane_b32 s7, v252, 3
	v_readlane_b32 s8, v252, 4
	v_readlane_b32 s9, v252, 5
	s_nop 3
	s_load_dwordx2 s[10:11], s[8:9], 0x0
	s_load_dwordx2 s[90:91], s[8:9], 0x28
	s_lshr_b32 s18, s44, 6
	s_lshl_b32 s19, s101, 7
	s_add_u32 s18, s18, s19
	s_lshr_b32 s19, s101, 5
	s_lshl_b32 s76, s18, 12
	s_lshl_b32 s77, s18, 13
	s_lshl_b32 s88, s68, 3
	s_add_u32 s88, s88, s19
	s_mul_i32 s88, s88, 0xc000
	s_waitcnt lgkmcnt(0)
	s_add_u32 s72, s6, 0x19400000
	s_addc_u32 s73, s7, 0
	s_add_u32 s72, s72, s76
	s_addc_u32 s73, s73, 0
	s_add_u32 s94, s4, 0x8000000
	s_addc_u32 s95, s5, 0
	s_add_u32 s94, s94, s76
	s_addc_u32 s95, s95, 0
	s_add_u32 s56, s6, 0x100000
	s_addc_u32 s57, s7, 0
	s_add_u32 s56, s56, s88
	s_addc_u32 s57, s57, 0
	s_cmp_eq_u32 s99, 0
	s_cbranch_scc0 .Lmp_site1
	s_add_u32 s18, s56, 0x4000
	s_addc_u32 s19, s57, 0
	s_add_u32 s20, s56, 0x6000
	s_addc_u32 s21, s57, 0
	s_add_u32 s30, s56, 0x8000
	s_addc_u32 s31, s57, 0
	s_lshl_b32 s88, s68, 15
	s_add_u32 s88, s88, 0x2000
	s_add_u32 s34, s90, s88
	s_addc_u32 s35, s91, 0
	s_add_u32 s90, s34, 0x2000
	s_addc_u32 s91, s35, 0
	s_add_u32 s56, s6, 0x31400000
	s_addc_u32 s57, s7, 0
	s_add_u32 s56, s56, s76
	s_addc_u32 s57, s57, 0
	s_mov_b64 s[58:59], s[94:95]
	s_mov_b64 s[70:71], s[94:95]
	s_cmp_eq_u32 s68, 3
	s_cbranch_scc0 .Lmp_s0_notlast
	s_add_u32 s70, s6, 0x29400000
	s_addc_u32 s71, s7, 0
	s_add_u32 s70, s70, s76
	s_addc_u32 s71, s71, 0

.Lmp_vec:
	s_add_u32 s36, s18, 0x1000
	s_addc_u32 s37, s19, 0
	global_load_dwordx4 v[32:35], v162, s[18:19]
	global_load_dwordx4 v[36:39], v162, s[18:19] offset:16
	global_load_dwordx4 v[40:43], v162, s[18:19] offset:2048
	global_load_dwordx4 v[44:47], v162, s[18:19] offset:2064
	global_load_dwordx4 v[48:51], v162, s[36:37]
	global_load_dwordx4 v[52:55], v162, s[36:37] offset:16
	global_load_dwordx4 v[56:59], v162, s[36:37] offset:2048
	global_load_dwordx4 v[60:63], v162, s[36:37] offset:2064
	s_add_u32 s36, s34, 0x1000
	s_addc_u32 s37, s35, 0
	global_load_dwordx4 v[128:131], v162, s[34:35]
	global_load_dwordx4 v[132:135], v162, s[34:35] offset:16
	global_load_dwordx4 v[136:139], v162, s[34:35] offset:2048
	global_load_dwordx4 v[140:143], v162, s[34:35] offset:2064
	global_load_dwordx4 v[144:147], v162, s[36:37]
	global_load_dwordx4 v[148:151], v162, s[36:37] offset:16
	global_load_dwordx4 v[152:155], v162, s[36:37] offset:2048
	global_load_dwordx4 v[156:159], v162, s[36:37] offset:2064
	s_waitcnt vmcnt(0)
	v_mul_f32_e32 v32, v32, v128
	v_mul_f32_e32 v33, v33, v129
	v_mul_f32_e32 v34, v34, v130
	v_mul_f32_e32 v35, v35, v131
	v_mul_f32_e32 v36, v36, v132
	v_mul_f32_e32 v37, v37, v133
	v_mul_f32_e32 v38, v38, v134
	v_mul_f32_e32 v39, v39, v135
	v_mul_f32_e32 v40, v40, v136
	v_mul_f32_e32 v41, v41, v137
	v_mul_f32_e32 v42, v42, v138
	v_mul_f32_e32 v43, v43, v139
	v_mul_f32_e32 v44, v44, v140
	v_mul_f32_e32 v45, v45, v141
	v_mul_f32_e32 v46, v46, v142
	v_mul_f32_e32 v47, v47, v143
	v_mul_f32_e32 v48, v48, v144
	v_mul_f32_e32 v49, v49, v145
	v_mul_f32_e32 v50, v50, v146
	v_mul_f32_e32 v51, v51, v147
	v_mul_f32_e32 v52, v52, v148
	v_mul_f32_e32 v53, v53, v149
	v_mul_f32_e32 v54, v54, v150
	v_mul_f32_e32 v55, v55, v151
	v_mul_f32_e32 v56, v56, v152
	v_mul_f32_e32 v57, v57, v153
	v_mul_f32_e32 v58, v58, v154
	v_mul_f32_e32 v59, v59, v155
	v_mul_f32_e32 v60, v60, v156
	v_mul_f32_e32 v61, v61, v157
	v_mul_f32_e32 v62, v62, v158
	v_mul_f32_e32 v63, v63, v159
	s_cmp_eq_u32 s99, 1
	s_cselect_b32 s88, s68, 0
	s_cmp_eq_u32 s88, 3
	s_cbranch_scc1 .Lmp_noh
	s_add_u32 s36, s90, 0x1000
	s_addc_u32 s37, s91, 0
	global_load_dwordx4 v[64:67], v162, s[90:91]
	global_load_dwordx4 v[68:71], v162, s[90:91] offset:16
	global_load_dwordx4 v[72:75], v162, s[90:91] offset:2048
	global_load_dwordx4 v[76:79], v162, s[90:91] offset:2064
	global_load_dwordx4 v[80:83], v162, s[36:37]
	global_load_dwordx4 v[84:87], v162, s[36:37] offset:16
	global_load_dwordx4 v[88:91], v162, s[36:37] offset:2048
	global_load_dwordx4 v[92:95], v162, s[36:37] offset:2064
	s_add_u32 s36, s30, 0x1000
	s_addc_u32 s37, s31, 0
	global_load_dwordx4 v[166:169], v162, s[30:31]
	global_load_dwordx4 v[170:173], v162, s[30:31] offset:16
	global_load_dwordx4 v[174:177], v162, s[30:31] offset:2048
	global_load_dwordx4 v[178:181], v162, s[30:31] offset:2064
	global_load_dwordx4 v[182:185], v162, s[36:37]
	global_load_dwordx4 v[186:189], v162, s[36:37] offset:16
	global_load_dwordx4 v[190:193], v162, s[36:37] offset:2048
	global_load_dwordx4 v[194:197], v162, s[36:37] offset:2064
	s_add_u32 s36, s20, 0x1000
	s_addc_u32 s37, s21, 0
	global_load_dwordx4 v[96:99], v162, s[20:21]
	global_load_dwordx4 v[100:103], v162, s[20:21] offset:16
	global_load_dwordx4 v[104:107], v162, s[20:21] offset:2048
	global_load_dwordx4 v[108:111], v162, s[20:21] offset:2064
	global_load_dwordx4 v[112:115], v162, s[36:37]
	global_load_dwordx4 v[116:119], v162, s[36:37] offset:16
	global_load_dwordx4 v[120:123], v162, s[36:37] offset:2048
	global_load_dwordx4 v[124:127], v162, s[36:37] offset:2064
	s_waitcnt vmcnt(8)
	v_add_f32_e32 v166, 1.0, v166
	v_add_f32_e32 v167, 1.0, v167
	v_add_f32_e32 v168, 1.0, v168
	v_add_f32_e32 v169, 1.0, v169
	v_add_f32_e32 v170, 1.0, v170
	v_add_f32_e32 v171, 1.0, v171
	v_add_f32_e32 v172, 1.0, v172
	v_add_f32_e32 v173, 1.0, v173
	v_add_f32_e32 v174, 1.0, v174
	v_add_f32_e32 v175, 1.0, v175
	v_add_f32_e32 v176, 1.0, v176
	v_add_f32_e32 v177, 1.0, v177
	v_add_f32_e32 v178, 1.0, v178
	v_add_f32_e32 v179, 1.0, v179
	v_add_f32_e32 v180, 1.0, v180
	v_add_f32_e32 v181, 1.0, v181
	v_add_f32_e32 v182, 1.0, v182
	v_add_f32_e32 v183, 1.0, v183
	v_add_f32_e32 v184, 1.0, v184
	v_add_f32_e32 v185, 1.0, v185
	v_add_f32_e32 v186, 1.0, v186
	v_add_f32_e32 v187, 1.0, v187
	v_add_f32_e32 v188, 1.0, v188
	v_add_f32_e32 v189, 1.0, v189
	v_add_f32_e32 v190, 1.0, v190
	v_add_f32_e32 v191, 1.0, v191
	v_add_f32_e32 v192, 1.0, v192
	v_add_f32_e32 v193, 1.0, v193
	v_add_f32_e32 v194, 1.0, v194
	v_add_f32_e32 v195, 1.0, v195
	v_add_f32_e32 v196, 1.0, v196
	v_add_f32_e32 v197, 1.0, v197
	v_mul_f32_e32 v64, v64, v166
	v_mul_f32_e32 v65, v65, v167
	v_mul_f32_e32 v66, v66, v168
	v_mul_f32_e32 v67, v67, v169
	v_mul_f32_e32 v68, v68, v170
	v_mul_f32_e32 v69, v69, v171
	v_mul_f32_e32 v70, v70, v172
	v_mul_f32_e32 v71, v71, v173
	v_mul_f32_e32 v72, v72, v174
	v_mul_f32_e32 v73, v73, v175
	v_mul_f32_e32 v74, v74, v176
	v_mul_f32_e32 v75, v75, v177
	v_mul_f32_e32 v76, v76, v178
	v_mul_f32_e32 v77, v77, v179
	v_mul_f32_e32 v78, v78, v180
	v_mul_f32_e32 v79, v79, v181
	v_mul_f32_e32 v80, v80, v182
	v_mul_f32_e32 v81, v81, v183
	v_mul_f32_e32 v82, v82, v184
	v_mul_f32_e32 v83, v83, v185
	v_mul_f32_e32 v84, v84, v186
	v_mul_f32_e32 v85, v85, v187
	v_mul_f32_e32 v86, v86, v188
	v_mul_f32_e32 v87, v87, v189
	v_mul_f32_e32 v88, v88, v190
	v_mul_f32_e32 v89, v89, v191
	v_mul_f32_e32 v90, v90, v192
	v_mul_f32_e32 v91, v91, v193
	v_mul_f32_e32 v92, v92, v194
	v_mul_f32_e32 v93, v93, v195
	v_mul_f32_e32 v94, v94, v196
	v_mul_f32_e32 v95, v95, v197
	s_waitcnt vmcnt(0)

.Lmp_V1:
	global_load_dwordx4 v[128:131], v163, s[56:57]
	global_load_dwordx4 v[132:135], v163, s[56:57] offset:1024
	global_load_dwordx4 v[136:139], v163, s[56:57] offset:2048
	global_load_dwordx4 v[140:143], v163, s[56:57] offset:3072
	global_load_dwordx4 v[144:147], v163, s[58:59]
	global_load_dwordx4 v[148:151], v163, s[58:59] offset:1024
	global_load_dwordx4 v[152:155], v163, s[58:59] offset:2048
	global_load_dwordx4 v[156:159], v163, s[58:59] offset:3072
	s_add_u32 s58, s58, 0x8000
	s_addc_u32 s59, s59, 0
	s_add_u32 s56, s56, 0x8000
	s_addc_u32 s57, s57, 0
	global_load_dwordx4 v[166:169], v163, s[56:57]
	global_load_dwordx4 v[170:173], v163, s[56:57] offset:1024
	global_load_dwordx4 v[174:177], v163, s[56:57] offset:2048
	global_load_dwordx4 v[178:181], v163, s[56:57] offset:3072
	global_load_dwordx4 v[182:185], v163, s[58:59]
	global_load_dwordx4 v[186:189], v163, s[58:59] offset:1024
	global_load_dwordx4 v[190:193], v163, s[58:59] offset:2048
	global_load_dwordx4 v[194:197], v163, s[58:59] offset:3072
	s_add_u32 s58, s58, 0x8000
	s_addc_u32 s59, s59, 0
	s_add_u32 s56, s56, 0x8000
	s_addc_u32 s57, s57, 0
	s_waitcnt vmcnt(8)
.Lmp_V1_loop:
	s_waitcnt vmcnt(16)
	v_mov_b32_e32 v250, 0
	v_mov_b32_e32 v251, 0
	v_lshlrev_b32_e32 v246, 16, v128
	v_and_b32_e32 v247, 0xffff0000, v128
	v_lshlrev_b32_e32 v248, 16, v129
	v_and_b32_e32 v249, 0xffff0000, v129
	v_fmac_f32_e32 v250, v246, v246
	v_fmac_f32_e32 v251, v247, v247
	v_fmac_f32_e32 v250, v248, v248
	v_fmac_f32_e32 v251, v249, v249
	v_lshlrev_b32_e32 v246, 16, v130
	v_and_b32_e32 v247, 0xffff0000, v130
	v_lshlrev_b32_e32 v248, 16, v131
	v_and_b32_e32 v249, 0xffff0000, v131
	v_fmac_f32_e32 v250, v246, v246
	v_fmac_f32_e32 v251, v247, v247
	v_fmac_f32_e32 v250, v248, v248
	v_fmac_f32_e32 v251, v249, v249
	v_lshlrev_b32_e32 v246, 16, v132
	v_and_b32_e32 v247, 0xffff0000, v132
	v_lshlrev_b32_e32 v248, 16, v133
	v_and_b32_e32 v249, 0xffff0000, v133
	v_fmac_f32_e32 v250, v246, v246
	v_fmac_f32_e32 v251, v247, v247
	v_fmac_f32_e32 v250, v248, v248
	v_fmac_f32_e32 v251, v249, v249
	v_lshlrev_b32_e32 v246, 16, v134
	v_and_b32_e32 v247, 0xffff0000, v134
	v_lshlrev_b32_e32 v248, 16, v135
	v_and_b32_e32 v249, 0xffff0000, v135
	v_fmac_f32_e32 v250, v246, v246
	v_fmac_f32_e32 v251, v247, v247
	v_fmac_f32_e32 v250, v248, v248
	v_fmac_f32_e32 v251, v249, v249
	v_lshlrev_b32_e32 v246, 16, v136
	v_and_b32_e32 v247, 0xffff0000, v136
	v_lshlrev_b32_e32 v248, 16, v137
	v_and_b32_e32 v249, 0xffff0000, v137
	v_fmac_f32_e32 v250, v246, v246
	v_fmac_f32_e32 v251, v247, v247
	v_fmac_f32_e32 v250, v248, v248
	v_fmac_f32_e32 v251, v249, v249
	v_lshlrev_b32_e32 v246, 16, v138
	v_and_b32_e32 v247, 0xffff0000, v138
	v_lshlrev_b32_e32 v248, 16, v139
	v_and_b32_e32 v249, 0xffff0000, v139
	v_fmac_f32_e32 v250, v246, v246
	v_fmac_f32_e32 v251, v247, v247
	v_fmac_f32_e32 v250, v248, v248
	v_fmac_f32_e32 v251, v249, v249
	v_lshlrev_b32_e32 v246, 16, v140
	v_and_b32_e32 v247, 0xffff0000, v140
	v_lshlrev_b32_e32 v248, 16, v141
	v_and_b32_e32 v249, 0xffff0000, v141
	v_fmac_f32_e32 v250, v246, v246
	v_fmac_f32_e32 v251, v247, v247
	v_fmac_f32_e32 v250, v248, v248
	v_fmac_f32_e32 v251, v249, v249
	v_lshlrev_b32_e32 v246, 16, v142
	v_and_b32_e32 v247, 0xffff0000, v142
	v_lshlrev_b32_e32 v248, 16, v143
	v_and_b32_e32 v249, 0xffff0000, v143
	v_fmac_f32_e32 v250, v246, v246
	v_fmac_f32_e32 v251, v247, v247
	v_fmac_f32_e32 v250, v248, v248
	v_fmac_f32_e32 v251, v249, v249
	v_add_f32_e32 v250, v250, v251
	s_nop 1
	v_add_f32_dpp v218, v250, v250 quad_perm:[1,0,3,2] row_mask:0xf bank_mask:0xf bound_ctrl:1
	s_nop 1
	v_add_f32_dpp v218, v218, v218 quad_perm:[2,3,0,1] row_mask:0xf bank_mask:0xf bound_ctrl:1
	s_nop 1
	v_add_f32_dpp v218, v218, v218 row_ror:4 row_mask:0xf bank_mask:0xf bound_ctrl:1
	s_nop 1
	v_add_f32_dpp v218, v218, v218 row_ror:8 row_mask:0xf bank_mask:0xf bound_ctrl:1
	s_nop 1
	v_readlane_b32 s8, v218, 0
	v_readlane_b32 s9, v218, 16
	v_readlane_b32 s10, v218, 32
	v_readlane_b32 s11, v218, 48
	s_nop 1
	v_mov_b32_e32 v218, s8
	v_add_f32_e32 v218, s9, v218
	v_mov_b32_e32 v219, s10
	v_add_f32_e32 v219, s11, v219
	v_add_f32_e32 v218, v218, v219
	v_mul_f32_e32 v218, 0x3a000000, v218
	v_add_f32_e32 v218, 0x358637bd, v218
	v_rsq_f32_e32 v218, v218
	s_nop 0
	v_lshlrev_b32_e32 v246, 16, v128
	v_and_b32_e32 v247, 0xffff0000, v128
	v_lshlrev_b32_e32 v248, 16, v129
	v_and_b32_e32 v249, 0xffff0000, v129
	v_mul_f32_e32 v246, v246, v218
	v_mul_f32_e32 v247, v247, v218
	v_mul_f32_e32 v248, v248, v218
	v_mul_f32_e32 v249, v249, v218
	v_lshlrev_b32_e32 v0, 16, v144
	v_and_b32_e32 v1, 0xffff0000, v144
	v_lshlrev_b32_e32 v2, 16, v145
	v_and_b32_e32 v3, 0xffff0000, v145
	v_fmac_f32_e32 v0, v246, v32
	v_fmac_f32_e32 v1, v247, v33
	v_fmac_f32_e32 v2, v248, v34
	v_fmac_f32_e32 v3, v249, v35
	v_lshlrev_b32_e32 v246, 16, v130
	v_and_b32_e32 v247, 0xffff0000, v130
	v_lshlrev_b32_e32 v248, 16, v131
	v_and_b32_e32 v249, 0xffff0000, v131
	v_mul_f32_e32 v246, v246, v218
	v_mul_f32_e32 v247, v247, v218
	v_mul_f32_e32 v248, v248, v218
	v_mul_f32_e32 v249, v249, v218
	v_lshlrev_b32_e32 v4, 16, v146
	v_and_b32_e32 v5, 0xffff0000, v146
	v_lshlrev_b32_e32 v6, 16, v147
	v_and_b32_e32 v7, 0xffff0000, v147
	v_fmac_f32_e32 v4, v246, v36
	v_fmac_f32_e32 v5, v247, v37
	v_fmac_f32_e32 v6, v248, v38
	v_fmac_f32_e32 v7, v249, v39
	v_lshlrev_b32_e32 v246, 16, v132
	v_and_b32_e32 v247, 0xffff0000, v132
	v_lshlrev_b32_e32 v248, 16, v133
	v_and_b32_e32 v249, 0xffff0000, v133
	v_mul_f32_e32 v246, v246, v218
	v_mul_f32_e32 v247, v247, v218
	v_mul_f32_e32 v248, v248, v218
	v_mul_f32_e32 v249, v249, v218
	v_lshlrev_b32_e32 v8, 16, v148
	v_and_b32_e32 v9, 0xffff0000, v148
	v_lshlrev_b32_e32 v10, 16, v149
	v_and_b32_e32 v11, 0xffff0000, v149
	v_fmac_f32_e32 v8, v246, v40
	v_fmac_f32_e32 v9, v247, v41
	v_fmac_f32_e32 v10, v248, v42
	v_fmac_f32_e32 v11, v249, v43
	v_lshlrev_b32_e32 v246, 16, v134
	v_and_b32_e32 v247, 0xffff0000, v134
	v_lshlrev_b32_e32 v248, 16, v135
	v_and_b32_e32 v249, 0xffff0000, v135
	v_mul_f32_e32 v246, v246, v218
	v_mul_f32_e32 v247, v247, v218
	v_mul_f32_e32 v248, v248, v218
	v_mul_f32_e32 v249, v249, v218
	v_lshlrev_b32_e32 v12, 16, v150
	v_and_b32_e32 v13, 0xffff0000, v150
	v_lshlrev_b32_e32 v14, 16, v151
	v_and_b32_e32 v15, 0xffff0000, v151
	v_fmac_f32_e32 v12, v246, v44
	v_fmac_f32_e32 v13, v247, v45
	v_fmac_f32_e32 v14, v248, v46
	v_fmac_f32_e32 v15, v249, v47
	v_lshlrev_b32_e32 v246, 16, v136
	v_and_b32_e32 v247, 0xffff0000, v136
	v_lshlrev_b32_e32 v248, 16, v137
	v_and_b32_e32 v249, 0xffff0000, v137
	v_mul_f32_e32 v246, v246, v218
	v_mul_f32_e32 v247, v247, v218
	v_mul_f32_e32 v248, v248, v218
	v_mul_f32_e32 v249, v249, v218
	v_lshlrev_b32_e32 v16, 16, v152
	v_and_b32_e32 v17, 0xffff0000, v152
	v_lshlrev_b32_e32 v18, 16, v153
	v_and_b32_e32 v19, 0xffff0000, v153
	v_fmac_f32_e32 v16, v246, v48
	v_fmac_f32_e32 v17, v247, v49
	v_fmac_f32_e32 v18, v248, v50
	v_fmac_f32_e32 v19, v249, v51
	v_lshlrev_b32_e32 v246, 16, v138
	v_and_b32_e32 v247, 0xffff0000, v138
	v_lshlrev_b32_e32 v248, 16, v139
	v_and_b32_e32 v249, 0xffff0000, v139
	v_mul_f32_e32 v246, v246, v218
	v_mul_f32_e32 v247, v247, v218
	v_mul_f32_e32 v248, v248, v218
	v_mul_f32_e32 v249, v249, v218
	v_lshlrev_b32_e32 v20, 16, v154
	v_and_b32_e32 v21, 0xffff0000, v154
	v_lshlrev_b32_e32 v22, 16, v155
	v_and_b32_e32 v23, 0xffff0000, v155
	v_fmac_f32_e32 v20, v246, v52
	v_fmac_f32_e32 v21, v247, v53
	v_fmac_f32_e32 v22, v248, v54
	v_fmac_f32_e32 v23, v249, v55
	v_lshlrev_b32_e32 v246, 16, v140
	v_and_b32_e32 v247, 0xffff0000, v140
	v_lshlrev_b32_e32 v248, 16, v141
	v_and_b32_e32 v249, 0xffff0000, v141
	v_mul_f32_e32 v246, v246, v218
	v_mul_f32_e32 v247, v247, v218
	v_mul_f32_e32 v248, v248, v218
	v_mul_f32_e32 v249, v249, v218
	v_lshlrev_b32_e32 v24, 16, v156
	v_and_b32_e32 v25, 0xffff0000, v156
	v_lshlrev_b32_e32 v26, 16, v157
	v_and_b32_e32 v27, 0xffff0000, v157
	v_fmac_f32_e32 v24, v246, v56
	v_fmac_f32_e32 v25, v247, v57
	v_fmac_f32_e32 v26, v248, v58
	v_fmac_f32_e32 v27, v249, v59
	v_lshlrev_b32_e32 v246, 16, v142
	v_and_b32_e32 v247, 0xffff0000, v142
	v_lshlrev_b32_e32 v248, 16, v143
	v_and_b32_e32 v249, 0xffff0000, v143
	v_mul_f32_e32 v246, v246, v218
	v_mul_f32_e32 v247, v247, v218
	v_mul_f32_e32 v248, v248, v218
	v_mul_f32_e32 v249, v249, v218
	v_lshlrev_b32_e32 v28, 16, v158
	v_and_b32_e32 v29, 0xffff0000, v158
	v_lshlrev_b32_e32 v30, 16, v159
	v_and_b32_e32 v31, 0xffff0000, v159
	v_fmac_f32_e32 v28, v246, v60
	v_fmac_f32_e32 v29, v247, v61
	v_fmac_f32_e32 v30, v248, v62
	v_fmac_f32_e32 v31, v249, v63
	global_load_dwordx4 v[128:131], v163, s[56:57]
	global_load_dwordx4 v[132:135], v163, s[56:57] offset:1024
	global_load_dwordx4 v[136:139], v163, s[56:57] offset:2048
	global_load_dwordx4 v[140:143], v163, s[56:57] offset:3072
	global_load_dwordx4 v[144:147], v163, s[58:59]
	global_load_dwordx4 v[148:151], v163, s[58:59] offset:1024
	global_load_dwordx4 v[152:155], v163, s[58:59] offset:2048
	global_load_dwordx4 v[156:159], v163, s[58:59] offset:3072
	s_add_u32 s58, s58, 0x8000
	s_addc_u32 s59, s59, 0
	s_add_u32 s56, s56, 0x8000
	s_addc_u32 s57, s57, 0
	v_mov_b32_e32 v250, 0
	v_mov_b32_e32 v251, 0
	v_cvt_pk_bf16_f32 v238, v0, v1
	v_cvt_pk_bf16_f32 v239, v2, v3
	v_fmac_f32_e32 v250, v0, v0
	v_fmac_f32_e32 v251, v1, v1
	v_fmac_f32_e32 v250, v2, v2
	v_fmac_f32_e32 v251, v3, v3
	v_cvt_pk_bf16_f32 v240, v4, v5
	v_cvt_pk_bf16_f32 v241, v6, v7
	v_fmac_f32_e32 v250, v4, v4
	v_fmac_f32_e32 v251, v5, v5
	v_fmac_f32_e32 v250, v6, v6
	v_fmac_f32_e32 v251, v7, v7
	global_store_dwordx4 v163, v[238:241], s[70:71]
	v_cvt_pk_bf16_f32 v242, v8, v9
	v_cvt_pk_bf16_f32 v243, v10, v11
	v_fmac_f32_e32 v250, v8, v8
	v_fmac_f32_e32 v251, v9, v9
	v_fmac_f32_e32 v250, v10, v10
	v_fmac_f32_e32 v251, v11, v11
	v_cvt_pk_bf16_f32 v244, v12, v13
	v_cvt_pk_bf16_f32 v245, v14, v15
	v_fmac_f32_e32 v250, v12, v12
	v_fmac_f32_e32 v251, v13, v13
	v_fmac_f32_e32 v250, v14, v14
	v_fmac_f32_e32 v251, v15, v15
	global_store_dwordx4 v163, v[242:245], s[70:71] offset:1024
	v_cvt_pk_bf16_f32 v238, v16, v17
	v_cvt_pk_bf16_f32 v239, v18, v19
	v_fmac_f32_e32 v250, v16, v16
	v_fmac_f32_e32 v251, v17, v17
	v_fmac_f32_e32 v250, v18, v18
	v_fmac_f32_e32 v251, v19, v19
	v_cvt_pk_bf16_f32 v240, v20, v21
	v_cvt_pk_bf16_f32 v241, v22, v23
	v_fmac_f32_e32 v250, v20, v20
	v_fmac_f32_e32 v251, v21, v21
	v_fmac_f32_e32 v250, v22, v22
	v_fmac_f32_e32 v251, v23, v23
	global_store_dwordx4 v163, v[238:241], s[70:71] offset:2048
	v_cvt_pk_bf16_f32 v242, v24, v25
	v_cvt_pk_bf16_f32 v243, v26, v27
	v_fmac_f32_e32 v250, v24, v24
	v_fmac_f32_e32 v251, v25, v25
	v_fmac_f32_e32 v250, v26, v26
	v_fmac_f32_e32 v251, v27, v27
	v_cvt_pk_bf16_f32 v244, v28, v29
	v_cvt_pk_bf16_f32 v245, v30, v31
	v_fmac_f32_e32 v250, v28, v28
	v_fmac_f32_e32 v251, v29, v29
	v_fmac_f32_e32 v250, v30, v30
	v_fmac_f32_e32 v251, v31, v31
	global_store_dwordx4 v163, v[242:245], s[70:71] offset:3072
	s_add_u32 s70, s70, 0x8000
	s_addc_u32 s71, s71, 0
	v_add_f32_e32 v250, v250, v251
	s_nop 1
	v_add_f32_dpp v218, v250, v250 quad_perm:[1,0,3,2] row_mask:0xf bank_mask:0xf bound_ctrl:1
	s_nop 1
	v_add_f32_dpp v218, v218, v218 quad_perm:[2,3,0,1] row_mask:0xf bank_mask:0xf bound_ctrl:1
	s_nop 1
	v_add_f32_dpp v218, v218, v218 row_ror:4 row_mask:0xf bank_mask:0xf bound_ctrl:1
	s_nop 1
	v_add_f32_dpp v218, v218, v218 row_ror:8 row_mask:0xf bank_mask:0xf bound_ctrl:1
	s_nop 1
	v_readlane_b32 s8, v218, 0
	v_readlane_b32 s9, v218, 16
	v_readlane_b32 s10, v218, 32
	v_readlane_b32 s11, v218, 48
	s_nop 1
	v_mov_b32_e32 v218, s8
	v_add_f32_e32 v218, s9, v218
	v_mov_b32_e32 v219, s10
	v_add_f32_e32 v219, s11, v219
	v_add_f32_e32 v218, v218, v219
	v_mul_f32_e32 v218, 0x3a000000, v218
	v_add_f32_e32 v218, 0x358637bd, v218
	v_rsq_f32_e32 v218, v218
	s_nop 0
	v_mul_f32_e32 v246, v0, v218
	v_mul_f32_e32 v247, v1, v218
	v_mul_f32_e32 v248, v2, v218
	v_mul_f32_e32 v249, v3, v218
	v_fma_f32 v246, v246, v64, v96
	v_fma_f32 v247, v247, v65, v97
	v_fma_f32 v248, v248, v66, v98
	v_fma_f32 v249, v249, v67, v99
	v_cvt_pk_bf16_f32 v238, v246, v247
	v_cvt_pk_bf16_f32 v239, v248, v249
	v_mul_f32_e32 v246, v4, v218
	v_mul_f32_e32 v247, v5, v218
	v_mul_f32_e32 v248, v6, v218
	v_mul_f32_e32 v249, v7, v218
	v_fma_f32 v246, v246, v68, v100
	v_fma_f32 v247, v247, v69, v101
	v_fma_f32 v248, v248, v70, v102
	v_fma_f32 v249, v249, v71, v103
	v_cvt_pk_bf16_f32 v240, v246, v247
	v_cvt_pk_bf16_f32 v241, v248, v249
	global_store_dwordx4 v163, v[238:241], s[72:73]
	v_mul_f32_e32 v246, v8, v218
	v_mul_f32_e32 v247, v9, v218
	v_mul_f32_e32 v248, v10, v218
	v_mul_f32_e32 v249, v11, v218
	v_fma_f32 v246, v246, v72, v104
	v_fma_f32 v247, v247, v73, v105
	v_fma_f32 v248, v248, v74, v106
	v_fma_f32 v249, v249, v75, v107
	v_cvt_pk_bf16_f32 v242, v246, v247
	v_cvt_pk_bf16_f32 v243, v248, v249
	v_mul_f32_e32 v246, v12, v218
	v_mul_f32_e32 v247, v13, v218
	v_mul_f32_e32 v248, v14, v218
	v_mul_f32_e32 v249, v15, v218
	v_fma_f32 v246, v246, v76, v108
	v_fma_f32 v247, v247, v77, v109
	v_fma_f32 v248, v248, v78, v110
	v_fma_f32 v249, v249, v79, v111
	v_cvt_pk_bf16_f32 v244, v246, v247
	v_cvt_pk_bf16_f32 v245, v248, v249
	global_store_dwordx4 v163, v[242:245], s[72:73] offset:1024
	v_mul_f32_e32 v246, v16, v218
	v_mul_f32_e32 v247, v17, v218
	v_mul_f32_e32 v248, v18, v218
	v_mul_f32_e32 v249, v19, v218
	v_fma_f32 v246, v246, v80, v112
	v_fma_f32 v247, v247, v81, v113
	v_fma_f32 v248, v248, v82, v114
	v_fma_f32 v249, v249, v83, v115
	v_cvt_pk_bf16_f32 v238, v246, v247
	v_cvt_pk_bf16_f32 v239, v248, v249
	v_mul_f32_e32 v246, v20, v218
	v_mul_f32_e32 v247, v21, v218
	v_mul_f32_e32 v248, v22, v218
	v_mul_f32_e32 v249, v23, v218
	v_fma_f32 v246, v246, v84, v116
	v_fma_f32 v247, v247, v85, v117
	v_fma_f32 v248, v248, v86, v118
	v_fma_f32 v249, v249, v87, v119
	v_cvt_pk_bf16_f32 v240, v246, v247
	v_cvt_pk_bf16_f32 v241, v248, v249
	global_store_dwordx4 v163, v[238:241], s[72:73] offset:2048
	v_mul_f32_e32 v246, v24, v218
	v_mul_f32_e32 v247, v25, v218
	v_mul_f32_e32 v248, v26, v218
	v_mul_f32_e32 v249, v27, v218
	v_fma_f32 v246, v246, v88, v120
	v_fma_f32 v247, v247, v89, v121
	v_fma_f32 v248, v248, v90, v122
	v_fma_f32 v249, v249, v91, v123
	v_cvt_pk_bf16_f32 v242, v246, v247
	v_cvt_pk_bf16_f32 v243, v248, v249
	v_mul_f32_e32 v246, v28, v218
	v_mul_f32_e32 v247, v29, v218
	v_mul_f32_e32 v248, v30, v218
	v_mul_f32_e32 v249, v31, v218
	v_fma_f32 v246, v246, v92, v124
	v_fma_f32 v247, v247, v93, v125
	v_fma_f32 v248, v248, v94, v126
	v_fma_f32 v249, v249, v95, v127
	v_cvt_pk_bf16_f32 v244, v246, v247
	v_cvt_pk_bf16_f32 v245, v248, v249
	global_store_dwordx4 v163, v[242:245], s[72:73] offset:3072
	s_add_u32 s72, s72, 0x8000
	s_addc_u32 s73, s73, 0
	s_waitcnt vmcnt(16)
	v_mov_b32_e32 v250, 0
	v_mov_b32_e32 v251, 0
	v_lshlrev_b32_e32 v246, 16, v166
	v_and_b32_e32 v247, 0xffff0000, v166
	v_lshlrev_b32_e32 v248, 16, v167
	v_and_b32_e32 v249, 0xffff0000, v167
	v_fmac_f32_e32 v250, v246, v246
	v_fmac_f32_e32 v251, v247, v247
	v_fmac_f32_e32 v250, v248, v248
	v_fmac_f32_e32 v251, v249, v249
	v_lshlrev_b32_e32 v246, 16, v168
	v_and_b32_e32 v247, 0xffff0000, v168
	v_lshlrev_b32_e32 v248, 16, v169
	v_and_b32_e32 v249, 0xffff0000, v169
	v_fmac_f32_e32 v250, v246, v246
	v_fmac_f32_e32 v251, v247, v247
	v_fmac_f32_e32 v250, v248, v248
	v_fmac_f32_e32 v251, v249, v249
	v_lshlrev_b32_e32 v246, 16, v170
	v_and_b32_e32 v247, 0xffff0000, v170
	v_lshlrev_b32_e32 v248, 16, v171
	v_and_b32_e32 v249, 0xffff0000, v171
	v_fmac_f32_e32 v250, v246, v246
	v_fmac_f32_e32 v251, v247, v247
	v_fmac_f32_e32 v250, v248, v248
	v_fmac_f32_e32 v251, v249, v249
	v_lshlrev_b32_e32 v246, 16, v172
	v_and_b32_e32 v247, 0xffff0000, v172
	v_lshlrev_b32_e32 v248, 16, v173
	v_and_b32_e32 v249, 0xffff0000, v173
	v_fmac_f32_e32 v250, v246, v246
	v_fmac_f32_e32 v251, v247, v247
	v_fmac_f32_e32 v250, v248, v248
	v_fmac_f32_e32 v251, v249, v249
	v_lshlrev_b32_e32 v246, 16, v174
	v_and_b32_e32 v247, 0xffff0000, v174
	v_lshlrev_b32_e32 v248, 16, v175
	v_and_b32_e32 v249, 0xffff0000, v175
	v_fmac_f32_e32 v250, v246, v246
	v_fmac_f32_e32 v251, v247, v247
	v_fmac_f32_e32 v250, v248, v248
	v_fmac_f32_e32 v251, v249, v249
	v_lshlrev_b32_e32 v246, 16, v176
	v_and_b32_e32 v247, 0xffff0000, v176
	v_lshlrev_b32_e32 v248, 16, v177
	v_and_b32_e32 v249, 0xffff0000, v177
	v_fmac_f32_e32 v250, v246, v246
	v_fmac_f32_e32 v251, v247, v247
	v_fmac_f32_e32 v250, v248, v248
	v_fmac_f32_e32 v251, v249, v249
	v_lshlrev_b32_e32 v246, 16, v178
	v_and_b32_e32 v247, 0xffff0000, v178
	v_lshlrev_b32_e32 v248, 16, v179
	v_and_b32_e32 v249, 0xffff0000, v179
	v_fmac_f32_e32 v250, v246, v246
	v_fmac_f32_e32 v251, v247, v247
	v_fmac_f32_e32 v250, v248, v248
	v_fmac_f32_e32 v251, v249, v249
	v_lshlrev_b32_e32 v246, 16, v180
	v_and_b32_e32 v247, 0xffff0000, v180
	v_lshlrev_b32_e32 v248, 16, v181
	v_and_b32_e32 v249, 0xffff0000, v181
	v_fmac_f32_e32 v250, v246, v246
	v_fmac_f32_e32 v251, v247, v247
	v_fmac_f32_e32 v250, v248, v248
	v_fmac_f32_e32 v251, v249, v249
	v_add_f32_e32 v250, v250, v251
	s_nop 1
	v_add_f32_dpp v218, v250, v250 quad_perm:[1,0,3,2] row_mask:0xf bank_mask:0xf bound_ctrl:1
	s_nop 1
	v_add_f32_dpp v218, v218, v218 quad_perm:[2,3,0,1] row_mask:0xf bank_mask:0xf bound_ctrl:1
	s_nop 1
	v_add_f32_dpp v218, v218, v218 row_ror:4 row_mask:0xf bank_mask:0xf bound_ctrl:1
	s_nop 1
	v_add_f32_dpp v218, v218, v218 row_ror:8 row_mask:0xf bank_mask:0xf bound_ctrl:1
	s_nop 1
	v_readlane_b32 s8, v218, 0
	v_readlane_b32 s9, v218, 16
	v_readlane_b32 s10, v218, 32
	v_readlane_b32 s11, v218, 48
	s_nop 1
	v_mov_b32_e32 v218, s8
	v_add_f32_e32 v218, s9, v218
	v_mov_b32_e32 v219, s10
	v_add_f32_e32 v219, s11, v219
	v_add_f32_e32 v218, v218, v219
	v_mul_f32_e32 v218, 0x3a000000, v218
	v_add_f32_e32 v218, 0x358637bd, v218
	v_rsq_f32_e32 v218, v218
	s_nop 0
	v_lshlrev_b32_e32 v246, 16, v166
	v_and_b32_e32 v247, 0xffff0000, v166
	v_lshlrev_b32_e32 v248, 16, v167
	v_and_b32_e32 v249, 0xffff0000, v167
	v_mul_f32_e32 v246, v246, v218
	v_mul_f32_e32 v247, v247, v218
	v_mul_f32_e32 v248, v248, v218
	v_mul_f32_e32 v249, v249, v218
	v_lshlrev_b32_e32 v0, 16, v182
	v_and_b32_e32 v1, 0xffff0000, v182
	v_lshlrev_b32_e32 v2, 16, v183
	v_and_b32_e32 v3, 0xffff0000, v183
	v_fmac_f32_e32 v0, v246, v32
	v_fmac_f32_e32 v1, v247, v33
	v_fmac_f32_e32 v2, v248, v34
	v_fmac_f32_e32 v3, v249, v35
	v_lshlrev_b32_e32 v246, 16, v168
	v_and_b32_e32 v247, 0xffff0000, v168
	v_lshlrev_b32_e32 v248, 16, v169
	v_and_b32_e32 v249, 0xffff0000, v169
	v_mul_f32_e32 v246, v246, v218
	v_mul_f32_e32 v247, v247, v218
	v_mul_f32_e32 v248, v248, v218
	v_mul_f32_e32 v249, v249, v218
	v_lshlrev_b32_e32 v4, 16, v184
	v_and_b32_e32 v5, 0xffff0000, v184
	v_lshlrev_b32_e32 v6, 16, v185
	v_and_b32_e32 v7, 0xffff0000, v185
	v_fmac_f32_e32 v4, v246, v36
	v_fmac_f32_e32 v5, v247, v37
	v_fmac_f32_e32 v6, v248, v38
	v_fmac_f32_e32 v7, v249, v39
	v_lshlrev_b32_e32 v246, 16, v170
	v_and_b32_e32 v247, 0xffff0000, v170
	v_lshlrev_b32_e32 v248, 16, v171
	v_and_b32_e32 v249, 0xffff0000, v171
	v_mul_f32_e32 v246, v246, v218
	v_mul_f32_e32 v247, v247, v218
	v_mul_f32_e32 v248, v248, v218
	v_mul_f32_e32 v249, v249, v218
	v_lshlrev_b32_e32 v8, 16, v186
	v_and_b32_e32 v9, 0xffff0000, v186
	v_lshlrev_b32_e32 v10, 16, v187
	v_and_b32_e32 v11, 0xffff0000, v187
	v_fmac_f32_e32 v8, v246, v40
	v_fmac_f32_e32 v9, v247, v41
	v_fmac_f32_e32 v10, v248, v42
	v_fmac_f32_e32 v11, v249, v43
	v_lshlrev_b32_e32 v246, 16, v172
	v_and_b32_e32 v247, 0xffff0000, v172
	v_lshlrev_b32_e32 v248, 16, v173
	v_and_b32_e32 v249, 0xffff0000, v173
	v_mul_f32_e32 v246, v246, v218
	v_mul_f32_e32 v247, v247, v218
	v_mul_f32_e32 v248, v248, v218
	v_mul_f32_e32 v249, v249, v218
	v_lshlrev_b32_e32 v12, 16, v188
	v_and_b32_e32 v13, 0xffff0000, v188
	v_lshlrev_b32_e32 v14, 16, v189
	v_and_b32_e32 v15, 0xffff0000, v189
	v_fmac_f32_e32 v12, v246, v44
	v_fmac_f32_e32 v13, v247, v45
	v_fmac_f32_e32 v14, v248, v46
	v_fmac_f32_e32 v15, v249, v47
	v_lshlrev_b32_e32 v246, 16, v174
	v_and_b32_e32 v247, 0xffff0000, v174
	v_lshlrev_b32_e32 v248, 16, v175
	v_and_b32_e32 v249, 0xffff0000, v175
	v_mul_f32_e32 v246, v246, v218
	v_mul_f32_e32 v247, v247, v218
	v_mul_f32_e32 v248, v248, v218
	v_mul_f32_e32 v249, v249, v218
	v_lshlrev_b32_e32 v16, 16, v190
	v_and_b32_e32 v17, 0xffff0000, v190
	v_lshlrev_b32_e32 v18, 16, v191
	v_and_b32_e32 v19, 0xffff0000, v191
	v_fmac_f32_e32 v16, v246, v48
	v_fmac_f32_e32 v17, v247, v49
	v_fmac_f32_e32 v18, v248, v50
	v_fmac_f32_e32 v19, v249, v51
	v_lshlrev_b32_e32 v246, 16, v176
	v_and_b32_e32 v247, 0xffff0000, v176
	v_lshlrev_b32_e32 v248, 16, v177
	v_and_b32_e32 v249, 0xffff0000, v177
	v_mul_f32_e32 v246, v246, v218
	v_mul_f32_e32 v247, v247, v218
	v_mul_f32_e32 v248, v248, v218
	v_mul_f32_e32 v249, v249, v218
	v_lshlrev_b32_e32 v20, 16, v192
	v_and_b32_e32 v21, 0xffff0000, v192
	v_lshlrev_b32_e32 v22, 16, v193
	v_and_b32_e32 v23, 0xffff0000, v193
	v_fmac_f32_e32 v20, v246, v52
	v_fmac_f32_e32 v21, v247, v53
	v_fmac_f32_e32 v22, v248, v54
	v_fmac_f32_e32 v23, v249, v55
	v_lshlrev_b32_e32 v246, 16, v178
	v_and_b32_e32 v247, 0xffff0000, v178
	v_lshlrev_b32_e32 v248, 16, v179
	v_and_b32_e32 v249, 0xffff0000, v179
	v_mul_f32_e32 v246, v246, v218
	v_mul_f32_e32 v247, v247, v218
	v_mul_f32_e32 v248, v248, v218
	v_mul_f32_e32 v249, v249, v218
	v_lshlrev_b32_e32 v24, 16, v194
	v_and_b32_e32 v25, 0xffff0000, v194
	v_lshlrev_b32_e32 v26, 16, v195
	v_and_b32_e32 v27, 0xffff0000, v195
	v_fmac_f32_e32 v24, v246, v56
	v_fmac_f32_e32 v25, v247, v57
	v_fmac_f32_e32 v26, v248, v58
	v_fmac_f32_e32 v27, v249, v59
	v_lshlrev_b32_e32 v246, 16, v180
	v_and_b32_e32 v247, 0xffff0000, v180
	v_lshlrev_b32_e32 v248, 16, v181
	v_and_b32_e32 v249, 0xffff0000, v181
	v_mul_f32_e32 v246, v246, v218
	v_mul_f32_e32 v247, v247, v218
	v_mul_f32_e32 v248, v248, v218
	v_mul_f32_e32 v249, v249, v218
	v_lshlrev_b32_e32 v28, 16, v196
	v_and_b32_e32 v29, 0xffff0000, v196
	v_lshlrev_b32_e32 v30, 16, v197
	v_and_b32_e32 v31, 0xffff0000, v197
	v_fmac_f32_e32 v28, v246, v60
	v_fmac_f32_e32 v29, v247, v61
	v_fmac_f32_e32 v30, v248, v62
	v_fmac_f32_e32 v31, v249, v63
	global_load_dwordx4 v[166:169], v163, s[56:57]
	global_load_dwordx4 v[170:173], v163, s[56:57] offset:1024
	global_load_dwordx4 v[174:177], v163, s[56:57] offset:2048
	global_load_dwordx4 v[178:181], v163, s[56:57] offset:3072
	global_load_dwordx4 v[182:185], v163, s[58:59]
	global_load_dwordx4 v[186:189], v163, s[58:59] offset:1024
	global_load_dwordx4 v[190:193], v163, s[58:59] offset:2048
	global_load_dwordx4 v[194:197], v163, s[58:59] offset:3072
	s_add_u32 s58, s58, 0x8000
	s_addc_u32 s59, s59, 0
	s_add_u32 s56, s56, 0x8000
	s_addc_u32 s57, s57, 0
	v_mov_b32_e32 v250, 0
	v_mov_b32_e32 v251, 0
	v_cvt_pk_bf16_f32 v238, v0, v1
	v_cvt_pk_bf16_f32 v239, v2, v3
	v_fmac_f32_e32 v250, v0, v0
	v_fmac_f32_e32 v251, v1, v1
	v_fmac_f32_e32 v250, v2, v2
	v_fmac_f32_e32 v251, v3, v3
	v_cvt_pk_bf16_f32 v240, v4, v5
	v_cvt_pk_bf16_f32 v241, v6, v7
	v_fmac_f32_e32 v250, v4, v4
	v_fmac_f32_e32 v251, v5, v5
	v_fmac_f32_e32 v250, v6, v6
	v_fmac_f32_e32 v251, v7, v7
	global_store_dwordx4 v163, v[238:241], s[70:71]
	v_cvt_pk_bf16_f32 v242, v8, v9
	v_cvt_pk_bf16_f32 v243, v10, v11
	v_fmac_f32_e32 v250, v8, v8
	v_fmac_f32_e32 v251, v9, v9
	v_fmac_f32_e32 v250, v10, v10
	v_fmac_f32_e32 v251, v11, v11
	v_cvt_pk_bf16_f32 v244, v12, v13
	v_cvt_pk_bf16_f32 v245, v14, v15
	v_fmac_f32_e32 v250, v12, v12
	v_fmac_f32_e32 v251, v13, v13
	v_fmac_f32_e32 v250, v14, v14
	v_fmac_f32_e32 v251, v15, v15
	global_store_dwordx4 v163, v[242:245], s[70:71] offset:1024
	v_cvt_pk_bf16_f32 v238, v16, v17
	v_cvt_pk_bf16_f32 v239, v18, v19
	v_fmac_f32_e32 v250, v16, v16
	v_fmac_f32_e32 v251, v17, v17
	v_fmac_f32_e32 v250, v18, v18
	v_fmac_f32_e32 v251, v19, v19
	v_cvt_pk_bf16_f32 v240, v20, v21
	v_cvt_pk_bf16_f32 v241, v22, v23
	v_fmac_f32_e32 v250, v20, v20
	v_fmac_f32_e32 v251, v21, v21
	v_fmac_f32_e32 v250, v22, v22
	v_fmac_f32_e32 v251, v23, v23
	global_store_dwordx4 v163, v[238:241], s[70:71] offset:2048
	v_cvt_pk_bf16_f32 v242, v24, v25
	v_cvt_pk_bf16_f32 v243, v26, v27
	v_fmac_f32_e32 v250, v24, v24
	v_fmac_f32_e32 v251, v25, v25
	v_fmac_f32_e32 v250, v26, v26
	v_fmac_f32_e32 v251, v27, v27
	v_cvt_pk_bf16_f32 v244, v28, v29
	v_cvt_pk_bf16_f32 v245, v30, v31
	v_fmac_f32_e32 v250, v28, v28
	v_fmac_f32_e32 v251, v29, v29
	v_fmac_f32_e32 v250, v30, v30
	v_fmac_f32_e32 v251, v31, v31
	global_store_dwordx4 v163, v[242:245], s[70:71] offset:3072
	s_add_u32 s70, s70, 0x8000
	s_addc_u32 s71, s71, 0
	v_add_f32_e32 v250, v250, v251
	s_nop 1
	v_add_f32_dpp v218, v250, v250 quad_perm:[1,0,3,2] row_mask:0xf bank_mask:0xf bound_ctrl:1
	s_nop 1
	v_add_f32_dpp v218, v218, v218 quad_perm:[2,3,0,1] row_mask:0xf bank_mask:0xf bound_ctrl:1
	s_nop 1
	v_add_f32_dpp v218, v218, v218 row_ror:4 row_mask:0xf bank_mask:0xf bound_ctrl:1
	s_nop 1
	v_add_f32_dpp v218, v218, v218 row_ror:8 row_mask:0xf bank_mask:0xf bound_ctrl:1
	s_nop 1
	v_readlane_b32 s8, v218, 0
	v_readlane_b32 s9, v218, 16
	v_readlane_b32 s10, v218, 32
	v_readlane_b32 s11, v218, 48
	s_nop 1
	v_mov_b32_e32 v218, s8
	v_add_f32_e32 v218, s9, v218
	v_mov_b32_e32 v219, s10
	v_add_f32_e32 v219, s11, v219
	v_add_f32_e32 v218, v218, v219
	v_mul_f32_e32 v218, 0x3a000000, v218
	v_add_f32_e32 v218, 0x358637bd, v218
	v_rsq_f32_e32 v218, v218
	s_nop 0
	v_mul_f32_e32 v246, v0, v218
	v_mul_f32_e32 v247, v1, v218
	v_mul_f32_e32 v248, v2, v218
	v_mul_f32_e32 v249, v3, v218
	v_fma_f32 v246, v246, v64, v96
	v_fma_f32 v247, v247, v65, v97
	v_fma_f32 v248, v248, v66, v98
	v_fma_f32 v249, v249, v67, v99
	v_cvt_pk_bf16_f32 v238, v246, v247
	v_cvt_pk_bf16_f32 v239, v248, v249
	v_mul_f32_e32 v246, v4, v218
	v_mul_f32_e32 v247, v5, v218
	v_mul_f32_e32 v248, v6, v218
	v_mul_f32_e32 v249, v7, v218
	v_fma_f32 v246, v246, v68, v100
	v_fma_f32 v247, v247, v69, v101
	v_fma_f32 v248, v248, v70, v102
	v_fma_f32 v249, v249, v71, v103
	v_cvt_pk_bf16_f32 v240, v246, v247
	v_cvt_pk_bf16_f32 v241, v248, v249
	global_store_dwordx4 v163, v[238:241], s[72:73]
	v_mul_f32_e32 v246, v8, v218
	v_mul_f32_e32 v247, v9, v218
	v_mul_f32_e32 v248, v10, v218
	v_mul_f32_e32 v249, v11, v218
	v_fma_f32 v246, v246, v72, v104
	v_fma_f32 v247, v247, v73, v105
	v_fma_f32 v248, v248, v74, v106
	v_fma_f32 v249, v249, v75, v107
	v_cvt_pk_bf16_f32 v242, v246, v247
	v_cvt_pk_bf16_f32 v243, v248, v249
	v_mul_f32_e32 v246, v12, v218
	v_mul_f32_e32 v247, v13, v218
	v_mul_f32_e32 v248, v14, v218
	v_mul_f32_e32 v249, v15, v218
	v_fma_f32 v246, v246, v76, v108
	v_fma_f32 v247, v247, v77, v109
	v_fma_f32 v248, v248, v78, v110
	v_fma_f32 v249, v249, v79, v111
	v_cvt_pk_bf16_f32 v244, v246, v247
	v_cvt_pk_bf16_f32 v245, v248, v249
	global_store_dwordx4 v163, v[242:245], s[72:73] offset:1024
	v_mul_f32_e32 v246, v16, v218
	v_mul_f32_e32 v247, v17, v218
	v_mul_f32_e32 v248, v18, v218
	v_mul_f32_e32 v249, v19, v218
	v_fma_f32 v246, v246, v80, v112
	v_fma_f32 v247, v247, v81, v113
	v_fma_f32 v248, v248, v82, v114
	v_fma_f32 v249, v249, v83, v115
	v_cvt_pk_bf16_f32 v238, v246, v247
	v_cvt_pk_bf16_f32 v239, v248, v249
	v_mul_f32_e32 v246, v20, v218
	v_mul_f32_e32 v247, v21, v218
	v_mul_f32_e32 v248, v22, v218
	v_mul_f32_e32 v249, v23, v218
	v_fma_f32 v246, v246, v84, v116
	v_fma_f32 v247, v247, v85, v117
	v_fma_f32 v248, v248, v86, v118
	v_fma_f32 v249, v249, v87, v119
	v_cvt_pk_bf16_f32 v240, v246, v247
	v_cvt_pk_bf16_f32 v241, v248, v249
	global_store_dwordx4 v163, v[238:241], s[72:73] offset:2048
	v_mul_f32_e32 v246, v24, v218
	v_mul_f32_e32 v247, v25, v218
	v_mul_f32_e32 v248, v26, v218
	v_mul_f32_e32 v249, v27, v218
	v_fma_f32 v246, v246, v88, v120
	v_fma_f32 v247, v247, v89, v121
	v_fma_f32 v248, v248, v90, v122
	v_fma_f32 v249, v249, v91, v123
	v_cvt_pk_bf16_f32 v242, v246, v247
	v_cvt_pk_bf16_f32 v243, v248, v249
	v_mul_f32_e32 v246, v28, v218
	v_mul_f32_e32 v247, v29, v218
	v_mul_f32_e32 v248, v30, v218
	v_mul_f32_e32 v249, v31, v218
	v_fma_f32 v246, v246, v92, v124
	v_fma_f32 v247, v247, v93, v125
	v_fma_f32 v248, v248, v94, v126
	v_fma_f32 v249, v249, v95, v127
	v_cvt_pk_bf16_f32 v244, v246, v247
	v_cvt_pk_bf16_f32 v245, v248, v249
	global_store_dwordx4 v163, v[242:245], s[72:73] offset:3072
	s_add_u32 s72, s72, 0x8000
	s_addc_u32 s73, s73, 0
	s_add_u32 s76, s76, 1
	s_cmp_lt_u32 s76, 7
	s_cbranch_scc1 .Lmp_V1_loop
	s_waitcnt vmcnt(16)
	v_mov_b32_e32 v250, 0
	v_mov_b32_e32 v251, 0
	v_lshlrev_b32_e32 v246, 16, v128
	v_and_b32_e32 v247, 0xffff0000, v128
	v_lshlrev_b32_e32 v248, 16, v129
	v_and_b32_e32 v249, 0xffff0000, v129
	v_fmac_f32_e32 v250, v246, v246
	v_fmac_f32_e32 v251, v247, v247
	v_fmac_f32_e32 v250, v248, v248
	v_fmac_f32_e32 v251, v249, v249
	v_lshlrev_b32_e32 v246, 16, v130
	v_and_b32_e32 v247, 0xffff0000, v130
	v_lshlrev_b32_e32 v248, 16, v131
	v_and_b32_e32 v249, 0xffff0000, v131
	v_fmac_f32_e32 v250, v246, v246
	v_fmac_f32_e32 v251, v247, v247
	v_fmac_f32_e32 v250, v248, v248
	v_fmac_f32_e32 v251, v249, v249
	v_lshlrev_b32_e32 v246, 16, v132
	v_and_b32_e32 v247, 0xffff0000, v132
	v_lshlrev_b32_e32 v248, 16, v133
	v_and_b32_e32 v249, 0xffff0000, v133
	v_fmac_f32_e32 v250, v246, v246
	v_fmac_f32_e32 v251, v247, v247
	v_fmac_f32_e32 v250, v248, v248
	v_fmac_f32_e32 v251, v249, v249
	v_lshlrev_b32_e32 v246, 16, v134
	v_and_b32_e32 v247, 0xffff0000, v134
	v_lshlrev_b32_e32 v248, 16, v135
	v_and_b32_e32 v249, 0xffff0000, v135
	v_fmac_f32_e32 v250, v246, v246
	v_fmac_f32_e32 v251, v247, v247
	v_fmac_f32_e32 v250, v248, v248
	v_fmac_f32_e32 v251, v249, v249
	v_lshlrev_b32_e32 v246, 16, v136
	v_and_b32_e32 v247, 0xffff0000, v136
	v_lshlrev_b32_e32 v248, 16, v137
	v_and_b32_e32 v249, 0xffff0000, v137
	v_fmac_f32_e32 v250, v246, v246
	v_fmac_f32_e32 v251, v247, v247
	v_fmac_f32_e32 v250, v248, v248
	v_fmac_f32_e32 v251, v249, v249
	v_lshlrev_b32_e32 v246, 16, v138
	v_and_b32_e32 v247, 0xffff0000, v138
	v_lshlrev_b32_e32 v248, 16, v139
	v_and_b32_e32 v249, 0xffff0000, v139
	v_fmac_f32_e32 v250, v246, v246
	v_fmac_f32_e32 v251, v247, v247
	v_fmac_f32_e32 v250, v248, v248
	v_fmac_f32_e32 v251, v249, v249
	v_lshlrev_b32_e32 v246, 16, v140
	v_and_b32_e32 v247, 0xffff0000, v140
	v_lshlrev_b32_e32 v248, 16, v141
	v_and_b32_e32 v249, 0xffff0000, v141
	v_fmac_f32_e32 v250, v246, v246
	v_fmac_f32_e32 v251, v247, v247
	v_fmac_f32_e32 v250, v248, v248
	v_fmac_f32_e32 v251, v249, v249
	v_lshlrev_b32_e32 v246, 16, v142
	v_and_b32_e32 v247, 0xffff0000, v142
	v_lshlrev_b32_e32 v248, 16, v143
	v_and_b32_e32 v249, 0xffff0000, v143
	v_fmac_f32_e32 v250, v246, v246
	v_fmac_f32_e32 v251, v247, v247
	v_fmac_f32_e32 v250, v248, v248
	v_fmac_f32_e32 v251, v249, v249
	v_add_f32_e32 v250, v250, v251
	s_nop 1
	v_add_f32_dpp v218, v250, v250 quad_perm:[1,0,3,2] row_mask:0xf bank_mask:0xf bound_ctrl:1
	s_nop 1
	v_add_f32_dpp v218, v218, v218 quad_perm:[2,3,0,1] row_mask:0xf bank_mask:0xf bound_ctrl:1
	s_nop 1
	v_add_f32_dpp v218, v218, v218 row_ror:4 row_mask:0xf bank_mask:0xf bound_ctrl:1
	s_nop 1
	v_add_f32_dpp v218, v218, v218 row_ror:8 row_mask:0xf bank_mask:0xf bound_ctrl:1
	s_nop 1
	v_readlane_b32 s8, v218, 0
	v_readlane_b32 s9, v218, 16
	v_readlane_b32 s10, v218, 32
	v_readlane_b32 s11, v218, 48
	s_nop 1
	v_mov_b32_e32 v218, s8
	v_add_f32_e32 v218, s9, v218
	v_mov_b32_e32 v219, s10
	v_add_f32_e32 v219, s11, v219
	v_add_f32_e32 v218, v218, v219
	v_mul_f32_e32 v218, 0x3a000000, v218
	v_add_f32_e32 v218, 0x358637bd, v218
	v_rsq_f32_e32 v218, v218
	s_nop 0
	v_lshlrev_b32_e32 v246, 16, v128
	v_and_b32_e32 v247, 0xffff0000, v128
	v_lshlrev_b32_e32 v248, 16, v129
	v_and_b32_e32 v249, 0xffff0000, v129
	v_mul_f32_e32 v246, v246, v218
	v_mul_f32_e32 v247, v247, v218
	v_mul_f32_e32 v248, v248, v218
	v_mul_f32_e32 v249, v249, v218
	v_lshlrev_b32_e32 v0, 16, v144
	v_and_b32_e32 v1, 0xffff0000, v144
	v_lshlrev_b32_e32 v2, 16, v145
	v_and_b32_e32 v3, 0xffff0000, v145
	v_fmac_f32_e32 v0, v246, v32
	v_fmac_f32_e32 v1, v247, v33
	v_fmac_f32_e32 v2, v248, v34
	v_fmac_f32_e32 v3, v249, v35
	v_lshlrev_b32_e32 v246, 16, v130
	v_and_b32_e32 v247, 0xffff0000, v130
	v_lshlrev_b32_e32 v248, 16, v131
	v_and_b32_e32 v249, 0xffff0000, v131
	v_mul_f32_e32 v246, v246, v218
	v_mul_f32_e32 v247, v247, v218
	v_mul_f32_e32 v248, v248, v218
	v_mul_f32_e32 v249, v249, v218
	v_lshlrev_b32_e32 v4, 16, v146
	v_and_b32_e32 v5, 0xffff0000, v146
	v_lshlrev_b32_e32 v6, 16, v147
	v_and_b32_e32 v7, 0xffff0000, v147
	v_fmac_f32_e32 v4, v246, v36
	v_fmac_f32_e32 v5, v247, v37
	v_fmac_f32_e32 v6, v248, v38
	v_fmac_f32_e32 v7, v249, v39
	v_lshlrev_b32_e32 v246, 16, v132
	v_and_b32_e32 v247, 0xffff0000, v132
	v_lshlrev_b32_e32 v248, 16, v133
	v_and_b32_e32 v249, 0xffff0000, v133
	v_mul_f32_e32 v246, v246, v218
	v_mul_f32_e32 v247, v247, v218
	v_mul_f32_e32 v248, v248, v218
	v_mul_f32_e32 v249, v249, v218
	v_lshlrev_b32_e32 v8, 16, v148
	v_and_b32_e32 v9, 0xffff0000, v148
	v_lshlrev_b32_e32 v10, 16, v149
	v_and_b32_e32 v11, 0xffff0000, v149
	v_fmac_f32_e32 v8, v246, v40
	v_fmac_f32_e32 v9, v247, v41
	v_fmac_f32_e32 v10, v248, v42
	v_fmac_f32_e32 v11, v249, v43
	v_lshlrev_b32_e32 v246, 16, v134
	v_and_b32_e32 v247, 0xffff0000, v134
	v_lshlrev_b32_e32 v248, 16, v135
	v_and_b32_e32 v249, 0xffff0000, v135
	v_mul_f32_e32 v246, v246, v218
	v_mul_f32_e32 v247, v247, v218
	v_mul_f32_e32 v248, v248, v218
	v_mul_f32_e32 v249, v249, v218
	v_lshlrev_b32_e32 v12, 16, v150
	v_and_b32_e32 v13, 0xffff0000, v150
	v_lshlrev_b32_e32 v14, 16, v151
	v_and_b32_e32 v15, 0xffff0000, v151
	v_fmac_f32_e32 v12, v246, v44
	v_fmac_f32_e32 v13, v247, v45
	v_fmac_f32_e32 v14, v248, v46
	v_fmac_f32_e32 v15, v249, v47
	v_lshlrev_b32_e32 v246, 16, v136
	v_and_b32_e32 v247, 0xffff0000, v136
	v_lshlrev_b32_e32 v248, 16, v137
	v_and_b32_e32 v249, 0xffff0000, v137
	v_mul_f32_e32 v246, v246, v218
	v_mul_f32_e32 v247, v247, v218
	v_mul_f32_e32 v248, v248, v218
	v_mul_f32_e32 v249, v249, v218
	v_lshlrev_b32_e32 v16, 16, v152
	v_and_b32_e32 v17, 0xffff0000, v152
	v_lshlrev_b32_e32 v18, 16, v153
	v_and_b32_e32 v19, 0xffff0000, v153
	v_fmac_f32_e32 v16, v246, v48
	v_fmac_f32_e32 v17, v247, v49
	v_fmac_f32_e32 v18, v248, v50
	v_fmac_f32_e32 v19, v249, v51
	v_lshlrev_b32_e32 v246, 16, v138
	v_and_b32_e32 v247, 0xffff0000, v138
	v_lshlrev_b32_e32 v248, 16, v139
	v_and_b32_e32 v249, 0xffff0000, v139
	v_mul_f32_e32 v246, v246, v218
	v_mul_f32_e32 v247, v247, v218
	v_mul_f32_e32 v248, v248, v218
	v_mul_f32_e32 v249, v249, v218
	v_lshlrev_b32_e32 v20, 16, v154
	v_and_b32_e32 v21, 0xffff0000, v154
	v_lshlrev_b32_e32 v22, 16, v155
	v_and_b32_e32 v23, 0xffff0000, v155
	v_fmac_f32_e32 v20, v246, v52
	v_fmac_f32_e32 v21, v247, v53
	v_fmac_f32_e32 v22, v248, v54
	v_fmac_f32_e32 v23, v249, v55
	v_lshlrev_b32_e32 v246, 16, v140
	v_and_b32_e32 v247, 0xffff0000, v140
	v_lshlrev_b32_e32 v248, 16, v141
	v_and_b32_e32 v249, 0xffff0000, v141
	v_mul_f32_e32 v246, v246, v218
	v_mul_f32_e32 v247, v247, v218
	v_mul_f32_e32 v248, v248, v218
	v_mul_f32_e32 v249, v249, v218
	v_lshlrev_b32_e32 v24, 16, v156
	v_and_b32_e32 v25, 0xffff0000, v156
	v_lshlrev_b32_e32 v26, 16, v157
	v_and_b32_e32 v27, 0xffff0000, v157
	v_fmac_f32_e32 v24, v246, v56
	v_fmac_f32_e32 v25, v247, v57
	v_fmac_f32_e32 v26, v248, v58
	v_fmac_f32_e32 v27, v249, v59
	v_lshlrev_b32_e32 v246, 16, v142
	v_and_b32_e32 v247, 0xffff0000, v142
	v_lshlrev_b32_e32 v248, 16, v143
	v_and_b32_e32 v249, 0xffff0000, v143
	v_mul_f32_e32 v246, v246, v218
	v_mul_f32_e32 v247, v247, v218
	v_mul_f32_e32 v248, v248, v218
	v_mul_f32_e32 v249, v249, v218
	v_lshlrev_b32_e32 v28, 16, v158
	v_and_b32_e32 v29, 0xffff0000, v158
	v_lshlrev_b32_e32 v30, 16, v159
	v_and_b32_e32 v31, 0xffff0000, v159
	v_fmac_f32_e32 v28, v246, v60
	v_fmac_f32_e32 v29, v247, v61
	v_fmac_f32_e32 v30, v248, v62
	v_fmac_f32_e32 v31, v249, v63
	v_mov_b32_e32 v250, 0
	v_mov_b32_e32 v251, 0
	v_cvt_pk_bf16_f32 v238, v0, v1
	v_cvt_pk_bf16_f32 v239, v2, v3
	v_fmac_f32_e32 v250, v0, v0
	v_fmac_f32_e32 v251, v1, v1
	v_fmac_f32_e32 v250, v2, v2
	v_fmac_f32_e32 v251, v3, v3
	v_cvt_pk_bf16_f32 v240, v4, v5
	v_cvt_pk_bf16_f32 v241, v6, v7
	v_fmac_f32_e32 v250, v4, v4
	v_fmac_f32_e32 v251, v5, v5
	v_fmac_f32_e32 v250, v6, v6
	v_fmac_f32_e32 v251, v7, v7
	global_store_dwordx4 v163, v[238:241], s[70:71]
	v_cvt_pk_bf16_f32 v242, v8, v9
	v_cvt_pk_bf16_f32 v243, v10, v11
	v_fmac_f32_e32 v250, v8, v8
	v_fmac_f32_e32 v251, v9, v9
	v_fmac_f32_e32 v250, v10, v10
	v_fmac_f32_e32 v251, v11, v11
	v_cvt_pk_bf16_f32 v244, v12, v13
	v_cvt_pk_bf16_f32 v245, v14, v15
	v_fmac_f32_e32 v250, v12, v12
	v_fmac_f32_e32 v251, v13, v13
	v_fmac_f32_e32 v250, v14, v14
	v_fmac_f32_e32 v251, v15, v15
	global_store_dwordx4 v163, v[242:245], s[70:71] offset:1024
	v_cvt_pk_bf16_f32 v238, v16, v17
	v_cvt_pk_bf16_f32 v239, v18, v19
	v_fmac_f32_e32 v250, v16, v16
	v_fmac_f32_e32 v251, v17, v17
	v_fmac_f32_e32 v250, v18, v18
	v_fmac_f32_e32 v251, v19, v19
	v_cvt_pk_bf16_f32 v240, v20, v21
	v_cvt_pk_bf16_f32 v241, v22, v23
	v_fmac_f32_e32 v250, v20, v20
	v_fmac_f32_e32 v251, v21, v21
	v_fmac_f32_e32 v250, v22, v22
	v_fmac_f32_e32 v251, v23, v23
	global_store_dwordx4 v163, v[238:241], s[70:71] offset:2048
	v_cvt_pk_bf16_f32 v242, v24, v25
	v_cvt_pk_bf16_f32 v243, v26, v27
	v_fmac_f32_e32 v250, v24, v24
	v_fmac_f32_e32 v251, v25, v25
	v_fmac_f32_e32 v250, v26, v26
	v_fmac_f32_e32 v251, v27, v27
	v_cvt_pk_bf16_f32 v244, v28, v29
	v_cvt_pk_bf16_f32 v245, v30, v31
	v_fmac_f32_e32 v250, v28, v28
	v_fmac_f32_e32 v251, v29, v29
	v_fmac_f32_e32 v250, v30, v30
	v_fmac_f32_e32 v251, v31, v31
	global_store_dwordx4 v163, v[242:245], s[70:71] offset:3072
	s_add_u32 s70, s70, 0x8000
	s_addc_u32 s71, s71, 0
	v_add_f32_e32 v250, v250, v251
	s_nop 1
	v_add_f32_dpp v218, v250, v250 quad_perm:[1,0,3,2] row_mask:0xf bank_mask:0xf bound_ctrl:1
	s_nop 1
	v_add_f32_dpp v218, v218, v218 quad_perm:[2,3,0,1] row_mask:0xf bank_mask:0xf bound_ctrl:1
	s_nop 1
	v_add_f32_dpp v218, v218, v218 row_ror:4 row_mask:0xf bank_mask:0xf bound_ctrl:1
	s_nop 1
	v_add_f32_dpp v218, v218, v218 row_ror:8 row_mask:0xf bank_mask:0xf bound_ctrl:1
	s_nop 1
	v_readlane_b32 s8, v218, 0
	v_readlane_b32 s9, v218, 16
	v_readlane_b32 s10, v218, 32
	v_readlane_b32 s11, v218, 48
	s_nop 1
	v_mov_b32_e32 v218, s8
	v_add_f32_e32 v218, s9, v218
	v_mov_b32_e32 v219, s10
	v_add_f32_e32 v219, s11, v219
	v_add_f32_e32 v218, v218, v219
	v_mul_f32_e32 v218, 0x3a000000, v218
	v_add_f32_e32 v218, 0x358637bd, v218
	v_rsq_f32_e32 v218, v218
	s_nop 0
	v_mul_f32_e32 v246, v0, v218
	v_mul_f32_e32 v247, v1, v218
	v_mul_f32_e32 v248, v2, v218
	v_mul_f32_e32 v249, v3, v218
	v_fma_f32 v246, v246, v64, v96
	v_fma_f32 v247, v247, v65, v97
	v_fma_f32 v248, v248, v66, v98
	v_fma_f32 v249, v249, v67, v99
	v_cvt_pk_bf16_f32 v238, v246, v247
	v_cvt_pk_bf16_f32 v239, v248, v249
	v_mul_f32_e32 v246, v4, v218
	v_mul_f32_e32 v247, v5, v218
	v_mul_f32_e32 v248, v6, v218
	v_mul_f32_e32 v249, v7, v218
	v_fma_f32 v246, v246, v68, v100
	v_fma_f32 v247, v247, v69, v101
	v_fma_f32 v248, v248, v70, v102
	v_fma_f32 v249, v249, v71, v103
	v_cvt_pk_bf16_f32 v240, v246, v247
	v_cvt_pk_bf16_f32 v241, v248, v249
	global_store_dwordx4 v163, v[238:241], s[72:73]
	v_mul_f32_e32 v246, v8, v218
	v_mul_f32_e32 v247, v9, v218
	v_mul_f32_e32 v248, v10, v218
	v_mul_f32_e32 v249, v11, v218
	v_fma_f32 v246, v246, v72, v104
	v_fma_f32 v247, v247, v73, v105
	v_fma_f32 v248, v248, v74, v106
	v_fma_f32 v249, v249, v75, v107
	v_cvt_pk_bf16_f32 v242, v246, v247
	v_cvt_pk_bf16_f32 v243, v248, v249
	v_mul_f32_e32 v246, v12, v218
	v_mul_f32_e32 v247, v13, v218
	v_mul_f32_e32 v248, v14, v218
	v_mul_f32_e32 v249, v15, v218
	v_fma_f32 v246, v246, v76, v108
	v_fma_f32 v247, v247, v77, v109
	v_fma_f32 v248, v248, v78, v110
	v_fma_f32 v249, v249, v79, v111
	v_cvt_pk_bf16_f32 v244, v246, v247
	v_cvt_pk_bf16_f32 v245, v248, v249
	global_store_dwordx4 v163, v[242:245], s[72:73] offset:1024
	v_mul_f32_e32 v246, v16, v218
	v_mul_f32_e32 v247, v17, v218
	v_mul_f32_e32 v248, v18, v218
	v_mul_f32_e32 v249, v19, v218
	v_fma_f32 v246, v246, v80, v112
	v_fma_f32 v247, v247, v81, v113
	v_fma_f32 v248, v248, v82, v114
	v_fma_f32 v249, v249, v83, v115
	v_cvt_pk_bf16_f32 v238, v246, v247
	v_cvt_pk_bf16_f32 v239, v248, v249
	v_mul_f32_e32 v246, v20, v218
	v_mul_f32_e32 v247, v21, v218
	v_mul_f32_e32 v248, v22, v218
	v_mul_f32_e32 v249, v23, v218
	v_fma_f32 v246, v246, v84, v116
	v_fma_f32 v247, v247, v85, v117
	v_fma_f32 v248, v248, v86, v118
	v_fma_f32 v249, v249, v87, v119
	v_cvt_pk_bf16_f32 v240, v246, v247
	v_cvt_pk_bf16_f32 v241, v248, v249
	global_store_dwordx4 v163, v[238:241], s[72:73] offset:2048
	v_mul_f32_e32 v246, v24, v218
	v_mul_f32_e32 v247, v25, v218
	v_mul_f32_e32 v248, v26, v218
	v_mul_f32_e32 v249, v27, v218
	v_fma_f32 v246, v246, v88, v120
	v_fma_f32 v247, v247, v89, v121
	v_fma_f32 v248, v248, v90, v122
	v_fma_f32 v249, v249, v91, v123
	v_cvt_pk_bf16_f32 v242, v246, v247
	v_cvt_pk_bf16_f32 v243, v248, v249
	v_mul_f32_e32 v246, v28, v218
	v_mul_f32_e32 v247, v29, v218
	v_mul_f32_e32 v248, v30, v218
	v_mul_f32_e32 v249, v31, v218
	v_fma_f32 v246, v246, v92, v124
	v_fma_f32 v247, v247, v93, v125
	v_fma_f32 v248, v248, v94, v126
	v_fma_f32 v249, v249, v95, v127
	v_cvt_pk_bf16_f32 v244, v246, v247
	v_cvt_pk_bf16_f32 v245, v248, v249
	global_store_dwordx4 v163, v[242:245], s[72:73] offset:3072
	s_add_u32 s72, s72, 0x8000
	s_addc_u32 s73, s73, 0
	s_waitcnt vmcnt(16)
	v_mov_b32_e32 v250, 0
	v_mov_b32_e32 v251, 0
	v_lshlrev_b32_e32 v246, 16, v166
	v_and_b32_e32 v247, 0xffff0000, v166
	v_lshlrev_b32_e32 v248, 16, v167
	v_and_b32_e32 v249, 0xffff0000, v167
	v_fmac_f32_e32 v250, v246, v246
	v_fmac_f32_e32 v251, v247, v247
	v_fmac_f32_e32 v250, v248, v248
	v_fmac_f32_e32 v251, v249, v249
	v_lshlrev_b32_e32 v246, 16, v168
	v_and_b32_e32 v247, 0xffff0000, v168
	v_lshlrev_b32_e32 v248, 16, v169
	v_and_b32_e32 v249, 0xffff0000, v169
	v_fmac_f32_e32 v250, v246, v246
	v_fmac_f32_e32 v251, v247, v247
	v_fmac_f32_e32 v250, v248, v248
	v_fmac_f32_e32 v251, v249, v249
	v_lshlrev_b32_e32 v246, 16, v170
	v_and_b32_e32 v247, 0xffff0000, v170
	v_lshlrev_b32_e32 v248, 16, v171
	v_and_b32_e32 v249, 0xffff0000, v171
	v_fmac_f32_e32 v250, v246, v246
	v_fmac_f32_e32 v251, v247, v247
	v_fmac_f32_e32 v250, v248, v248
	v_fmac_f32_e32 v251, v249, v249
	v_lshlrev_b32_e32 v246, 16, v172
	v_and_b32_e32 v247, 0xffff0000, v172
	v_lshlrev_b32_e32 v248, 16, v173
	v_and_b32_e32 v249, 0xffff0000, v173
	v_fmac_f32_e32 v250, v246, v246
	v_fmac_f32_e32 v251, v247, v247
	v_fmac_f32_e32 v250, v248, v248
	v_fmac_f32_e32 v251, v249, v249
	v_lshlrev_b32_e32 v246, 16, v174
	v_and_b32_e32 v247, 0xffff0000, v174
	v_lshlrev_b32_e32 v248, 16, v175
	v_and_b32_e32 v249, 0xffff0000, v175
	v_fmac_f32_e32 v250, v246, v246
	v_fmac_f32_e32 v251, v247, v247
	v_fmac_f32_e32 v250, v248, v248
	v_fmac_f32_e32 v251, v249, v249
	v_lshlrev_b32_e32 v246, 16, v176
	v_and_b32_e32 v247, 0xffff0000, v176
	v_lshlrev_b32_e32 v248, 16, v177
	v_and_b32_e32 v249, 0xffff0000, v177
	v_fmac_f32_e32 v250, v246, v246
	v_fmac_f32_e32 v251, v247, v247
	v_fmac_f32_e32 v250, v248, v248
	v_fmac_f32_e32 v251, v249, v249
	v_lshlrev_b32_e32 v246, 16, v178
	v_and_b32_e32 v247, 0xffff0000, v178
	v_lshlrev_b32_e32 v248, 16, v179
	v_and_b32_e32 v249, 0xffff0000, v179
	v_fmac_f32_e32 v250, v246, v246
	v_fmac_f32_e32 v251, v247, v247
	v_fmac_f32_e32 v250, v248, v248
	v_fmac_f32_e32 v251, v249, v249
	v_lshlrev_b32_e32 v246, 16, v180
	v_and_b32_e32 v247, 0xffff0000, v180
	v_lshlrev_b32_e32 v248, 16, v181
	v_and_b32_e32 v249, 0xffff0000, v181
	v_fmac_f32_e32 v250, v246, v246
	v_fmac_f32_e32 v251, v247, v247
	v_fmac_f32_e32 v250, v248, v248
	v_fmac_f32_e32 v251, v249, v249
	v_add_f32_e32 v250, v250, v251
	s_nop 1
	v_add_f32_dpp v218, v250, v250 quad_perm:[1,0,3,2] row_mask:0xf bank_mask:0xf bound_ctrl:1
	s_nop 1
	v_add_f32_dpp v218, v218, v218 quad_perm:[2,3,0,1] row_mask:0xf bank_mask:0xf bound_ctrl:1
	s_nop 1
	v_add_f32_dpp v218, v218, v218 row_ror:4 row_mask:0xf bank_mask:0xf bound_ctrl:1
	s_nop 1
	v_add_f32_dpp v218, v218, v218 row_ror:8 row_mask:0xf bank_mask:0xf bound_ctrl:1
	s_nop 1
	v_readlane_b32 s8, v218, 0
	v_readlane_b32 s9, v218, 16
	v_readlane_b32 s10, v218, 32
	v_readlane_b32 s11, v218, 48
	s_nop 1
	v_mov_b32_e32 v218, s8
	v_add_f32_e32 v218, s9, v218
	v_mov_b32_e32 v219, s10
	v_add_f32_e32 v219, s11, v219
	v_add_f32_e32 v218, v218, v219
	v_mul_f32_e32 v218, 0x3a000000, v218
	v_add_f32_e32 v218, 0x358637bd, v218
	v_rsq_f32_e32 v218, v218
	s_nop 0
	v_lshlrev_b32_e32 v246, 16, v166
	v_and_b32_e32 v247, 0xffff0000, v166
	v_lshlrev_b32_e32 v248, 16, v167
	v_and_b32_e32 v249, 0xffff0000, v167
	v_mul_f32_e32 v246, v246, v218
	v_mul_f32_e32 v247, v247, v218
	v_mul_f32_e32 v248, v248, v218
	v_mul_f32_e32 v249, v249, v218
	v_lshlrev_b32_e32 v0, 16, v182
	v_and_b32_e32 v1, 0xffff0000, v182
	v_lshlrev_b32_e32 v2, 16, v183
	v_and_b32_e32 v3, 0xffff0000, v183
	v_fmac_f32_e32 v0, v246, v32
	v_fmac_f32_e32 v1, v247, v33
	v_fmac_f32_e32 v2, v248, v34
	v_fmac_f32_e32 v3, v249, v35
	v_lshlrev_b32_e32 v246, 16, v168
	v_and_b32_e32 v247, 0xffff0000, v168
	v_lshlrev_b32_e32 v248, 16, v169
	v_and_b32_e32 v249, 0xffff0000, v169
	v_mul_f32_e32 v246, v246, v218
	v_mul_f32_e32 v247, v247, v218
	v_mul_f32_e32 v248, v248, v218
	v_mul_f32_e32 v249, v249, v218
	v_lshlrev_b32_e32 v4, 16, v184
	v_and_b32_e32 v5, 0xffff0000, v184
	v_lshlrev_b32_e32 v6, 16, v185
	v_and_b32_e32 v7, 0xffff0000, v185
	v_fmac_f32_e32 v4, v246, v36
	v_fmac_f32_e32 v5, v247, v37
	v_fmac_f32_e32 v6, v248, v38
	v_fmac_f32_e32 v7, v249, v39
	v_lshlrev_b32_e32 v246, 16, v170
	v_and_b32_e32 v247, 0xffff0000, v170
	v_lshlrev_b32_e32 v248, 16, v171
	v_and_b32_e32 v249, 0xffff0000, v171
	v_mul_f32_e32 v246, v246, v218
	v_mul_f32_e32 v247, v247, v218
	v_mul_f32_e32 v248, v248, v218
	v_mul_f32_e32 v249, v249, v218
	v_lshlrev_b32_e32 v8, 16, v186
	v_and_b32_e32 v9, 0xffff0000, v186
	v_lshlrev_b32_e32 v10, 16, v187
	v_and_b32_e32 v11, 0xffff0000, v187
	v_fmac_f32_e32 v8, v246, v40
	v_fmac_f32_e32 v9, v247, v41
	v_fmac_f32_e32 v10, v248, v42
	v_fmac_f32_e32 v11, v249, v43
	v_lshlrev_b32_e32 v246, 16, v172
	v_and_b32_e32 v247, 0xffff0000, v172
	v_lshlrev_b32_e32 v248, 16, v173
	v_and_b32_e32 v249, 0xffff0000, v173
	v_mul_f32_e32 v246, v246, v218
	v_mul_f32_e32 v247, v247, v218
	v_mul_f32_e32 v248, v248, v218
	v_mul_f32_e32 v249, v249, v218
	v_lshlrev_b32_e32 v12, 16, v188
	v_and_b32_e32 v13, 0xffff0000, v188
	v_lshlrev_b32_e32 v14, 16, v189
	v_and_b32_e32 v15, 0xffff0000, v189
	v_fmac_f32_e32 v12, v246, v44
	v_fmac_f32_e32 v13, v247, v45
	v_fmac_f32_e32 v14, v248, v46
	v_fmac_f32_e32 v15, v249, v47
	v_lshlrev_b32_e32 v246, 16, v174
	v_and_b32_e32 v247, 0xffff0000, v174
	v_lshlrev_b32_e32 v248, 16, v175
	v_and_b32_e32 v249, 0xffff0000, v175
	v_mul_f32_e32 v246, v246, v218
	v_mul_f32_e32 v247, v247, v218
	v_mul_f32_e32 v248, v248, v218
	v_mul_f32_e32 v249, v249, v218
	v_lshlrev_b32_e32 v16, 16, v190
	v_and_b32_e32 v17, 0xffff0000, v190
	v_lshlrev_b32_e32 v18, 16, v191
	v_and_b32_e32 v19, 0xffff0000, v191
	v_fmac_f32_e32 v16, v246, v48
	v_fmac_f32_e32 v17, v247, v49
	v_fmac_f32_e32 v18, v248, v50
	v_fmac_f32_e32 v19, v249, v51
	v_lshlrev_b32_e32 v246, 16, v176
	v_and_b32_e32 v247, 0xffff0000, v176
	v_lshlrev_b32_e32 v248, 16, v177
	v_and_b32_e32 v249, 0xffff0000, v177
	v_mul_f32_e32 v246, v246, v218
	v_mul_f32_e32 v247, v247, v218
	v_mul_f32_e32 v248, v248, v218
	v_mul_f32_e32 v249, v249, v218
	v_lshlrev_b32_e32 v20, 16, v192
	v_and_b32_e32 v21, 0xffff0000, v192
	v_lshlrev_b32_e32 v22, 16, v193
	v_and_b32_e32 v23, 0xffff0000, v193
	v_fmac_f32_e32 v20, v246, v52
	v_fmac_f32_e32 v21, v247, v53
	v_fmac_f32_e32 v22, v248, v54
	v_fmac_f32_e32 v23, v249, v55
	v_lshlrev_b32_e32 v246, 16, v178
	v_and_b32_e32 v247, 0xffff0000, v178
	v_lshlrev_b32_e32 v248, 16, v179
	v_and_b32_e32 v249, 0xffff0000, v179
	v_mul_f32_e32 v246, v246, v218
	v_mul_f32_e32 v247, v247, v218
	v_mul_f32_e32 v248, v248, v218
	v_mul_f32_e32 v249, v249, v218
	v_lshlrev_b32_e32 v24, 16, v194
	v_and_b32_e32 v25, 0xffff0000, v194
	v_lshlrev_b32_e32 v26, 16, v195
	v_and_b32_e32 v27, 0xffff0000, v195
	v_fmac_f32_e32 v24, v246, v56
	v_fmac_f32_e32 v25, v247, v57
	v_fmac_f32_e32 v26, v248, v58
	v_fmac_f32_e32 v27, v249, v59
	v_lshlrev_b32_e32 v246, 16, v180
	v_and_b32_e32 v247, 0xffff0000, v180
	v_lshlrev_b32_e32 v248, 16, v181
	v_and_b32_e32 v249, 0xffff0000, v181
	v_mul_f32_e32 v246, v246, v218
	v_mul_f32_e32 v247, v247, v218
	v_mul_f32_e32 v248, v248, v218
	v_mul_f32_e32 v249, v249, v218
	v_lshlrev_b32_e32 v28, 16, v196
	v_and_b32_e32 v29, 0xffff0000, v196
	v_lshlrev_b32_e32 v30, 16, v197
	v_and_b32_e32 v31, 0xffff0000, v197
	v_fmac_f32_e32 v28, v246, v60
	v_fmac_f32_e32 v29, v247, v61
	v_fmac_f32_e32 v30, v248, v62
	v_fmac_f32_e32 v31, v249, v63
	v_mov_b32_e32 v250, 0
	v_mov_b32_e32 v251, 0
	v_cvt_pk_bf16_f32 v238, v0, v1
	v_cvt_pk_bf16_f32 v239, v2, v3
	v_fmac_f32_e32 v250, v0, v0
	v_fmac_f32_e32 v251, v1, v1
	v_fmac_f32_e32 v250, v2, v2
	v_fmac_f32_e32 v251, v3, v3
	v_cvt_pk_bf16_f32 v240, v4, v5
	v_cvt_pk_bf16_f32 v241, v6, v7
	v_fmac_f32_e32 v250, v4, v4
	v_fmac_f32_e32 v251, v5, v5
	v_fmac_f32_e32 v250, v6, v6
	v_fmac_f32_e32 v251, v7, v7
	global_store_dwordx4 v163, v[238:241], s[70:71]
	v_cvt_pk_bf16_f32 v242, v8, v9
	v_cvt_pk_bf16_f32 v243, v10, v11
	v_fmac_f32_e32 v250, v8, v8
	v_fmac_f32_e32 v251, v9, v9
	v_fmac_f32_e32 v250, v10, v10
	v_fmac_f32_e32 v251, v11, v11
	v_cvt_pk_bf16_f32 v244, v12, v13
	v_cvt_pk_bf16_f32 v245, v14, v15
	v_fmac_f32_e32 v250, v12, v12
	v_fmac_f32_e32 v251, v13, v13
	v_fmac_f32_e32 v250, v14, v14
	v_fmac_f32_e32 v251, v15, v15
	global_store_dwordx4 v163, v[242:245], s[70:71] offset:1024
	v_cvt_pk_bf16_f32 v238, v16, v17
	v_cvt_pk_bf16_f32 v239, v18, v19
	v_fmac_f32_e32 v250, v16, v16
	v_fmac_f32_e32 v251, v17, v17
	v_fmac_f32_e32 v250, v18, v18
	v_fmac_f32_e32 v251, v19, v19
	v_cvt_pk_bf16_f32 v240, v20, v21
	v_cvt_pk_bf16_f32 v241, v22, v23
	v_fmac_f32_e32 v250, v20, v20
	v_fmac_f32_e32 v251, v21, v21
	v_fmac_f32_e32 v250, v22, v22
	v_fmac_f32_e32 v251, v23, v23
	global_store_dwordx4 v163, v[238:241], s[70:71] offset:2048
	v_cvt_pk_bf16_f32 v242, v24, v25
	v_cvt_pk_bf16_f32 v243, v26, v27
	v_fmac_f32_e32 v250, v24, v24
	v_fmac_f32_e32 v251, v25, v25
	v_fmac_f32_e32 v250, v26, v26
	v_fmac_f32_e32 v251, v27, v27
	v_cvt_pk_bf16_f32 v244, v28, v29
	v_cvt_pk_bf16_f32 v245, v30, v31
	v_fmac_f32_e32 v250, v28, v28
	v_fmac_f32_e32 v251, v29, v29
	v_fmac_f32_e32 v250, v30, v30
	v_fmac_f32_e32 v251, v31, v31
	global_store_dwordx4 v163, v[242:245], s[70:71] offset:3072
	s_add_u32 s70, s70, 0x8000
	s_addc_u32 s71, s71, 0
	v_add_f32_e32 v250, v250, v251
	s_nop 1
	v_add_f32_dpp v218, v250, v250 quad_perm:[1,0,3,2] row_mask:0xf bank_mask:0xf bound_ctrl:1
	s_nop 1
	v_add_f32_dpp v218, v218, v218 quad_perm:[2,3,0,1] row_mask:0xf bank_mask:0xf bound_ctrl:1
	s_nop 1
	v_add_f32_dpp v218, v218, v218 row_ror:4 row_mask:0xf bank_mask:0xf bound_ctrl:1
	s_nop 1
	v_add_f32_dpp v218, v218, v218 row_ror:8 row_mask:0xf bank_mask:0xf bound_ctrl:1
	s_nop 1
	v_readlane_b32 s8, v218, 0
	v_readlane_b32 s9, v218, 16
	v_readlane_b32 s10, v218, 32
	v_readlane_b32 s11, v218, 48
	s_nop 1
	v_mov_b32_e32 v218, s8
	v_add_f32_e32 v218, s9, v218
	v_mov_b32_e32 v219, s10
	v_add_f32_e32 v219, s11, v219
	v_add_f32_e32 v218, v218, v219
	v_mul_f32_e32 v218, 0x3a000000, v218
	v_add_f32_e32 v218, 0x358637bd, v218
	v_rsq_f32_e32 v218, v218
	s_nop 0
	v_mul_f32_e32 v246, v0, v218
	v_mul_f32_e32 v247, v1, v218
	v_mul_f32_e32 v248, v2, v218
	v_mul_f32_e32 v249, v3, v218
	v_fma_f32 v246, v246, v64, v96
	v_fma_f32 v247, v247, v65, v97
	v_fma_f32 v248, v248, v66, v98
	v_fma_f32 v249, v249, v67, v99
	v_cvt_pk_bf16_f32 v238, v246, v247
	v_cvt_pk_bf16_f32 v239, v248, v249
	v_mul_f32_e32 v246, v4, v218
	v_mul_f32_e32 v247, v5, v218
	v_mul_f32_e32 v248, v6, v218
	v_mul_f32_e32 v249, v7, v218
	v_fma_f32 v246, v246, v68, v100
	v_fma_f32 v247, v247, v69, v101
	v_fma_f32 v248, v248, v70, v102
	v_fma_f32 v249, v249, v71, v103
	v_cvt_pk_bf16_f32 v240, v246, v247
	v_cvt_pk_bf16_f32 v241, v248, v249
	global_store_dwordx4 v163, v[238:241], s[72:73]
	v_mul_f32_e32 v246, v8, v218
	v_mul_f32_e32 v247, v9, v218
	v_mul_f32_e32 v248, v10, v218
	v_mul_f32_e32 v249, v11, v218
	v_fma_f32 v246, v246, v72, v104
	v_fma_f32 v247, v247, v73, v105
	v_fma_f32 v248, v248, v74, v106
	v_fma_f32 v249, v249, v75, v107
	v_cvt_pk_bf16_f32 v242, v246, v247
	v_cvt_pk_bf16_f32 v243, v248, v249
	v_mul_f32_e32 v246, v12, v218
	v_mul_f32_e32 v247, v13, v218
	v_mul_f32_e32 v248, v14, v218
	v_mul_f32_e32 v249, v15, v218
	v_fma_f32 v246, v246, v76, v108
	v_fma_f32 v247, v247, v77, v109
	v_fma_f32 v248, v248, v78, v110
	v_fma_f32 v249, v249, v79, v111
	v_cvt_pk_bf16_f32 v244, v246, v247
	v_cvt_pk_bf16_f32 v245, v248, v249
	global_store_dwordx4 v163, v[242:245], s[72:73] offset:1024
	v_mul_f32_e32 v246, v16, v218
	v_mul_f32_e32 v247, v17, v218
	v_mul_f32_e32 v248, v18, v218
	v_mul_f32_e32 v249, v19, v218
	v_fma_f32 v246, v246, v80, v112
	v_fma_f32 v247, v247, v81, v113
	v_fma_f32 v248, v248, v82, v114
	v_fma_f32 v249, v249, v83, v115
	v_cvt_pk_bf16_f32 v238, v246, v247
	v_cvt_pk_bf16_f32 v239, v248, v249
	v_mul_f32_e32 v246, v20, v218
	v_mul_f32_e32 v247, v21, v218
	v_mul_f32_e32 v248, v22, v218
	v_mul_f32_e32 v249, v23, v218
	v_fma_f32 v246, v246, v84, v116
	v_fma_f32 v247, v247, v85, v117
	v_fma_f32 v248, v248, v86, v118
	v_fma_f32 v249, v249, v87, v119
	v_cvt_pk_bf16_f32 v240, v246, v247
	v_cvt_pk_bf16_f32 v241, v248, v249
	global_store_dwordx4 v163, v[238:241], s[72:73] offset:2048
	v_mul_f32_e32 v246, v24, v218
	v_mul_f32_e32 v247, v25, v218
	v_mul_f32_e32 v248, v26, v218
	v_mul_f32_e32 v249, v27, v218
	v_fma_f32 v246, v246, v88, v120
	v_fma_f32 v247, v247, v89, v121
	v_fma_f32 v248, v248, v90, v122
	v_fma_f32 v249, v249, v91, v123
	v_cvt_pk_bf16_f32 v242, v246, v247
	v_cvt_pk_bf16_f32 v243, v248, v249
	v_mul_f32_e32 v246, v28, v218
	v_mul_f32_e32 v247, v29, v218
	v_mul_f32_e32 v248, v30, v218
	v_mul_f32_e32 v249, v31, v218
	v_fma_f32 v246, v246, v92, v124
	v_fma_f32 v247, v247, v93, v125
	v_fma_f32 v248, v248, v94, v126
	v_fma_f32 v249, v249, v95, v127
	v_cvt_pk_bf16_f32 v244, v246, v247
	v_cvt_pk_bf16_f32 v245, v248, v249
	global_store_dwordx4 v163, v[242:245], s[72:73] offset:3072
	s_add_u32 s72, s72, 0x8000
	s_addc_u32 s73, s73, 0
	s_branch .Lmp_done
.Lmp_V2:
	global_load_dwordx4 v[128:131], v163, s[56:57]
	global_load_dwordx4 v[132:135], v163, s[56:57] offset:1024
	global_load_dwordx4 v[136:139], v163, s[56:57] offset:2048
	global_load_dwordx4 v[140:143], v163, s[56:57] offset:3072
	global_load_dwordx4 v[198:201], v162, s[58:59]
	global_load_dwordx4 v[202:205], v162, s[58:59] offset:16
	global_load_dwordx4 v[206:209], v162, s[58:59] offset:2048
	global_load_dwordx4 v[210:213], v162, s[58:59] offset:2064
	s_add_u32 s10, s58, 0x1000
	s_addc_u32 s11, s59, 0
	global_load_dwordx4 v[214:217], v162, s[10:11]
	global_load_dwordx4 v[226:229], v162, s[10:11] offset:16
	global_load_dwordx4 v[230:233], v162, s[10:11] offset:2048
	global_load_dwordx4 v[234:237], v162, s[10:11] offset:2064
	s_add_u32 s58, s58, 0x10000
	s_addc_u32 s59, s59, 0
	s_add_u32 s56, s56, 0x8000
	s_addc_u32 s57, s57, 0
	global_load_dwordx4 v[166:169], v163, s[56:57]
	global_load_dwordx4 v[170:173], v163, s[56:57] offset:1024
	global_load_dwordx4 v[174:177], v163, s[56:57] offset:2048
	global_load_dwordx4 v[178:181], v163, s[56:57] offset:3072
	global_load_dwordx4 v[144:147], v162, s[58:59]
	global_load_dwordx4 v[148:151], v162, s[58:59] offset:16
	global_load_dwordx4 v[152:155], v162, s[58:59] offset:2048
	global_load_dwordx4 v[156:159], v162, s[58:59] offset:2064
	s_add_u32 s10, s58, 0x1000
	s_addc_u32 s11, s59, 0
	global_load_dwordx4 v[182:185], v162, s[10:11]
	global_load_dwordx4 v[186:189], v162, s[10:11] offset:16
	global_load_dwordx4 v[190:193], v162, s[10:11] offset:2048
	global_load_dwordx4 v[194:197], v162, s[10:11] offset:2064
	s_add_u32 s58, s58, 0x10000
	s_addc_u32 s59, s59, 0
	s_add_u32 s56, s56, 0x8000
	s_addc_u32 s57, s57, 0
	s_waitcnt vmcnt(12)
.Lmp_V2_loop:
	s_waitcnt vmcnt(20)
	v_mov_b32_e32 v250, 0
	v_mov_b32_e32 v251, 0
	v_lshlrev_b32_e32 v246, 16, v128
	v_and_b32_e32 v247, 0xffff0000, v128
	v_lshlrev_b32_e32 v248, 16, v129
	v_and_b32_e32 v249, 0xffff0000, v129
	v_fmac_f32_e32 v250, v246, v246
	v_fmac_f32_e32 v251, v247, v247
	v_fmac_f32_e32 v250, v248, v248
	v_fmac_f32_e32 v251, v249, v249
	v_lshlrev_b32_e32 v246, 16, v130
	v_and_b32_e32 v247, 0xffff0000, v130
	v_lshlrev_b32_e32 v248, 16, v131
	v_and_b32_e32 v249, 0xffff0000, v131
	v_fmac_f32_e32 v250, v246, v246
	v_fmac_f32_e32 v251, v247, v247
	v_fmac_f32_e32 v250, v248, v248
	v_fmac_f32_e32 v251, v249, v249
	v_lshlrev_b32_e32 v246, 16, v132
	v_and_b32_e32 v247, 0xffff0000, v132
	v_lshlrev_b32_e32 v248, 16, v133
	v_and_b32_e32 v249, 0xffff0000, v133
	v_fmac_f32_e32 v250, v246, v246
	v_fmac_f32_e32 v251, v247, v247
	v_fmac_f32_e32 v250, v248, v248
	v_fmac_f32_e32 v251, v249, v249
	v_lshlrev_b32_e32 v246, 16, v134
	v_and_b32_e32 v247, 0xffff0000, v134
	v_lshlrev_b32_e32 v248, 16, v135
	v_and_b32_e32 v249, 0xffff0000, v135
	v_fmac_f32_e32 v250, v246, v246
	v_fmac_f32_e32 v251, v247, v247
	v_fmac_f32_e32 v250, v248, v248
	v_fmac_f32_e32 v251, v249, v249
	v_lshlrev_b32_e32 v246, 16, v136
	v_and_b32_e32 v247, 0xffff0000, v136
	v_lshlrev_b32_e32 v248, 16, v137
	v_and_b32_e32 v249, 0xffff0000, v137
	v_fmac_f32_e32 v250, v246, v246
	v_fmac_f32_e32 v251, v247, v247
	v_fmac_f32_e32 v250, v248, v248
	v_fmac_f32_e32 v251, v249, v249
	v_lshlrev_b32_e32 v246, 16, v138
	v_and_b32_e32 v247, 0xffff0000, v138
	v_lshlrev_b32_e32 v248, 16, v139
	v_and_b32_e32 v249, 0xffff0000, v139
	v_fmac_f32_e32 v250, v246, v246
	v_fmac_f32_e32 v251, v247, v247
	v_fmac_f32_e32 v250, v248, v248
	v_fmac_f32_e32 v251, v249, v249
	v_lshlrev_b32_e32 v246, 16, v140
	v_and_b32_e32 v247, 0xffff0000, v140
	v_lshlrev_b32_e32 v248, 16, v141
	v_and_b32_e32 v249, 0xffff0000, v141
	v_fmac_f32_e32 v250, v246, v246
	v_fmac_f32_e32 v251, v247, v247
	v_fmac_f32_e32 v250, v248, v248
	v_fmac_f32_e32 v251, v249, v249
	v_lshlrev_b32_e32 v246, 16, v142
	v_and_b32_e32 v247, 0xffff0000, v142
	v_lshlrev_b32_e32 v248, 16, v143
	v_and_b32_e32 v249, 0xffff0000, v143
	v_fmac_f32_e32 v250, v246, v246
	v_fmac_f32_e32 v251, v247, v247
	v_fmac_f32_e32 v250, v248, v248
	v_fmac_f32_e32 v251, v249, v249
	v_add_f32_e32 v250, v250, v251
	s_nop 1
	v_add_f32_dpp v218, v250, v250 quad_perm:[1,0,3,2] row_mask:0xf bank_mask:0xf bound_ctrl:1
	s_nop 1
	v_add_f32_dpp v218, v218, v218 quad_perm:[2,3,0,1] row_mask:0xf bank_mask:0xf bound_ctrl:1
	s_nop 1
	v_add_f32_dpp v218, v218, v218 row_ror:4 row_mask:0xf bank_mask:0xf bound_ctrl:1
	s_nop 1
	v_add_f32_dpp v218, v218, v218 row_ror:8 row_mask:0xf bank_mask:0xf bound_ctrl:1
	s_nop 1
	v_readlane_b32 s8, v218, 0
	v_readlane_b32 s9, v218, 16
	v_readlane_b32 s10, v218, 32
	v_readlane_b32 s11, v218, 48
	s_nop 1
	v_mov_b32_e32 v218, s8
	v_add_f32_e32 v218, s9, v218
	v_mov_b32_e32 v219, s10
	v_add_f32_e32 v219, s11, v219
	v_add_f32_e32 v218, v218, v219
	v_mul_f32_e32 v218, 0x3a000000, v218
	v_add_f32_e32 v218, 0x358637bd, v218
	v_rsq_f32_e32 v218, v218
	s_nop 0
	v_lshlrev_b32_e32 v246, 16, v128
	v_and_b32_e32 v247, 0xffff0000, v128
	v_lshlrev_b32_e32 v248, 16, v129
	v_and_b32_e32 v249, 0xffff0000, v129
	v_mul_f32_e32 v246, v246, v218
	v_mul_f32_e32 v247, v247, v218
	v_mul_f32_e32 v248, v248, v218
	v_mul_f32_e32 v249, v249, v218
	v_fma_f32 v0, v246, v32, v198
	v_fma_f32 v1, v247, v33, v199
	v_fma_f32 v2, v248, v34, v200
	v_fma_f32 v3, v249, v35, v201
	v_lshlrev_b32_e32 v246, 16, v130
	v_and_b32_e32 v247, 0xffff0000, v130
	v_lshlrev_b32_e32 v248, 16, v131
	v_and_b32_e32 v249, 0xffff0000, v131
	v_mul_f32_e32 v246, v246, v218
	v_mul_f32_e32 v247, v247, v218
	v_mul_f32_e32 v248, v248, v218
	v_mul_f32_e32 v249, v249, v218
	v_fma_f32 v4, v246, v36, v202
	v_fma_f32 v5, v247, v37, v203
	v_fma_f32 v6, v248, v38, v204
	v_fma_f32 v7, v249, v39, v205
	v_lshlrev_b32_e32 v246, 16, v132
	v_and_b32_e32 v247, 0xffff0000, v132
	v_lshlrev_b32_e32 v248, 16, v133
	v_and_b32_e32 v249, 0xffff0000, v133
	v_mul_f32_e32 v246, v246, v218
	v_mul_f32_e32 v247, v247, v218
	v_mul_f32_e32 v248, v248, v218
	v_mul_f32_e32 v249, v249, v218
	v_fma_f32 v8, v246, v40, v206
	v_fma_f32 v9, v247, v41, v207
	v_fma_f32 v10, v248, v42, v208
	v_fma_f32 v11, v249, v43, v209
	v_lshlrev_b32_e32 v246, 16, v134
	v_and_b32_e32 v247, 0xffff0000, v134
	v_lshlrev_b32_e32 v248, 16, v135
	v_and_b32_e32 v249, 0xffff0000, v135
	v_mul_f32_e32 v246, v246, v218
	v_mul_f32_e32 v247, v247, v218
	v_mul_f32_e32 v248, v248, v218
	v_mul_f32_e32 v249, v249, v218
	v_fma_f32 v12, v246, v44, v210
	v_fma_f32 v13, v247, v45, v211
	v_fma_f32 v14, v248, v46, v212
	v_fma_f32 v15, v249, v47, v213
	v_lshlrev_b32_e32 v246, 16, v136
	v_and_b32_e32 v247, 0xffff0000, v136
	v_lshlrev_b32_e32 v248, 16, v137
	v_and_b32_e32 v249, 0xffff0000, v137
	v_mul_f32_e32 v246, v246, v218
	v_mul_f32_e32 v247, v247, v218
	v_mul_f32_e32 v248, v248, v218
	v_mul_f32_e32 v249, v249, v218
	v_fma_f32 v16, v246, v48, v214
	v_fma_f32 v17, v247, v49, v215
	v_fma_f32 v18, v248, v50, v216
	v_fma_f32 v19, v249, v51, v217
	v_lshlrev_b32_e32 v246, 16, v138
	v_and_b32_e32 v247, 0xffff0000, v138
	v_lshlrev_b32_e32 v248, 16, v139
	v_and_b32_e32 v249, 0xffff0000, v139
	v_mul_f32_e32 v246, v246, v218
	v_mul_f32_e32 v247, v247, v218
	v_mul_f32_e32 v248, v248, v218
	v_mul_f32_e32 v249, v249, v218
	v_fma_f32 v20, v246, v52, v226
	v_fma_f32 v21, v247, v53, v227
	v_fma_f32 v22, v248, v54, v228
	v_fma_f32 v23, v249, v55, v229
	v_lshlrev_b32_e32 v246, 16, v140
	v_and_b32_e32 v247, 0xffff0000, v140
	v_lshlrev_b32_e32 v248, 16, v141
	v_and_b32_e32 v249, 0xffff0000, v141
	v_mul_f32_e32 v246, v246, v218
	v_mul_f32_e32 v247, v247, v218
	v_mul_f32_e32 v248, v248, v218
	v_mul_f32_e32 v249, v249, v218
	v_fma_f32 v24, v246, v56, v230
	v_fma_f32 v25, v247, v57, v231
	v_fma_f32 v26, v248, v58, v232
	v_fma_f32 v27, v249, v59, v233
	v_lshlrev_b32_e32 v246, 16, v142
	v_and_b32_e32 v247, 0xffff0000, v142
	v_lshlrev_b32_e32 v248, 16, v143
	v_and_b32_e32 v249, 0xffff0000, v143
	v_mul_f32_e32 v246, v246, v218
	v_mul_f32_e32 v247, v247, v218
	v_mul_f32_e32 v248, v248, v218
	v_mul_f32_e32 v249, v249, v218
	v_fma_f32 v28, v246, v60, v234
	v_fma_f32 v29, v247, v61, v235
	v_fma_f32 v30, v248, v62, v236
	v_fma_f32 v31, v249, v63, v237
	global_load_dwordx4 v[128:131], v163, s[56:57]
	global_load_dwordx4 v[132:135], v163, s[56:57] offset:1024
	global_load_dwordx4 v[136:139], v163, s[56:57] offset:2048
	global_load_dwordx4 v[140:143], v163, s[56:57] offset:3072
	global_load_dwordx4 v[198:201], v162, s[58:59]
	global_load_dwordx4 v[202:205], v162, s[58:59] offset:16
	global_load_dwordx4 v[206:209], v162, s[58:59] offset:2048
	global_load_dwordx4 v[210:213], v162, s[58:59] offset:2064
	s_add_u32 s10, s58, 0x1000
	s_addc_u32 s11, s59, 0
	global_load_dwordx4 v[214:217], v162, s[10:11]
	global_load_dwordx4 v[226:229], v162, s[10:11] offset:16
	global_load_dwordx4 v[230:233], v162, s[10:11] offset:2048
	global_load_dwordx4 v[234:237], v162, s[10:11] offset:2064
	s_add_u32 s58, s58, 0x10000
	s_addc_u32 s59, s59, 0
	s_add_u32 s56, s56, 0x8000
	s_addc_u32 s57, s57, 0
	v_mov_b32_e32 v250, 0
	v_mov_b32_e32 v251, 0
	v_cvt_pk_bf16_f32 v238, v0, v1
	v_cvt_pk_bf16_f32 v239, v2, v3
	v_fmac_f32_e32 v250, v0, v0
	v_fmac_f32_e32 v251, v1, v1
	v_fmac_f32_e32 v250, v2, v2
	v_fmac_f32_e32 v251, v3, v3
	v_cvt_pk_bf16_f32 v240, v4, v5
	v_cvt_pk_bf16_f32 v241, v6, v7
	v_fmac_f32_e32 v250, v4, v4
	v_fmac_f32_e32 v251, v5, v5
	v_fmac_f32_e32 v250, v6, v6
	v_fmac_f32_e32 v251, v7, v7
	global_store_dwordx4 v163, v[238:241], s[70:71]
	v_cvt_pk_bf16_f32 v242, v8, v9
	v_cvt_pk_bf16_f32 v243, v10, v11
	v_fmac_f32_e32 v250, v8, v8
	v_fmac_f32_e32 v251, v9, v9
	v_fmac_f32_e32 v250, v10, v10
	v_fmac_f32_e32 v251, v11, v11
	v_cvt_pk_bf16_f32 v244, v12, v13
	v_cvt_pk_bf16_f32 v245, v14, v15
	v_fmac_f32_e32 v250, v12, v12
	v_fmac_f32_e32 v251, v13, v13
	v_fmac_f32_e32 v250, v14, v14
	v_fmac_f32_e32 v251, v15, v15
	global_store_dwordx4 v163, v[242:245], s[70:71] offset:1024
	v_cvt_pk_bf16_f32 v238, v16, v17
	v_cvt_pk_bf16_f32 v239, v18, v19
	v_fmac_f32_e32 v250, v16, v16
	v_fmac_f32_e32 v251, v17, v17
	v_fmac_f32_e32 v250, v18, v18
	v_fmac_f32_e32 v251, v19, v19
	v_cvt_pk_bf16_f32 v240, v20, v21
	v_cvt_pk_bf16_f32 v241, v22, v23
	v_fmac_f32_e32 v250, v20, v20
	v_fmac_f32_e32 v251, v21, v21
	v_fmac_f32_e32 v250, v22, v22
	v_fmac_f32_e32 v251, v23, v23
	global_store_dwordx4 v163, v[238:241], s[70:71] offset:2048
	v_cvt_pk_bf16_f32 v242, v24, v25
	v_cvt_pk_bf16_f32 v243, v26, v27
	v_fmac_f32_e32 v250, v24, v24
	v_fmac_f32_e32 v251, v25, v25
	v_fmac_f32_e32 v250, v26, v26
	v_fmac_f32_e32 v251, v27, v27
	v_cvt_pk_bf16_f32 v244, v28, v29
	v_cvt_pk_bf16_f32 v245, v30, v31
	v_fmac_f32_e32 v250, v28, v28
	v_fmac_f32_e32 v251, v29, v29
	v_fmac_f32_e32 v250, v30, v30
	v_fmac_f32_e32 v251, v31, v31
	global_store_dwordx4 v163, v[242:245], s[70:71] offset:3072
	s_add_u32 s70, s70, 0x8000
	s_addc_u32 s71, s71, 0
	v_add_f32_e32 v250, v250, v251
	s_nop 1
	v_add_f32_dpp v218, v250, v250 quad_perm:[1,0,3,2] row_mask:0xf bank_mask:0xf bound_ctrl:1
	s_nop 1
	v_add_f32_dpp v218, v218, v218 quad_perm:[2,3,0,1] row_mask:0xf bank_mask:0xf bound_ctrl:1
	s_nop 1
	v_add_f32_dpp v218, v218, v218 row_ror:4 row_mask:0xf bank_mask:0xf bound_ctrl:1
	s_nop 1
	v_add_f32_dpp v218, v218, v218 row_ror:8 row_mask:0xf bank_mask:0xf bound_ctrl:1
	s_nop 1
	v_readlane_b32 s8, v218, 0
	v_readlane_b32 s9, v218, 16
	v_readlane_b32 s10, v218, 32
	v_readlane_b32 s11, v218, 48
	s_nop 1
	v_mov_b32_e32 v218, s8
	v_add_f32_e32 v218, s9, v218
	v_mov_b32_e32 v219, s10
	v_add_f32_e32 v219, s11, v219
	v_add_f32_e32 v218, v218, v219
	v_mul_f32_e32 v218, 0x3a000000, v218
	v_add_f32_e32 v218, 0x358637bd, v218
	v_rsq_f32_e32 v218, v218
	s_nop 0
	v_mul_f32_e32 v246, v0, v218
	v_mul_f32_e32 v247, v1, v218
	v_mul_f32_e32 v248, v2, v218
	v_mul_f32_e32 v249, v3, v218
	v_fma_f32 v246, v246, v64, v96
	v_fma_f32 v247, v247, v65, v97
	v_fma_f32 v248, v248, v66, v98
	v_fma_f32 v249, v249, v67, v99
	v_cvt_pk_bf16_f32 v238, v246, v247
	v_cvt_pk_bf16_f32 v239, v248, v249
	v_mul_f32_e32 v246, v4, v218
	v_mul_f32_e32 v247, v5, v218
	v_mul_f32_e32 v248, v6, v218
	v_mul_f32_e32 v249, v7, v218
	v_fma_f32 v246, v246, v68, v100
	v_fma_f32 v247, v247, v69, v101
	v_fma_f32 v248, v248, v70, v102
	v_fma_f32 v249, v249, v71, v103
	v_cvt_pk_bf16_f32 v240, v246, v247
	v_cvt_pk_bf16_f32 v241, v248, v249
	global_store_dwordx4 v163, v[238:241], s[72:73]
	v_mul_f32_e32 v246, v8, v218
	v_mul_f32_e32 v247, v9, v218
	v_mul_f32_e32 v248, v10, v218
	v_mul_f32_e32 v249, v11, v218
	v_fma_f32 v246, v246, v72, v104
	v_fma_f32 v247, v247, v73, v105
	v_fma_f32 v248, v248, v74, v106
	v_fma_f32 v249, v249, v75, v107
	v_cvt_pk_bf16_f32 v242, v246, v247
	v_cvt_pk_bf16_f32 v243, v248, v249
	v_mul_f32_e32 v246, v12, v218
	v_mul_f32_e32 v247, v13, v218
	v_mul_f32_e32 v248, v14, v218
	v_mul_f32_e32 v249, v15, v218
	v_fma_f32 v246, v246, v76, v108
	v_fma_f32 v247, v247, v77, v109
	v_fma_f32 v248, v248, v78, v110
	v_fma_f32 v249, v249, v79, v111
	v_cvt_pk_bf16_f32 v244, v246, v247
	v_cvt_pk_bf16_f32 v245, v248, v249
	global_store_dwordx4 v163, v[242:245], s[72:73] offset:1024
	v_mul_f32_e32 v246, v16, v218
	v_mul_f32_e32 v247, v17, v218
	v_mul_f32_e32 v248, v18, v218
	v_mul_f32_e32 v249, v19, v218
	v_fma_f32 v246, v246, v80, v112
	v_fma_f32 v247, v247, v81, v113
	v_fma_f32 v248, v248, v82, v114
	v_fma_f32 v249, v249, v83, v115
	v_cvt_pk_bf16_f32 v238, v246, v247
	v_cvt_pk_bf16_f32 v239, v248, v249
	v_mul_f32_e32 v246, v20, v218
	v_mul_f32_e32 v247, v21, v218
	v_mul_f32_e32 v248, v22, v218
	v_mul_f32_e32 v249, v23, v218
	v_fma_f32 v246, v246, v84, v116
	v_fma_f32 v247, v247, v85, v117
	v_fma_f32 v248, v248, v86, v118
	v_fma_f32 v249, v249, v87, v119
	v_cvt_pk_bf16_f32 v240, v246, v247
	v_cvt_pk_bf16_f32 v241, v248, v249
	global_store_dwordx4 v163, v[238:241], s[72:73] offset:2048
	v_mul_f32_e32 v246, v24, v218
	v_mul_f32_e32 v247, v25, v218
	v_mul_f32_e32 v248, v26, v218
	v_mul_f32_e32 v249, v27, v218
	v_fma_f32 v246, v246, v88, v120
	v_fma_f32 v247, v247, v89, v121
	v_fma_f32 v248, v248, v90, v122
	v_fma_f32 v249, v249, v91, v123
	v_cvt_pk_bf16_f32 v242, v246, v247
	v_cvt_pk_bf16_f32 v243, v248, v249
	v_mul_f32_e32 v246, v28, v218
	v_mul_f32_e32 v247, v29, v218
	v_mul_f32_e32 v248, v30, v218
	v_mul_f32_e32 v249, v31, v218
	v_fma_f32 v246, v246, v92, v124
	v_fma_f32 v247, v247, v93, v125
	v_fma_f32 v248, v248, v94, v126
	v_fma_f32 v249, v249, v95, v127
	v_cvt_pk_bf16_f32 v244, v246, v247
	v_cvt_pk_bf16_f32 v245, v248, v249
	global_store_dwordx4 v163, v[242:245], s[72:73] offset:3072
	s_add_u32 s72, s72, 0x8000
	s_addc_u32 s73, s73, 0
	s_waitcnt vmcnt(20)
	v_mov_b32_e32 v250, 0
	v_mov_b32_e32 v251, 0
	v_lshlrev_b32_e32 v246, 16, v166
	v_and_b32_e32 v247, 0xffff0000, v166
	v_lshlrev_b32_e32 v248, 16, v167
	v_and_b32_e32 v249, 0xffff0000, v167
	v_fmac_f32_e32 v250, v246, v246
	v_fmac_f32_e32 v251, v247, v247
	v_fmac_f32_e32 v250, v248, v248
	v_fmac_f32_e32 v251, v249, v249
	v_lshlrev_b32_e32 v246, 16, v168
	v_and_b32_e32 v247, 0xffff0000, v168
	v_lshlrev_b32_e32 v248, 16, v169
	v_and_b32_e32 v249, 0xffff0000, v169
	v_fmac_f32_e32 v250, v246, v246
	v_fmac_f32_e32 v251, v247, v247
	v_fmac_f32_e32 v250, v248, v248
	v_fmac_f32_e32 v251, v249, v249
	v_lshlrev_b32_e32 v246, 16, v170
	v_and_b32_e32 v247, 0xffff0000, v170
	v_lshlrev_b32_e32 v248, 16, v171
	v_and_b32_e32 v249, 0xffff0000, v171
	v_fmac_f32_e32 v250, v246, v246
	v_fmac_f32_e32 v251, v247, v247
	v_fmac_f32_e32 v250, v248, v248
	v_fmac_f32_e32 v251, v249, v249
	v_lshlrev_b32_e32 v246, 16, v172
	v_and_b32_e32 v247, 0xffff0000, v172
	v_lshlrev_b32_e32 v248, 16, v173
	v_and_b32_e32 v249, 0xffff0000, v173
	v_fmac_f32_e32 v250, v246, v246
	v_fmac_f32_e32 v251, v247, v247
	v_fmac_f32_e32 v250, v248, v248
	v_fmac_f32_e32 v251, v249, v249
	v_lshlrev_b32_e32 v246, 16, v174
	v_and_b32_e32 v247, 0xffff0000, v174
	v_lshlrev_b32_e32 v248, 16, v175
	v_and_b32_e32 v249, 0xffff0000, v175
	v_fmac_f32_e32 v250, v246, v246
	v_fmac_f32_e32 v251, v247, v247
	v_fmac_f32_e32 v250, v248, v248
	v_fmac_f32_e32 v251, v249, v249
	v_lshlrev_b32_e32 v246, 16, v176
	v_and_b32_e32 v247, 0xffff0000, v176
	v_lshlrev_b32_e32 v248, 16, v177
	v_and_b32_e32 v249, 0xffff0000, v177
	v_fmac_f32_e32 v250, v246, v246
	v_fmac_f32_e32 v251, v247, v247
	v_fmac_f32_e32 v250, v248, v248
	v_fmac_f32_e32 v251, v249, v249
	v_lshlrev_b32_e32 v246, 16, v178
	v_and_b32_e32 v247, 0xffff0000, v178
	v_lshlrev_b32_e32 v248, 16, v179
	v_and_b32_e32 v249, 0xffff0000, v179
	v_fmac_f32_e32 v250, v246, v246
	v_fmac_f32_e32 v251, v247, v247
	v_fmac_f32_e32 v250, v248, v248
	v_fmac_f32_e32 v251, v249, v249
	v_lshlrev_b32_e32 v246, 16, v180
	v_and_b32_e32 v247, 0xffff0000, v180
	v_lshlrev_b32_e32 v248, 16, v181
	v_and_b32_e32 v249, 0xffff0000, v181
	v_fmac_f32_e32 v250, v246, v246
	v_fmac_f32_e32 v251, v247, v247
	v_fmac_f32_e32 v250, v248, v248
	v_fmac_f32_e32 v251, v249, v249
	v_add_f32_e32 v250, v250, v251
	s_nop 1
	v_add_f32_dpp v218, v250, v250 quad_perm:[1,0,3,2] row_mask:0xf bank_mask:0xf bound_ctrl:1
	s_nop 1
	v_add_f32_dpp v218, v218, v218 quad_perm:[2,3,0,1] row_mask:0xf bank_mask:0xf bound_ctrl:1
	s_nop 1
	v_add_f32_dpp v218, v218, v218 row_ror:4 row_mask:0xf bank_mask:0xf bound_ctrl:1
	s_nop 1
	v_add_f32_dpp v218, v218, v218 row_ror:8 row_mask:0xf bank_mask:0xf bound_ctrl:1
	s_nop 1
	v_readlane_b32 s8, v218, 0
	v_readlane_b32 s9, v218, 16
	v_readlane_b32 s10, v218, 32
	v_readlane_b32 s11, v218, 48
	s_nop 1
	v_mov_b32_e32 v218, s8
	v_add_f32_e32 v218, s9, v218
	v_mov_b32_e32 v219, s10
	v_add_f32_e32 v219, s11, v219
	v_add_f32_e32 v218, v218, v219
	v_mul_f32_e32 v218, 0x3a000000, v218
	v_add_f32_e32 v218, 0x358637bd, v218
	v_rsq_f32_e32 v218, v218
	s_nop 0
	v_lshlrev_b32_e32 v246, 16, v166
	v_and_b32_e32 v247, 0xffff0000, v166
	v_lshlrev_b32_e32 v248, 16, v167
	v_and_b32_e32 v249, 0xffff0000, v167
	v_mul_f32_e32 v246, v246, v218
	v_mul_f32_e32 v247, v247, v218
	v_mul_f32_e32 v248, v248, v218
	v_mul_f32_e32 v249, v249, v218
	v_fma_f32 v0, v246, v32, v144
	v_fma_f32 v1, v247, v33, v145
	v_fma_f32 v2, v248, v34, v146
	v_fma_f32 v3, v249, v35, v147
	v_lshlrev_b32_e32 v246, 16, v168
	v_and_b32_e32 v247, 0xffff0000, v168
	v_lshlrev_b32_e32 v248, 16, v169
	v_and_b32_e32 v249, 0xffff0000, v169
	v_mul_f32_e32 v246, v246, v218
	v_mul_f32_e32 v247, v247, v218
	v_mul_f32_e32 v248, v248, v218
	v_mul_f32_e32 v249, v249, v218
	v_fma_f32 v4, v246, v36, v148
	v_fma_f32 v5, v247, v37, v149
	v_fma_f32 v6, v248, v38, v150
	v_fma_f32 v7, v249, v39, v151
	v_lshlrev_b32_e32 v246, 16, v170
	v_and_b32_e32 v247, 0xffff0000, v170
	v_lshlrev_b32_e32 v248, 16, v171
	v_and_b32_e32 v249, 0xffff0000, v171
	v_mul_f32_e32 v246, v246, v218
	v_mul_f32_e32 v247, v247, v218
	v_mul_f32_e32 v248, v248, v218
	v_mul_f32_e32 v249, v249, v218
	v_fma_f32 v8, v246, v40, v152
	v_fma_f32 v9, v247, v41, v153
	v_fma_f32 v10, v248, v42, v154
	v_fma_f32 v11, v249, v43, v155
	v_lshlrev_b32_e32 v246, 16, v172
	v_and_b32_e32 v247, 0xffff0000, v172
	v_lshlrev_b32_e32 v248, 16, v173
	v_and_b32_e32 v249, 0xffff0000, v173
	v_mul_f32_e32 v246, v246, v218
	v_mul_f32_e32 v247, v247, v218
	v_mul_f32_e32 v248, v248, v218
	v_mul_f32_e32 v249, v249, v218
	v_fma_f32 v12, v246, v44, v156
	v_fma_f32 v13, v247, v45, v157
	v_fma_f32 v14, v248, v46, v158
	v_fma_f32 v15, v249, v47, v159
	v_lshlrev_b32_e32 v246, 16, v174
	v_and_b32_e32 v247, 0xffff0000, v174
	v_lshlrev_b32_e32 v248, 16, v175
	v_and_b32_e32 v249, 0xffff0000, v175
	v_mul_f32_e32 v246, v246, v218
	v_mul_f32_e32 v247, v247, v218
	v_mul_f32_e32 v248, v248, v218
	v_mul_f32_e32 v249, v249, v218
	v_fma_f32 v16, v246, v48, v182
	v_fma_f32 v17, v247, v49, v183
	v_fma_f32 v18, v248, v50, v184
	v_fma_f32 v19, v249, v51, v185
	v_lshlrev_b32_e32 v246, 16, v176
	v_and_b32_e32 v247, 0xffff0000, v176
	v_lshlrev_b32_e32 v248, 16, v177
	v_and_b32_e32 v249, 0xffff0000, v177
	v_mul_f32_e32 v246, v246, v218
	v_mul_f32_e32 v247, v247, v218
	v_mul_f32_e32 v248, v248, v218
	v_mul_f32_e32 v249, v249, v218
	v_fma_f32 v20, v246, v52, v186
	v_fma_f32 v21, v247, v53, v187
	v_fma_f32 v22, v248, v54, v188
	v_fma_f32 v23, v249, v55, v189
	v_lshlrev_b32_e32 v246, 16, v178
	v_and_b32_e32 v247, 0xffff0000, v178
	v_lshlrev_b32_e32 v248, 16, v179
	v_and_b32_e32 v249, 0xffff0000, v179
	v_mul_f32_e32 v246, v246, v218
	v_mul_f32_e32 v247, v247, v218
	v_mul_f32_e32 v248, v248, v218
	v_mul_f32_e32 v249, v249, v218
	v_fma_f32 v24, v246, v56, v190
	v_fma_f32 v25, v247, v57, v191
	v_fma_f32 v26, v248, v58, v192
	v_fma_f32 v27, v249, v59, v193
	v_lshlrev_b32_e32 v246, 16, v180
	v_and_b32_e32 v247, 0xffff0000, v180
	v_lshlrev_b32_e32 v248, 16, v181
	v_and_b32_e32 v249, 0xffff0000, v181
	v_mul_f32_e32 v246, v246, v218
	v_mul_f32_e32 v247, v247, v218
	v_mul_f32_e32 v248, v248, v218
	v_mul_f32_e32 v249, v249, v218
	v_fma_f32 v28, v246, v60, v194
	v_fma_f32 v29, v247, v61, v195
	v_fma_f32 v30, v248, v62, v196
	v_fma_f32 v31, v249, v63, v197
	global_load_dwordx4 v[166:169], v163, s[56:57]
	global_load_dwordx4 v[170:173], v163, s[56:57] offset:1024
	global_load_dwordx4 v[174:177], v163, s[56:57] offset:2048
	global_load_dwordx4 v[178:181], v163, s[56:57] offset:3072
	global_load_dwordx4 v[144:147], v162, s[58:59]
	global_load_dwordx4 v[148:151], v162, s[58:59] offset:16
	global_load_dwordx4 v[152:155], v162, s[58:59] offset:2048
	global_load_dwordx4 v[156:159], v162, s[58:59] offset:2064
	s_add_u32 s10, s58, 0x1000
	s_addc_u32 s11, s59, 0
	global_load_dwordx4 v[182:185], v162, s[10:11]
	global_load_dwordx4 v[186:189], v162, s[10:11] offset:16
	global_load_dwordx4 v[190:193], v162, s[10:11] offset:2048
	global_load_dwordx4 v[194:197], v162, s[10:11] offset:2064
	s_add_u32 s58, s58, 0x10000
	s_addc_u32 s59, s59, 0
	s_add_u32 s56, s56, 0x8000
	s_addc_u32 s57, s57, 0
	v_mov_b32_e32 v250, 0
	v_mov_b32_e32 v251, 0
	v_cvt_pk_bf16_f32 v238, v0, v1
	v_cvt_pk_bf16_f32 v239, v2, v3
	v_fmac_f32_e32 v250, v0, v0
	v_fmac_f32_e32 v251, v1, v1
	v_fmac_f32_e32 v250, v2, v2
	v_fmac_f32_e32 v251, v3, v3
	v_cvt_pk_bf16_f32 v240, v4, v5
	v_cvt_pk_bf16_f32 v241, v6, v7
	v_fmac_f32_e32 v250, v4, v4
	v_fmac_f32_e32 v251, v5, v5
	v_fmac_f32_e32 v250, v6, v6
	v_fmac_f32_e32 v251, v7, v7
	global_store_dwordx4 v163, v[238:241], s[70:71]
	v_cvt_pk_bf16_f32 v242, v8, v9
	v_cvt_pk_bf16_f32 v243, v10, v11
	v_fmac_f32_e32 v250, v8, v8
	v_fmac_f32_e32 v251, v9, v9
	v_fmac_f32_e32 v250, v10, v10
	v_fmac_f32_e32 v251, v11, v11
	v_cvt_pk_bf16_f32 v244, v12, v13
	v_cvt_pk_bf16_f32 v245, v14, v15
	v_fmac_f32_e32 v250, v12, v12
	v_fmac_f32_e32 v251, v13, v13
	v_fmac_f32_e32 v250, v14, v14
	v_fmac_f32_e32 v251, v15, v15
	global_store_dwordx4 v163, v[242:245], s[70:71] offset:1024
	v_cvt_pk_bf16_f32 v238, v16, v17
	v_cvt_pk_bf16_f32 v239, v18, v19
	v_fmac_f32_e32 v250, v16, v16
	v_fmac_f32_e32 v251, v17, v17
	v_fmac_f32_e32 v250, v18, v18
	v_fmac_f32_e32 v251, v19, v19
	v_cvt_pk_bf16_f32 v240, v20, v21
	v_cvt_pk_bf16_f32 v241, v22, v23
	v_fmac_f32_e32 v250, v20, v20
	v_fmac_f32_e32 v251, v21, v21
	v_fmac_f32_e32 v250, v22, v22
	v_fmac_f32_e32 v251, v23, v23
	global_store_dwordx4 v163, v[238:241], s[70:71] offset:2048
	v_cvt_pk_bf16_f32 v242, v24, v25
	v_cvt_pk_bf16_f32 v243, v26, v27
	v_fmac_f32_e32 v250, v24, v24
	v_fmac_f32_e32 v251, v25, v25
	v_fmac_f32_e32 v250, v26, v26
	v_fmac_f32_e32 v251, v27, v27
	v_cvt_pk_bf16_f32 v244, v28, v29
	v_cvt_pk_bf16_f32 v245, v30, v31
	v_fmac_f32_e32 v250, v28, v28
	v_fmac_f32_e32 v251, v29, v29
	v_fmac_f32_e32 v250, v30, v30
	v_fmac_f32_e32 v251, v31, v31
	global_store_dwordx4 v163, v[242:245], s[70:71] offset:3072
	s_add_u32 s70, s70, 0x8000
	s_addc_u32 s71, s71, 0
	v_add_f32_e32 v250, v250, v251
	s_nop 1
	v_add_f32_dpp v218, v250, v250 quad_perm:[1,0,3,2] row_mask:0xf bank_mask:0xf bound_ctrl:1
	s_nop 1
	v_add_f32_dpp v218, v218, v218 quad_perm:[2,3,0,1] row_mask:0xf bank_mask:0xf bound_ctrl:1
	s_nop 1
	v_add_f32_dpp v218, v218, v218 row_ror:4 row_mask:0xf bank_mask:0xf bound_ctrl:1
	s_nop 1
	v_add_f32_dpp v218, v218, v218 row_ror:8 row_mask:0xf bank_mask:0xf bound_ctrl:1
	s_nop 1
	v_readlane_b32 s8, v218, 0
	v_readlane_b32 s9, v218, 16
	v_readlane_b32 s10, v218, 32
	v_readlane_b32 s11, v218, 48
	s_nop 1
	v_mov_b32_e32 v218, s8
	v_add_f32_e32 v218, s9, v218
	v_mov_b32_e32 v219, s10
	v_add_f32_e32 v219, s11, v219
	v_add_f32_e32 v218, v218, v219
	v_mul_f32_e32 v218, 0x3a000000, v218
	v_add_f32_e32 v218, 0x358637bd, v218
	v_rsq_f32_e32 v218, v218
	s_nop 0
	v_mul_f32_e32 v246, v0, v218
	v_mul_f32_e32 v247, v1, v218
	v_mul_f32_e32 v248, v2, v218
	v_mul_f32_e32 v249, v3, v218
	v_fma_f32 v246, v246, v64, v96
	v_fma_f32 v247, v247, v65, v97
	v_fma_f32 v248, v248, v66, v98
	v_fma_f32 v249, v249, v67, v99
	v_cvt_pk_bf16_f32 v238, v246, v247
	v_cvt_pk_bf16_f32 v239, v248, v249
	v_mul_f32_e32 v246, v4, v218
	v_mul_f32_e32 v247, v5, v218
	v_mul_f32_e32 v248, v6, v218
	v_mul_f32_e32 v249, v7, v218
	v_fma_f32 v246, v246, v68, v100
	v_fma_f32 v247, v247, v69, v101
	v_fma_f32 v248, v248, v70, v102
	v_fma_f32 v249, v249, v71, v103
	v_cvt_pk_bf16_f32 v240, v246, v247
	v_cvt_pk_bf16_f32 v241, v248, v249
	global_store_dwordx4 v163, v[238:241], s[72:73]
	v_mul_f32_e32 v246, v8, v218
	v_mul_f32_e32 v247, v9, v218
	v_mul_f32_e32 v248, v10, v218
	v_mul_f32_e32 v249, v11, v218
	v_fma_f32 v246, v246, v72, v104
	v_fma_f32 v247, v247, v73, v105
	v_fma_f32 v248, v248, v74, v106
	v_fma_f32 v249, v249, v75, v107
	v_cvt_pk_bf16_f32 v242, v246, v247
	v_cvt_pk_bf16_f32 v243, v248, v249
	v_mul_f32_e32 v246, v12, v218
	v_mul_f32_e32 v247, v13, v218
	v_mul_f32_e32 v248, v14, v218
	v_mul_f32_e32 v249, v15, v218
	v_fma_f32 v246, v246, v76, v108
	v_fma_f32 v247, v247, v77, v109
	v_fma_f32 v248, v248, v78, v110
	v_fma_f32 v249, v249, v79, v111
	v_cvt_pk_bf16_f32 v244, v246, v247
	v_cvt_pk_bf16_f32 v245, v248, v249
	global_store_dwordx4 v163, v[242:245], s[72:73] offset:1024
	v_mul_f32_e32 v246, v16, v218
	v_mul_f32_e32 v247, v17, v218
	v_mul_f32_e32 v248, v18, v218
	v_mul_f32_e32 v249, v19, v218
	v_fma_f32 v246, v246, v80, v112
	v_fma_f32 v247, v247, v81, v113
	v_fma_f32 v248, v248, v82, v114
	v_fma_f32 v249, v249, v83, v115
	v_cvt_pk_bf16_f32 v238, v246, v247
	v_cvt_pk_bf16_f32 v239, v248, v249
	v_mul_f32_e32 v246, v20, v218
	v_mul_f32_e32 v247, v21, v218
	v_mul_f32_e32 v248, v22, v218
	v_mul_f32_e32 v249, v23, v218
	v_fma_f32 v246, v246, v84, v116
	v_fma_f32 v247, v247, v85, v117
	v_fma_f32 v248, v248, v86, v118
	v_fma_f32 v249, v249, v87, v119
	v_cvt_pk_bf16_f32 v240, v246, v247
	v_cvt_pk_bf16_f32 v241, v248, v249
	global_store_dwordx4 v163, v[238:241], s[72:73] offset:2048
	v_mul_f32_e32 v246, v24, v218
	v_mul_f32_e32 v247, v25, v218
	v_mul_f32_e32 v248, v26, v218
	v_mul_f32_e32 v249, v27, v218
	v_fma_f32 v246, v246, v88, v120
	v_fma_f32 v247, v247, v89, v121
	v_fma_f32 v248, v248, v90, v122
	v_fma_f32 v249, v249, v91, v123
	v_cvt_pk_bf16_f32 v242, v246, v247
	v_cvt_pk_bf16_f32 v243, v248, v249
	v_mul_f32_e32 v246, v28, v218
	v_mul_f32_e32 v247, v29, v218
	v_mul_f32_e32 v248, v30, v218
	v_mul_f32_e32 v249, v31, v218
	v_fma_f32 v246, v246, v92, v124
	v_fma_f32 v247, v247, v93, v125
	v_fma_f32 v248, v248, v94, v126
	v_fma_f32 v249, v249, v95, v127
	v_cvt_pk_bf16_f32 v244, v246, v247
	v_cvt_pk_bf16_f32 v245, v248, v249
	global_store_dwordx4 v163, v[242:245], s[72:73] offset:3072
	s_add_u32 s72, s72, 0x8000
	s_addc_u32 s73, s73, 0
	s_add_u32 s76, s76, 1
	s_cmp_lt_u32 s76, 7
	s_cbranch_scc1 .Lmp_V2_loop
	s_waitcnt vmcnt(20)
	v_mov_b32_e32 v250, 0
	v_mov_b32_e32 v251, 0
	v_lshlrev_b32_e32 v246, 16, v128
	v_and_b32_e32 v247, 0xffff0000, v128
	v_lshlrev_b32_e32 v248, 16, v129
	v_and_b32_e32 v249, 0xffff0000, v129
	v_fmac_f32_e32 v250, v246, v246
	v_fmac_f32_e32 v251, v247, v247
	v_fmac_f32_e32 v250, v248, v248
	v_fmac_f32_e32 v251, v249, v249
	v_lshlrev_b32_e32 v246, 16, v130
	v_and_b32_e32 v247, 0xffff0000, v130
	v_lshlrev_b32_e32 v248, 16, v131
	v_and_b32_e32 v249, 0xffff0000, v131
	v_fmac_f32_e32 v250, v246, v246
	v_fmac_f32_e32 v251, v247, v247
	v_fmac_f32_e32 v250, v248, v248
	v_fmac_f32_e32 v251, v249, v249
	v_lshlrev_b32_e32 v246, 16, v132
	v_and_b32_e32 v247, 0xffff0000, v132
	v_lshlrev_b32_e32 v248, 16, v133
	v_and_b32_e32 v249, 0xffff0000, v133
	v_fmac_f32_e32 v250, v246, v246
	v_fmac_f32_e32 v251, v247, v247
	v_fmac_f32_e32 v250, v248, v248
	v_fmac_f32_e32 v251, v249, v249
	v_lshlrev_b32_e32 v246, 16, v134
	v_and_b32_e32 v247, 0xffff0000, v134
	v_lshlrev_b32_e32 v248, 16, v135
	v_and_b32_e32 v249, 0xffff0000, v135
	v_fmac_f32_e32 v250, v246, v246
	v_fmac_f32_e32 v251, v247, v247
	v_fmac_f32_e32 v250, v248, v248
	v_fmac_f32_e32 v251, v249, v249
	v_lshlrev_b32_e32 v246, 16, v136
	v_and_b32_e32 v247, 0xffff0000, v136
	v_lshlrev_b32_e32 v248, 16, v137
	v_and_b32_e32 v249, 0xffff0000, v137
	v_fmac_f32_e32 v250, v246, v246
	v_fmac_f32_e32 v251, v247, v247
	v_fmac_f32_e32 v250, v248, v248
	v_fmac_f32_e32 v251, v249, v249
	v_lshlrev_b32_e32 v246, 16, v138
	v_and_b32_e32 v247, 0xffff0000, v138
	v_lshlrev_b32_e32 v248, 16, v139
	v_and_b32_e32 v249, 0xffff0000, v139
	v_fmac_f32_e32 v250, v246, v246
	v_fmac_f32_e32 v251, v247, v247
	v_fmac_f32_e32 v250, v248, v248
	v_fmac_f32_e32 v251, v249, v249
	v_lshlrev_b32_e32 v246, 16, v140
	v_and_b32_e32 v247, 0xffff0000, v140
	v_lshlrev_b32_e32 v248, 16, v141
	v_and_b32_e32 v249, 0xffff0000, v141
	v_fmac_f32_e32 v250, v246, v246
	v_fmac_f32_e32 v251, v247, v247
	v_fmac_f32_e32 v250, v248, v248
	v_fmac_f32_e32 v251, v249, v249
	v_lshlrev_b32_e32 v246, 16, v142
	v_and_b32_e32 v247, 0xffff0000, v142
	v_lshlrev_b32_e32 v248, 16, v143
	v_and_b32_e32 v249, 0xffff0000, v143
	v_fmac_f32_e32 v250, v246, v246
	v_fmac_f32_e32 v251, v247, v247
	v_fmac_f32_e32 v250, v248, v248
	v_fmac_f32_e32 v251, v249, v249
	v_add_f32_e32 v250, v250, v251
	s_nop 1
	v_add_f32_dpp v218, v250, v250 quad_perm:[1,0,3,2] row_mask:0xf bank_mask:0xf bound_ctrl:1
	s_nop 1
	v_add_f32_dpp v218, v218, v218 quad_perm:[2,3,0,1] row_mask:0xf bank_mask:0xf bound_ctrl:1
	s_nop 1
	v_add_f32_dpp v218, v218, v218 row_ror:4 row_mask:0xf bank_mask:0xf bound_ctrl:1
	s_nop 1
	v_add_f32_dpp v218, v218, v218 row_ror:8 row_mask:0xf bank_mask:0xf bound_ctrl:1
	s_nop 1
	v_readlane_b32 s8, v218, 0
	v_readlane_b32 s9, v218, 16
	v_readlane_b32 s10, v218, 32
	v_readlane_b32 s11, v218, 48
	s_nop 1
	v_mov_b32_e32 v218, s8
	v_add_f32_e32 v218, s9, v218
	v_mov_b32_e32 v219, s10
	v_add_f32_e32 v219, s11, v219
	v_add_f32_e32 v218, v218, v219
	v_mul_f32_e32 v218, 0x3a000000, v218
	v_add_f32_e32 v218, 0x358637bd, v218
	v_rsq_f32_e32 v218, v218
	s_nop 0
	v_lshlrev_b32_e32 v246, 16, v128
	v_and_b32_e32 v247, 0xffff0000, v128
	v_lshlrev_b32_e32 v248, 16, v129
	v_and_b32_e32 v249, 0xffff0000, v129
	v_mul_f32_e32 v246, v246, v218
	v_mul_f32_e32 v247, v247, v218
	v_mul_f32_e32 v248, v248, v218
	v_mul_f32_e32 v249, v249, v218
	v_fma_f32 v0, v246, v32, v198
	v_fma_f32 v1, v247, v33, v199
	v_fma_f32 v2, v248, v34, v200
	v_fma_f32 v3, v249, v35, v201
	v_lshlrev_b32_e32 v246, 16, v130
	v_and_b32_e32 v247, 0xffff0000, v130
	v_lshlrev_b32_e32 v248, 16, v131
	v_and_b32_e32 v249, 0xffff0000, v131
	v_mul_f32_e32 v246, v246, v218
	v_mul_f32_e32 v247, v247, v218
	v_mul_f32_e32 v248, v248, v218
	v_mul_f32_e32 v249, v249, v218
	v_fma_f32 v4, v246, v36, v202
	v_fma_f32 v5, v247, v37, v203
	v_fma_f32 v6, v248, v38, v204
	v_fma_f32 v7, v249, v39, v205
	v_lshlrev_b32_e32 v246, 16, v132
	v_and_b32_e32 v247, 0xffff0000, v132
	v_lshlrev_b32_e32 v248, 16, v133
	v_and_b32_e32 v249, 0xffff0000, v133
	v_mul_f32_e32 v246, v246, v218
	v_mul_f32_e32 v247, v247, v218
	v_mul_f32_e32 v248, v248, v218
	v_mul_f32_e32 v249, v249, v218
	v_fma_f32 v8, v246, v40, v206
	v_fma_f32 v9, v247, v41, v207
	v_fma_f32 v10, v248, v42, v208
	v_fma_f32 v11, v249, v43, v209
	v_lshlrev_b32_e32 v246, 16, v134
	v_and_b32_e32 v247, 0xffff0000, v134
	v_lshlrev_b32_e32 v248, 16, v135
	v_and_b32_e32 v249, 0xffff0000, v135
	v_mul_f32_e32 v246, v246, v218
	v_mul_f32_e32 v247, v247, v218
	v_mul_f32_e32 v248, v248, v218
	v_mul_f32_e32 v249, v249, v218
	v_fma_f32 v12, v246, v44, v210
	v_fma_f32 v13, v247, v45, v211
	v_fma_f32 v14, v248, v46, v212
	v_fma_f32 v15, v249, v47, v213
	v_lshlrev_b32_e32 v246, 16, v136
	v_and_b32_e32 v247, 0xffff0000, v136
	v_lshlrev_b32_e32 v248, 16, v137
	v_and_b32_e32 v249, 0xffff0000, v137
	v_mul_f32_e32 v246, v246, v218
	v_mul_f32_e32 v247, v247, v218
	v_mul_f32_e32 v248, v248, v218
	v_mul_f32_e32 v249, v249, v218
	v_fma_f32 v16, v246, v48, v214
	v_fma_f32 v17, v247, v49, v215
	v_fma_f32 v18, v248, v50, v216
	v_fma_f32 v19, v249, v51, v217
	v_lshlrev_b32_e32 v246, 16, v138
	v_and_b32_e32 v247, 0xffff0000, v138
	v_lshlrev_b32_e32 v248, 16, v139
	v_and_b32_e32 v249, 0xffff0000, v139
	v_mul_f32_e32 v246, v246, v218
	v_mul_f32_e32 v247, v247, v218
	v_mul_f32_e32 v248, v248, v218
	v_mul_f32_e32 v249, v249, v218
	v_fma_f32 v20, v246, v52, v226
	v_fma_f32 v21, v247, v53, v227
	v_fma_f32 v22, v248, v54, v228
	v_fma_f32 v23, v249, v55, v229
	v_lshlrev_b32_e32 v246, 16, v140
	v_and_b32_e32 v247, 0xffff0000, v140
	v_lshlrev_b32_e32 v248, 16, v141
	v_and_b32_e32 v249, 0xffff0000, v141
	v_mul_f32_e32 v246, v246, v218
	v_mul_f32_e32 v247, v247, v218
	v_mul_f32_e32 v248, v248, v218
	v_mul_f32_e32 v249, v249, v218
	v_fma_f32 v24, v246, v56, v230
	v_fma_f32 v25, v247, v57, v231
	v_fma_f32 v26, v248, v58, v232
	v_fma_f32 v27, v249, v59, v233
	v_lshlrev_b32_e32 v246, 16, v142
	v_and_b32_e32 v247, 0xffff0000, v142
	v_lshlrev_b32_e32 v248, 16, v143
	v_and_b32_e32 v249, 0xffff0000, v143
	v_mul_f32_e32 v246, v246, v218
	v_mul_f32_e32 v247, v247, v218
	v_mul_f32_e32 v248, v248, v218
	v_mul_f32_e32 v249, v249, v218
	v_fma_f32 v28, v246, v60, v234
	v_fma_f32 v29, v247, v61, v235
	v_fma_f32 v30, v248, v62, v236
	v_fma_f32 v31, v249, v63, v237
	v_mov_b32_e32 v250, 0
	v_mov_b32_e32 v251, 0
	v_cvt_pk_bf16_f32 v238, v0, v1
	v_cvt_pk_bf16_f32 v239, v2, v3
	v_fmac_f32_e32 v250, v0, v0
	v_fmac_f32_e32 v251, v1, v1
	v_fmac_f32_e32 v250, v2, v2
	v_fmac_f32_e32 v251, v3, v3
	v_cvt_pk_bf16_f32 v240, v4, v5
	v_cvt_pk_bf16_f32 v241, v6, v7
	v_fmac_f32_e32 v250, v4, v4
	v_fmac_f32_e32 v251, v5, v5
	v_fmac_f32_e32 v250, v6, v6
	v_fmac_f32_e32 v251, v7, v7
	global_store_dwordx4 v163, v[238:241], s[70:71]
	v_cvt_pk_bf16_f32 v242, v8, v9
	v_cvt_pk_bf16_f32 v243, v10, v11
	v_fmac_f32_e32 v250, v8, v8
	v_fmac_f32_e32 v251, v9, v9
	v_fmac_f32_e32 v250, v10, v10
	v_fmac_f32_e32 v251, v11, v11
	v_cvt_pk_bf16_f32 v244, v12, v13
	v_cvt_pk_bf16_f32 v245, v14, v15
	v_fmac_f32_e32 v250, v12, v12
	v_fmac_f32_e32 v251, v13, v13
	v_fmac_f32_e32 v250, v14, v14
	v_fmac_f32_e32 v251, v15, v15
	global_store_dwordx4 v163, v[242:245], s[70:71] offset:1024
	v_cvt_pk_bf16_f32 v238, v16, v17
	v_cvt_pk_bf16_f32 v239, v18, v19
	v_fmac_f32_e32 v250, v16, v16
	v_fmac_f32_e32 v251, v17, v17
	v_fmac_f32_e32 v250, v18, v18
	v_fmac_f32_e32 v251, v19, v19
	v_cvt_pk_bf16_f32 v240, v20, v21
	v_cvt_pk_bf16_f32 v241, v22, v23
	v_fmac_f32_e32 v250, v20, v20
	v_fmac_f32_e32 v251, v21, v21
	v_fmac_f32_e32 v250, v22, v22
	v_fmac_f32_e32 v251, v23, v23
	global_store_dwordx4 v163, v[238:241], s[70:71] offset:2048
	v_cvt_pk_bf16_f32 v242, v24, v25
	v_cvt_pk_bf16_f32 v243, v26, v27
	v_fmac_f32_e32 v250, v24, v24
	v_fmac_f32_e32 v251, v25, v25
	v_fmac_f32_e32 v250, v26, v26
	v_fmac_f32_e32 v251, v27, v27
	v_cvt_pk_bf16_f32 v244, v28, v29
	v_cvt_pk_bf16_f32 v245, v30, v31
	v_fmac_f32_e32 v250, v28, v28
	v_fmac_f32_e32 v251, v29, v29
	v_fmac_f32_e32 v250, v30, v30
	v_fmac_f32_e32 v251, v31, v31
	global_store_dwordx4 v163, v[242:245], s[70:71] offset:3072
	s_add_u32 s70, s70, 0x8000
	s_addc_u32 s71, s71, 0
	v_add_f32_e32 v250, v250, v251
	s_nop 1
	v_add_f32_dpp v218, v250, v250 quad_perm:[1,0,3,2] row_mask:0xf bank_mask:0xf bound_ctrl:1
	s_nop 1
	v_add_f32_dpp v218, v218, v218 quad_perm:[2,3,0,1] row_mask:0xf bank_mask:0xf bound_ctrl:1
	s_nop 1
	v_add_f32_dpp v218, v218, v218 row_ror:4 row_mask:0xf bank_mask:0xf bound_ctrl:1
	s_nop 1
	v_add_f32_dpp v218, v218, v218 row_ror:8 row_mask:0xf bank_mask:0xf bound_ctrl:1
	s_nop 1
	v_readlane_b32 s8, v218, 0
	v_readlane_b32 s9, v218, 16
	v_readlane_b32 s10, v218, 32
	v_readlane_b32 s11, v218, 48
	s_nop 1
	v_mov_b32_e32 v218, s8
	v_add_f32_e32 v218, s9, v218
	v_mov_b32_e32 v219, s10
	v_add_f32_e32 v219, s11, v219
	v_add_f32_e32 v218, v218, v219
	v_mul_f32_e32 v218, 0x3a000000, v218
	v_add_f32_e32 v218, 0x358637bd, v218
	v_rsq_f32_e32 v218, v218
	s_nop 0
	v_mul_f32_e32 v246, v0, v218
	v_mul_f32_e32 v247, v1, v218
	v_mul_f32_e32 v248, v2, v218
	v_mul_f32_e32 v249, v3, v218
	v_fma_f32 v246, v246, v64, v96
	v_fma_f32 v247, v247, v65, v97
	v_fma_f32 v248, v248, v66, v98
	v_fma_f32 v249, v249, v67, v99
	v_cvt_pk_bf16_f32 v238, v246, v247
	v_cvt_pk_bf16_f32 v239, v248, v249
	v_mul_f32_e32 v246, v4, v218
	v_mul_f32_e32 v247, v5, v218
	v_mul_f32_e32 v248, v6, v218
	v_mul_f32_e32 v249, v7, v218
	v_fma_f32 v246, v246, v68, v100
	v_fma_f32 v247, v247, v69, v101
	v_fma_f32 v248, v248, v70, v102
	v_fma_f32 v249, v249, v71, v103
	v_cvt_pk_bf16_f32 v240, v246, v247
	v_cvt_pk_bf16_f32 v241, v248, v249
	global_store_dwordx4 v163, v[238:241], s[72:73]
	v_mul_f32_e32 v246, v8, v218
	v_mul_f32_e32 v247, v9, v218
	v_mul_f32_e32 v248, v10, v218
	v_mul_f32_e32 v249, v11, v218
	v_fma_f32 v246, v246, v72, v104
	v_fma_f32 v247, v247, v73, v105
	v_fma_f32 v248, v248, v74, v106
	v_fma_f32 v249, v249, v75, v107
	v_cvt_pk_bf16_f32 v242, v246, v247
	v_cvt_pk_bf16_f32 v243, v248, v249
	v_mul_f32_e32 v246, v12, v218
	v_mul_f32_e32 v247, v13, v218
	v_mul_f32_e32 v248, v14, v218
	v_mul_f32_e32 v249, v15, v218
	v_fma_f32 v246, v246, v76, v108
	v_fma_f32 v247, v247, v77, v109
	v_fma_f32 v248, v248, v78, v110
	v_fma_f32 v249, v249, v79, v111
	v_cvt_pk_bf16_f32 v244, v246, v247
	v_cvt_pk_bf16_f32 v245, v248, v249
	global_store_dwordx4 v163, v[242:245], s[72:73] offset:1024
	v_mul_f32_e32 v246, v16, v218
	v_mul_f32_e32 v247, v17, v218
	v_mul_f32_e32 v248, v18, v218
	v_mul_f32_e32 v249, v19, v218
	v_fma_f32 v246, v246, v80, v112
	v_fma_f32 v247, v247, v81, v113
	v_fma_f32 v248, v248, v82, v114
	v_fma_f32 v249, v249, v83, v115
	v_cvt_pk_bf16_f32 v238, v246, v247
	v_cvt_pk_bf16_f32 v239, v248, v249
	v_mul_f32_e32 v246, v20, v218
	v_mul_f32_e32 v247, v21, v218
	v_mul_f32_e32 v248, v22, v218
	v_mul_f32_e32 v249, v23, v218
	v_fma_f32 v246, v246, v84, v116
	v_fma_f32 v247, v247, v85, v117
	v_fma_f32 v248, v248, v86, v118
	v_fma_f32 v249, v249, v87, v119
	v_cvt_pk_bf16_f32 v240, v246, v247
	v_cvt_pk_bf16_f32 v241, v248, v249
	global_store_dwordx4 v163, v[238:241], s[72:73] offset:2048
	v_mul_f32_e32 v246, v24, v218
	v_mul_f32_e32 v247, v25, v218
	v_mul_f32_e32 v248, v26, v218
	v_mul_f32_e32 v249, v27, v218
	v_fma_f32 v246, v246, v88, v120
	v_fma_f32 v247, v247, v89, v121
	v_fma_f32 v248, v248, v90, v122
	v_fma_f32 v249, v249, v91, v123
	v_cvt_pk_bf16_f32 v242, v246, v247
	v_cvt_pk_bf16_f32 v243, v248, v249
	v_mul_f32_e32 v246, v28, v218
	v_mul_f32_e32 v247, v29, v218
	v_mul_f32_e32 v248, v30, v218
	v_mul_f32_e32 v249, v31, v218
	v_fma_f32 v246, v246, v92, v124
	v_fma_f32 v247, v247, v93, v125
	v_fma_f32 v248, v248, v94, v126
	v_fma_f32 v249, v249, v95, v127
	v_cvt_pk_bf16_f32 v244, v246, v247
	v_cvt_pk_bf16_f32 v245, v248, v249
	global_store_dwordx4 v163, v[242:245], s[72:73] offset:3072
	s_add_u32 s72, s72, 0x8000
	s_addc_u32 s73, s73, 0
	s_waitcnt vmcnt(16)
	v_mov_b32_e32 v250, 0
	v_mov_b32_e32 v251, 0
	v_lshlrev_b32_e32 v246, 16, v166
	v_and_b32_e32 v247, 0xffff0000, v166
	v_lshlrev_b32_e32 v248, 16, v167
	v_and_b32_e32 v249, 0xffff0000, v167
	v_fmac_f32_e32 v250, v246, v246
	v_fmac_f32_e32 v251, v247, v247
	v_fmac_f32_e32 v250, v248, v248
	v_fmac_f32_e32 v251, v249, v249
	v_lshlrev_b32_e32 v246, 16, v168
	v_and_b32_e32 v247, 0xffff0000, v168
	v_lshlrev_b32_e32 v248, 16, v169
	v_and_b32_e32 v249, 0xffff0000, v169
	v_fmac_f32_e32 v250, v246, v246
	v_fmac_f32_e32 v251, v247, v247
	v_fmac_f32_e32 v250, v248, v248
	v_fmac_f32_e32 v251, v249, v249
	v_lshlrev_b32_e32 v246, 16, v170
	v_and_b32_e32 v247, 0xffff0000, v170
	v_lshlrev_b32_e32 v248, 16, v171
	v_and_b32_e32 v249, 0xffff0000, v171
	v_fmac_f32_e32 v250, v246, v246
	v_fmac_f32_e32 v251, v247, v247
	v_fmac_f32_e32 v250, v248, v248
	v_fmac_f32_e32 v251, v249, v249
	v_lshlrev_b32_e32 v246, 16, v172
	v_and_b32_e32 v247, 0xffff0000, v172
	v_lshlrev_b32_e32 v248, 16, v173
	v_and_b32_e32 v249, 0xffff0000, v173
	v_fmac_f32_e32 v250, v246, v246
	v_fmac_f32_e32 v251, v247, v247
	v_fmac_f32_e32 v250, v248, v248
	v_fmac_f32_e32 v251, v249, v249
	v_lshlrev_b32_e32 v246, 16, v174
	v_and_b32_e32 v247, 0xffff0000, v174
	v_lshlrev_b32_e32 v248, 16, v175
	v_and_b32_e32 v249, 0xffff0000, v175
	v_fmac_f32_e32 v250, v246, v246
	v_fmac_f32_e32 v251, v247, v247
	v_fmac_f32_e32 v250, v248, v248
	v_fmac_f32_e32 v251, v249, v249
	v_lshlrev_b32_e32 v246, 16, v176
	v_and_b32_e32 v247, 0xffff0000, v176
	v_lshlrev_b32_e32 v248, 16, v177
	v_and_b32_e32 v249, 0xffff0000, v177
	v_fmac_f32_e32 v250, v246, v246
	v_fmac_f32_e32 v251, v247, v247
	v_fmac_f32_e32 v250, v248, v248
	v_fmac_f32_e32 v251, v249, v249
	v_lshlrev_b32_e32 v246, 16, v178
	v_and_b32_e32 v247, 0xffff0000, v178
	v_lshlrev_b32_e32 v248, 16, v179
	v_and_b32_e32 v249, 0xffff0000, v179
	v_fmac_f32_e32 v250, v246, v246
	v_fmac_f32_e32 v251, v247, v247
	v_fmac_f32_e32 v250, v248, v248
	v_fmac_f32_e32 v251, v249, v249
	v_lshlrev_b32_e32 v246, 16, v180
	v_and_b32_e32 v247, 0xffff0000, v180
	v_lshlrev_b32_e32 v248, 16, v181
	v_and_b32_e32 v249, 0xffff0000, v181
	v_fmac_f32_e32 v250, v246, v246
	v_fmac_f32_e32 v251, v247, v247
	v_fmac_f32_e32 v250, v248, v248
	v_fmac_f32_e32 v251, v249, v249
	v_add_f32_e32 v250, v250, v251
	s_nop 1
	v_add_f32_dpp v218, v250, v250 quad_perm:[1,0,3,2] row_mask:0xf bank_mask:0xf bound_ctrl:1
	s_nop 1
	v_add_f32_dpp v218, v218, v218 quad_perm:[2,3,0,1] row_mask:0xf bank_mask:0xf bound_ctrl:1
	s_nop 1
	v_add_f32_dpp v218, v218, v218 row_ror:4 row_mask:0xf bank_mask:0xf bound_ctrl:1
	s_nop 1
	v_add_f32_dpp v218, v218, v218 row_ror:8 row_mask:0xf bank_mask:0xf bound_ctrl:1
	s_nop 1
	v_readlane_b32 s8, v218, 0
	v_readlane_b32 s9, v218, 16
	v_readlane_b32 s10, v218, 32
	v_readlane_b32 s11, v218, 48
	s_nop 1
	v_mov_b32_e32 v218, s8
	v_add_f32_e32 v218, s9, v218
	v_mov_b32_e32 v219, s10
	v_add_f32_e32 v219, s11, v219
	v_add_f32_e32 v218, v218, v219
	v_mul_f32_e32 v218, 0x3a000000, v218
	v_add_f32_e32 v218, 0x358637bd, v218
	v_rsq_f32_e32 v218, v218
	s_nop 0
	v_lshlrev_b32_e32 v246, 16, v166
	v_and_b32_e32 v247, 0xffff0000, v166
	v_lshlrev_b32_e32 v248, 16, v167
	v_and_b32_e32 v249, 0xffff0000, v167
	v_mul_f32_e32 v246, v246, v218
	v_mul_f32_e32 v247, v247, v218
	v_mul_f32_e32 v248, v248, v218
	v_mul_f32_e32 v249, v249, v218
	v_fma_f32 v0, v246, v32, v144
	v_fma_f32 v1, v247, v33, v145
	v_fma_f32 v2, v248, v34, v146
	v_fma_f32 v3, v249, v35, v147
	v_lshlrev_b32_e32 v246, 16, v168
	v_and_b32_e32 v247, 0xffff0000, v168
	v_lshlrev_b32_e32 v248, 16, v169
	v_and_b32_e32 v249, 0xffff0000, v169
	v_mul_f32_e32 v246, v246, v218
	v_mul_f32_e32 v247, v247, v218
	v_mul_f32_e32 v248, v248, v218
	v_mul_f32_e32 v249, v249, v218
	v_fma_f32 v4, v246, v36, v148
	v_fma_f32 v5, v247, v37, v149
	v_fma_f32 v6, v248, v38, v150
	v_fma_f32 v7, v249, v39, v151
	v_lshlrev_b32_e32 v246, 16, v170
	v_and_b32_e32 v247, 0xffff0000, v170
	v_lshlrev_b32_e32 v248, 16, v171
	v_and_b32_e32 v249, 0xffff0000, v171
	v_mul_f32_e32 v246, v246, v218
	v_mul_f32_e32 v247, v247, v218
	v_mul_f32_e32 v248, v248, v218
	v_mul_f32_e32 v249, v249, v218
	v_fma_f32 v8, v246, v40, v152
	v_fma_f32 v9, v247, v41, v153
	v_fma_f32 v10, v248, v42, v154
	v_fma_f32 v11, v249, v43, v155
	v_lshlrev_b32_e32 v246, 16, v172
	v_and_b32_e32 v247, 0xffff0000, v172
	v_lshlrev_b32_e32 v248, 16, v173
	v_and_b32_e32 v249, 0xffff0000, v173
	v_mul_f32_e32 v246, v246, v218
	v_mul_f32_e32 v247, v247, v218
	v_mul_f32_e32 v248, v248, v218
	v_mul_f32_e32 v249, v249, v218
	v_fma_f32 v12, v246, v44, v156
	v_fma_f32 v13, v247, v45, v157
	v_fma_f32 v14, v248, v46, v158
	v_fma_f32 v15, v249, v47, v159
	v_lshlrev_b32_e32 v246, 16, v174
	v_and_b32_e32 v247, 0xffff0000, v174
	v_lshlrev_b32_e32 v248, 16, v175
	v_and_b32_e32 v249, 0xffff0000, v175
	v_mul_f32_e32 v246, v246, v218
	v_mul_f32_e32 v247, v247, v218
	v_mul_f32_e32 v248, v248, v218
	v_mul_f32_e32 v249, v249, v218
	v_fma_f32 v16, v246, v48, v182
	v_fma_f32 v17, v247, v49, v183
	v_fma_f32 v18, v248, v50, v184
	v_fma_f32 v19, v249, v51, v185
	v_lshlrev_b32_e32 v246, 16, v176
	v_and_b32_e32 v247, 0xffff0000, v176
	v_lshlrev_b32_e32 v248, 16, v177
	v_and_b32_e32 v249, 0xffff0000, v177
	v_mul_f32_e32 v246, v246, v218
	v_mul_f32_e32 v247, v247, v218
	v_mul_f32_e32 v248, v248, v218
	v_mul_f32_e32 v249, v249, v218
	v_fma_f32 v20, v246, v52, v186
	v_fma_f32 v21, v247, v53, v187
	v_fma_f32 v22, v248, v54, v188
	v_fma_f32 v23, v249, v55, v189
	v_lshlrev_b32_e32 v246, 16, v178
	v_and_b32_e32 v247, 0xffff0000, v178
	v_lshlrev_b32_e32 v248, 16, v179
	v_and_b32_e32 v249, 0xffff0000, v179
	v_mul_f32_e32 v246, v246, v218
	v_mul_f32_e32 v247, v247, v218
	v_mul_f32_e32 v248, v248, v218
	v_mul_f32_e32 v249, v249, v218
	v_fma_f32 v24, v246, v56, v190
	v_fma_f32 v25, v247, v57, v191
	v_fma_f32 v26, v248, v58, v192
	v_fma_f32 v27, v249, v59, v193
	v_lshlrev_b32_e32 v246, 16, v180
	v_and_b32_e32 v247, 0xffff0000, v180
	v_lshlrev_b32_e32 v248, 16, v181
	v_and_b32_e32 v249, 0xffff0000, v181
	v_mul_f32_e32 v246, v246, v218
	v_mul_f32_e32 v247, v247, v218
	v_mul_f32_e32 v248, v248, v218
	v_mul_f32_e32 v249, v249, v218
	v_fma_f32 v28, v246, v60, v194
	v_fma_f32 v29, v247, v61, v195
	v_fma_f32 v30, v248, v62, v196
	v_fma_f32 v31, v249, v63, v197
	v_mov_b32_e32 v250, 0
	v_mov_b32_e32 v251, 0
	v_cvt_pk_bf16_f32 v238, v0, v1
	v_cvt_pk_bf16_f32 v239, v2, v3
	v_fmac_f32_e32 v250, v0, v0
	v_fmac_f32_e32 v251, v1, v1
	v_fmac_f32_e32 v250, v2, v2
	v_fmac_f32_e32 v251, v3, v3
	v_cvt_pk_bf16_f32 v240, v4, v5
	v_cvt_pk_bf16_f32 v241, v6, v7
	v_fmac_f32_e32 v250, v4, v4
	v_fmac_f32_e32 v251, v5, v5
	v_fmac_f32_e32 v250, v6, v6
	v_fmac_f32_e32 v251, v7, v7
	global_store_dwordx4 v163, v[238:241], s[70:71]
	v_cvt_pk_bf16_f32 v242, v8, v9
	v_cvt_pk_bf16_f32 v243, v10, v11
	v_fmac_f32_e32 v250, v8, v8
	v_fmac_f32_e32 v251, v9, v9
	v_fmac_f32_e32 v250, v10, v10
	v_fmac_f32_e32 v251, v11, v11
	v_cvt_pk_bf16_f32 v244, v12, v13
	v_cvt_pk_bf16_f32 v245, v14, v15
	v_fmac_f32_e32 v250, v12, v12
	v_fmac_f32_e32 v251, v13, v13
	v_fmac_f32_e32 v250, v14, v14
	v_fmac_f32_e32 v251, v15, v15
	global_store_dwordx4 v163, v[242:245], s[70:71] offset:1024
	v_cvt_pk_bf16_f32 v238, v16, v17
	v_cvt_pk_bf16_f32 v239, v18, v19
	v_fmac_f32_e32 v250, v16, v16
	v_fmac_f32_e32 v251, v17, v17
	v_fmac_f32_e32 v250, v18, v18
	v_fmac_f32_e32 v251, v19, v19
	v_cvt_pk_bf16_f32 v240, v20, v21
	v_cvt_pk_bf16_f32 v241, v22, v23
	v_fmac_f32_e32 v250, v20, v20
	v_fmac_f32_e32 v251, v21, v21
	v_fmac_f32_e32 v250, v22, v22
	v_fmac_f32_e32 v251, v23, v23
	global_store_dwordx4 v163, v[238:241], s[70:71] offset:2048
	v_cvt_pk_bf16_f32 v242, v24, v25
	v_cvt_pk_bf16_f32 v243, v26, v27
	v_fmac_f32_e32 v250, v24, v24
	v_fmac_f32_e32 v251, v25, v25
	v_fmac_f32_e32 v250, v26, v26
	v_fmac_f32_e32 v251, v27, v27
	v_cvt_pk_bf16_f32 v244, v28, v29
	v_cvt_pk_bf16_f32 v245, v30, v31
	v_fmac_f32_e32 v250, v28, v28
	v_fmac_f32_e32 v251, v29, v29
	v_fmac_f32_e32 v250, v30, v30
	v_fmac_f32_e32 v251, v31, v31
	global_store_dwordx4 v163, v[242:245], s[70:71] offset:3072
	s_add_u32 s70, s70, 0x8000
	s_addc_u32 s71, s71, 0
	v_add_f32_e32 v250, v250, v251
	s_nop 1
	v_add_f32_dpp v218, v250, v250 quad_perm:[1,0,3,2] row_mask:0xf bank_mask:0xf bound_ctrl:1
	s_nop 1
	v_add_f32_dpp v218, v218, v218 quad_perm:[2,3,0,1] row_mask:0xf bank_mask:0xf bound_ctrl:1
	s_nop 1
	v_add_f32_dpp v218, v218, v218 row_ror:4 row_mask:0xf bank_mask:0xf bound_ctrl:1
	s_nop 1
	v_add_f32_dpp v218, v218, v218 row_ror:8 row_mask:0xf bank_mask:0xf bound_ctrl:1
	s_nop 1
	v_readlane_b32 s8, v218, 0
	v_readlane_b32 s9, v218, 16
	v_readlane_b32 s10, v218, 32
	v_readlane_b32 s11, v218, 48
	s_nop 1
	v_mov_b32_e32 v218, s8
	v_add_f32_e32 v218, s9, v218
	v_mov_b32_e32 v219, s10
	v_add_f32_e32 v219, s11, v219
	v_add_f32_e32 v218, v218, v219
	v_mul_f32_e32 v218, 0x3a000000, v218
	v_add_f32_e32 v218, 0x358637bd, v218
	v_rsq_f32_e32 v218, v218
	s_nop 0
	v_mul_f32_e32 v246, v0, v218
	v_mul_f32_e32 v247, v1, v218
	v_mul_f32_e32 v248, v2, v218
	v_mul_f32_e32 v249, v3, v218
	v_fma_f32 v246, v246, v64, v96
	v_fma_f32 v247, v247, v65, v97
	v_fma_f32 v248, v248, v66, v98
	v_fma_f32 v249, v249, v67, v99
	v_cvt_pk_bf16_f32 v238, v246, v247
	v_cvt_pk_bf16_f32 v239, v248, v249
	v_mul_f32_e32 v246, v4, v218
	v_mul_f32_e32 v247, v5, v218
	v_mul_f32_e32 v248, v6, v218
	v_mul_f32_e32 v249, v7, v218
	v_fma_f32 v246, v246, v68, v100
	v_fma_f32 v247, v247, v69, v101
	v_fma_f32 v248, v248, v70, v102
	v_fma_f32 v249, v249, v71, v103
	v_cvt_pk_bf16_f32 v240, v246, v247
	v_cvt_pk_bf16_f32 v241, v248, v249
	global_store_dwordx4 v163, v[238:241], s[72:73]
	v_mul_f32_e32 v246, v8, v218
	v_mul_f32_e32 v247, v9, v218
	v_mul_f32_e32 v248, v10, v218
	v_mul_f32_e32 v249, v11, v218
	v_fma_f32 v246, v246, v72, v104
	v_fma_f32 v247, v247, v73, v105
	v_fma_f32 v248, v248, v74, v106
	v_fma_f32 v249, v249, v75, v107
	v_cvt_pk_bf16_f32 v242, v246, v247
	v_cvt_pk_bf16_f32 v243, v248, v249
	v_mul_f32_e32 v246, v12, v218
	v_mul_f32_e32 v247, v13, v218
	v_mul_f32_e32 v248, v14, v218
	v_mul_f32_e32 v249, v15, v218
	v_fma_f32 v246, v246, v76, v108
	v_fma_f32 v247, v247, v77, v109
	v_fma_f32 v248, v248, v78, v110
	v_fma_f32 v249, v249, v79, v111
	v_cvt_pk_bf16_f32 v244, v246, v247
	v_cvt_pk_bf16_f32 v245, v248, v249
	global_store_dwordx4 v163, v[242:245], s[72:73] offset:1024
	v_mul_f32_e32 v246, v16, v218
	v_mul_f32_e32 v247, v17, v218
	v_mul_f32_e32 v248, v18, v218
	v_mul_f32_e32 v249, v19, v218
	v_fma_f32 v246, v246, v80, v112
	v_fma_f32 v247, v247, v81, v113
	v_fma_f32 v248, v248, v82, v114
	v_fma_f32 v249, v249, v83, v115
	v_cvt_pk_bf16_f32 v238, v246, v247
	v_cvt_pk_bf16_f32 v239, v248, v249
	v_mul_f32_e32 v246, v20, v218
	v_mul_f32_e32 v247, v21, v218
	v_mul_f32_e32 v248, v22, v218
	v_mul_f32_e32 v249, v23, v218
	v_fma_f32 v246, v246, v84, v116
	v_fma_f32 v247, v247, v85, v117
	v_fma_f32 v248, v248, v86, v118
	v_fma_f32 v249, v249, v87, v119
	v_cvt_pk_bf16_f32 v240, v246, v247
	v_cvt_pk_bf16_f32 v241, v248, v249
	global_store_dwordx4 v163, v[238:241], s[72:73] offset:2048
	v_mul_f32_e32 v246, v24, v218
	v_mul_f32_e32 v247, v25, v218
	v_mul_f32_e32 v248, v26, v218
	v_mul_f32_e32 v249, v27, v218
	v_fma_f32 v246, v246, v88, v120
	v_fma_f32 v247, v247, v89, v121
	v_fma_f32 v248, v248, v90, v122
	v_fma_f32 v249, v249, v91, v123
	v_cvt_pk_bf16_f32 v242, v246, v247
	v_cvt_pk_bf16_f32 v243, v248, v249
	v_mul_f32_e32 v246, v28, v218
	v_mul_f32_e32 v247, v29, v218
	v_mul_f32_e32 v248, v30, v218
	v_mul_f32_e32 v249, v31, v218
	v_fma_f32 v246, v246, v92, v124
	v_fma_f32 v247, v247, v93, v125
	v_fma_f32 v248, v248, v94, v126
	v_fma_f32 v249, v249, v95, v127
	v_cvt_pk_bf16_f32 v244, v246, v247
	v_cvt_pk_bf16_f32 v245, v248, v249
	global_store_dwordx4 v163, v[242:245], s[72:73] offset:3072
	s_add_u32 s72, s72, 0x8000
	s_addc_u32 s73, s73, 0
	s_branch .Lmp_done

.Lmp_V3_loop:
	s_waitcnt vmcnt(16)
	v_mov_b32_e32 v250, 0
	v_mov_b32_e32 v251, 0
	v_lshlrev_b32_e32 v246, 16, v128
	v_and_b32_e32 v247, 0xffff0000, v128
	v_lshlrev_b32_e32 v248, 16, v129
	v_and_b32_e32 v249, 0xffff0000, v129
	v_fmac_f32_e32 v250, v246, v246
	v_fmac_f32_e32 v251, v247, v247
	v_fmac_f32_e32 v250, v248, v248
	v_fmac_f32_e32 v251, v249, v249
	v_lshlrev_b32_e32 v246, 16, v130
	v_and_b32_e32 v247, 0xffff0000, v130
	v_lshlrev_b32_e32 v248, 16, v131
	v_and_b32_e32 v249, 0xffff0000, v131
	v_fmac_f32_e32 v250, v246, v246
	v_fmac_f32_e32 v251, v247, v247
	v_fmac_f32_e32 v250, v248, v248
	v_fmac_f32_e32 v251, v249, v249
	v_lshlrev_b32_e32 v246, 16, v132
	v_and_b32_e32 v247, 0xffff0000, v132
	v_lshlrev_b32_e32 v248, 16, v133
	v_and_b32_e32 v249, 0xffff0000, v133
	v_fmac_f32_e32 v250, v246, v246
	v_fmac_f32_e32 v251, v247, v247
	v_fmac_f32_e32 v250, v248, v248
	v_fmac_f32_e32 v251, v249, v249
	v_lshlrev_b32_e32 v246, 16, v134
	v_and_b32_e32 v247, 0xffff0000, v134
	v_lshlrev_b32_e32 v248, 16, v135
	v_and_b32_e32 v249, 0xffff0000, v135
	v_fmac_f32_e32 v250, v246, v246
	v_fmac_f32_e32 v251, v247, v247
	v_fmac_f32_e32 v250, v248, v248
	v_fmac_f32_e32 v251, v249, v249
	v_lshlrev_b32_e32 v246, 16, v136
	v_and_b32_e32 v247, 0xffff0000, v136
	v_lshlrev_b32_e32 v248, 16, v137
	v_and_b32_e32 v249, 0xffff0000, v137
	v_fmac_f32_e32 v250, v246, v246
	v_fmac_f32_e32 v251, v247, v247
	v_fmac_f32_e32 v250, v248, v248
	v_fmac_f32_e32 v251, v249, v249
	v_lshlrev_b32_e32 v246, 16, v138
	v_and_b32_e32 v247, 0xffff0000, v138
	v_lshlrev_b32_e32 v248, 16, v139
	v_and_b32_e32 v249, 0xffff0000, v139
	v_fmac_f32_e32 v250, v246, v246
	v_fmac_f32_e32 v251, v247, v247
	v_fmac_f32_e32 v250, v248, v248
	v_fmac_f32_e32 v251, v249, v249
	v_lshlrev_b32_e32 v246, 16, v140
	v_and_b32_e32 v247, 0xffff0000, v140
	v_lshlrev_b32_e32 v248, 16, v141
	v_and_b32_e32 v249, 0xffff0000, v141
	v_fmac_f32_e32 v250, v246, v246
	v_fmac_f32_e32 v251, v247, v247
	v_fmac_f32_e32 v250, v248, v248
	v_fmac_f32_e32 v251, v249, v249
	v_lshlrev_b32_e32 v246, 16, v142
	v_and_b32_e32 v247, 0xffff0000, v142
	v_lshlrev_b32_e32 v248, 16, v143
	v_and_b32_e32 v249, 0xffff0000, v143
	v_fmac_f32_e32 v250, v246, v246
	v_fmac_f32_e32 v251, v247, v247
	v_fmac_f32_e32 v250, v248, v248
	v_fmac_f32_e32 v251, v249, v249
	v_add_f32_e32 v250, v250, v251
	s_nop 1
	v_add_f32_dpp v218, v250, v250 quad_perm:[1,0,3,2] row_mask:0xf bank_mask:0xf bound_ctrl:1
	s_nop 1
	v_add_f32_dpp v218, v218, v218 quad_perm:[2,3,0,1] row_mask:0xf bank_mask:0xf bound_ctrl:1
	s_nop 1
	v_add_f32_dpp v218, v218, v218 row_ror:4 row_mask:0xf bank_mask:0xf bound_ctrl:1
	s_nop 1
	v_add_f32_dpp v218, v218, v218 row_ror:8 row_mask:0xf bank_mask:0xf bound_ctrl:1
	s_nop 1
	v_readlane_b32 s8, v218, 0
	v_readlane_b32 s9, v218, 16
	v_readlane_b32 s10, v218, 32
	v_readlane_b32 s11, v218, 48
	s_nop 1
	v_mov_b32_e32 v218, s8
	v_add_f32_e32 v218, s9, v218
	v_mov_b32_e32 v219, s10
	v_add_f32_e32 v219, s11, v219
	v_add_f32_e32 v218, v218, v219
	v_mul_f32_e32 v218, 0x3a000000, v218
	v_add_f32_e32 v218, 0x358637bd, v218
	v_rsq_f32_e32 v218, v218
	s_nop 0
	v_lshlrev_b32_e32 v246, 16, v128
	v_and_b32_e32 v247, 0xffff0000, v128
	v_lshlrev_b32_e32 v248, 16, v129
	v_and_b32_e32 v249, 0xffff0000, v129
	v_mul_f32_e32 v246, v246, v218
	v_mul_f32_e32 v247, v247, v218
	v_mul_f32_e32 v248, v248, v218
	v_mul_f32_e32 v249, v249, v218
	v_lshlrev_b32_e32 v0, 16, v144
	v_and_b32_e32 v1, 0xffff0000, v144
	v_lshlrev_b32_e32 v2, 16, v145
	v_and_b32_e32 v3, 0xffff0000, v145
	v_fmac_f32_e32 v0, v246, v32
	v_fmac_f32_e32 v1, v247, v33
	v_fmac_f32_e32 v2, v248, v34
	v_fmac_f32_e32 v3, v249, v35
	v_lshlrev_b32_e32 v246, 16, v130
	v_and_b32_e32 v247, 0xffff0000, v130
	v_lshlrev_b32_e32 v248, 16, v131
	v_and_b32_e32 v249, 0xffff0000, v131
	v_mul_f32_e32 v246, v246, v218
	v_mul_f32_e32 v247, v247, v218
	v_mul_f32_e32 v248, v248, v218
	v_mul_f32_e32 v249, v249, v218
	v_lshlrev_b32_e32 v4, 16, v146
	v_and_b32_e32 v5, 0xffff0000, v146
	v_lshlrev_b32_e32 v6, 16, v147
	v_and_b32_e32 v7, 0xffff0000, v147
	v_fmac_f32_e32 v4, v246, v36
	v_fmac_f32_e32 v5, v247, v37
	v_fmac_f32_e32 v6, v248, v38
	v_fmac_f32_e32 v7, v249, v39
	v_lshlrev_b32_e32 v246, 16, v132
	v_and_b32_e32 v247, 0xffff0000, v132
	v_lshlrev_b32_e32 v248, 16, v133
	v_and_b32_e32 v249, 0xffff0000, v133
	v_mul_f32_e32 v246, v246, v218
	v_mul_f32_e32 v247, v247, v218
	v_mul_f32_e32 v248, v248, v218
	v_mul_f32_e32 v249, v249, v218
	v_lshlrev_b32_e32 v8, 16, v148
	v_and_b32_e32 v9, 0xffff0000, v148
	v_lshlrev_b32_e32 v10, 16, v149
	v_and_b32_e32 v11, 0xffff0000, v149
	v_fmac_f32_e32 v8, v246, v40
	v_fmac_f32_e32 v9, v247, v41
	v_fmac_f32_e32 v10, v248, v42
	v_fmac_f32_e32 v11, v249, v43
	v_lshlrev_b32_e32 v246, 16, v134
	v_and_b32_e32 v247, 0xffff0000, v134
	v_lshlrev_b32_e32 v248, 16, v135
	v_and_b32_e32 v249, 0xffff0000, v135
	v_mul_f32_e32 v246, v246, v218
	v_mul_f32_e32 v247, v247, v218
	v_mul_f32_e32 v248, v248, v218
	v_mul_f32_e32 v249, v249, v218
	v_lshlrev_b32_e32 v12, 16, v150
	v_and_b32_e32 v13, 0xffff0000, v150
	v_lshlrev_b32_e32 v14, 16, v151
	v_and_b32_e32 v15, 0xffff0000, v151
	v_fmac_f32_e32 v12, v246, v44
	v_fmac_f32_e32 v13, v247, v45
	v_fmac_f32_e32 v14, v248, v46
	v_fmac_f32_e32 v15, v249, v47
	v_lshlrev_b32_e32 v246, 16, v136
	v_and_b32_e32 v247, 0xffff0000, v136
	v_lshlrev_b32_e32 v248, 16, v137
	v_and_b32_e32 v249, 0xffff0000, v137
	v_mul_f32_e32 v246, v246, v218
	v_mul_f32_e32 v247, v247, v218
	v_mul_f32_e32 v248, v248, v218
	v_mul_f32_e32 v249, v249, v218
	v_lshlrev_b32_e32 v16, 16, v152
	v_and_b32_e32 v17, 0xffff0000, v152
	v_lshlrev_b32_e32 v18, 16, v153
	v_and_b32_e32 v19, 0xffff0000, v153
	v_fmac_f32_e32 v16, v246, v48
	v_fmac_f32_e32 v17, v247, v49
	v_fmac_f32_e32 v18, v248, v50
	v_fmac_f32_e32 v19, v249, v51
	v_lshlrev_b32_e32 v246, 16, v138
	v_and_b32_e32 v247, 0xffff0000, v138
	v_lshlrev_b32_e32 v248, 16, v139
	v_and_b32_e32 v249, 0xffff0000, v139
	v_mul_f32_e32 v246, v246, v218
	v_mul_f32_e32 v247, v247, v218
	v_mul_f32_e32 v248, v248, v218
	v_mul_f32_e32 v249, v249, v218
	v_lshlrev_b32_e32 v20, 16, v154
	v_and_b32_e32 v21, 0xffff0000, v154
	v_lshlrev_b32_e32 v22, 16, v155
	v_and_b32_e32 v23, 0xffff0000, v155
	v_fmac_f32_e32 v20, v246, v52
	v_fmac_f32_e32 v21, v247, v53
	v_fmac_f32_e32 v22, v248, v54
	v_fmac_f32_e32 v23, v249, v55
	v_lshlrev_b32_e32 v246, 16, v140
	v_and_b32_e32 v247, 0xffff0000, v140
	v_lshlrev_b32_e32 v248, 16, v141
	v_and_b32_e32 v249, 0xffff0000, v141
	v_mul_f32_e32 v246, v246, v218
	v_mul_f32_e32 v247, v247, v218
	v_mul_f32_e32 v248, v248, v218
	v_mul_f32_e32 v249, v249, v218
	v_lshlrev_b32_e32 v24, 16, v156
	v_and_b32_e32 v25, 0xffff0000, v156
	v_lshlrev_b32_e32 v26, 16, v157
	v_and_b32_e32 v27, 0xffff0000, v157
	v_fmac_f32_e32 v24, v246, v56
	v_fmac_f32_e32 v25, v247, v57
	v_fmac_f32_e32 v26, v248, v58
	v_fmac_f32_e32 v27, v249, v59
	v_lshlrev_b32_e32 v246, 16, v142
	v_and_b32_e32 v247, 0xffff0000, v142
	v_lshlrev_b32_e32 v248, 16, v143
	v_and_b32_e32 v249, 0xffff0000, v143
	v_mul_f32_e32 v246, v246, v218
	v_mul_f32_e32 v247, v247, v218
	v_mul_f32_e32 v248, v248, v218
	v_mul_f32_e32 v249, v249, v218
	v_lshlrev_b32_e32 v28, 16, v158
	v_and_b32_e32 v29, 0xffff0000, v158
	v_lshlrev_b32_e32 v30, 16, v159
	v_and_b32_e32 v31, 0xffff0000, v159
	v_fmac_f32_e32 v28, v246, v60
	v_fmac_f32_e32 v29, v247, v61
	v_fmac_f32_e32 v30, v248, v62
	v_fmac_f32_e32 v31, v249, v63
	global_load_dwordx4 v[128:131], v163, s[56:57]
	global_load_dwordx4 v[132:135], v163, s[56:57] offset:1024
	global_load_dwordx4 v[136:139], v163, s[56:57] offset:2048
	global_load_dwordx4 v[140:143], v163, s[56:57] offset:3072
	global_load_dwordx4 v[144:147], v163, s[58:59]
	global_load_dwordx4 v[148:151], v163, s[58:59] offset:1024
	global_load_dwordx4 v[152:155], v163, s[58:59] offset:2048
	global_load_dwordx4 v[156:159], v163, s[58:59] offset:3072
	s_add_u32 s58, s58, 0x8000
	s_addc_u32 s59, s59, 0
	s_add_u32 s56, s56, 0x8000
	s_addc_u32 s57, s57, 0
	global_store_dwordx4 v162, v[0:3], s[70:71]
	global_store_dwordx4 v162, v[4:7], s[70:71] offset:16
	global_store_dwordx4 v162, v[8:11], s[70:71] offset:2048
	global_store_dwordx4 v162, v[12:15], s[70:71] offset:2064
	s_add_u32 s10, s70, 0x1000
	s_addc_u32 s11, s71, 0
	global_store_dwordx4 v162, v[16:19], s[10:11]
	global_store_dwordx4 v162, v[20:23], s[10:11] offset:16
	global_store_dwordx4 v162, v[24:27], s[10:11] offset:2048
	global_store_dwordx4 v162, v[28:31], s[10:11] offset:2064
	s_add_u32 s70, s70, 0x10000
	s_addc_u32 s71, s71, 0
	s_waitcnt vmcnt(16)
	v_mov_b32_e32 v250, 0
	v_mov_b32_e32 v251, 0
	v_lshlrev_b32_e32 v246, 16, v166
	v_and_b32_e32 v247, 0xffff0000, v166
	v_lshlrev_b32_e32 v248, 16, v167
	v_and_b32_e32 v249, 0xffff0000, v167
	v_fmac_f32_e32 v250, v246, v246
	v_fmac_f32_e32 v251, v247, v247
	v_fmac_f32_e32 v250, v248, v248
	v_fmac_f32_e32 v251, v249, v249
	v_lshlrev_b32_e32 v246, 16, v168
	v_and_b32_e32 v247, 0xffff0000, v168
	v_lshlrev_b32_e32 v248, 16, v169
	v_and_b32_e32 v249, 0xffff0000, v169
	v_fmac_f32_e32 v250, v246, v246
	v_fmac_f32_e32 v251, v247, v247
	v_fmac_f32_e32 v250, v248, v248
	v_fmac_f32_e32 v251, v249, v249
	v_lshlrev_b32_e32 v246, 16, v170
	v_and_b32_e32 v247, 0xffff0000, v170
	v_lshlrev_b32_e32 v248, 16, v171
	v_and_b32_e32 v249, 0xffff0000, v171
	v_fmac_f32_e32 v250, v246, v246
	v_fmac_f32_e32 v251, v247, v247
	v_fmac_f32_e32 v250, v248, v248
	v_fmac_f32_e32 v251, v249, v249
	v_lshlrev_b32_e32 v246, 16, v172
	v_and_b32_e32 v247, 0xffff0000, v172
	v_lshlrev_b32_e32 v248, 16, v173
	v_and_b32_e32 v249, 0xffff0000, v173
	v_fmac_f32_e32 v250, v246, v246
	v_fmac_f32_e32 v251, v247, v247
	v_fmac_f32_e32 v250, v248, v248
	v_fmac_f32_e32 v251, v249, v249
	v_lshlrev_b32_e32 v246, 16, v174
	v_and_b32_e32 v247, 0xffff0000, v174
	v_lshlrev_b32_e32 v248, 16, v175
	v_and_b32_e32 v249, 0xffff0000, v175
	v_fmac_f32_e32 v250, v246, v246
	v_fmac_f32_e32 v251, v247, v247
	v_fmac_f32_e32 v250, v248, v248
	v_fmac_f32_e32 v251, v249, v249
	v_lshlrev_b32_e32 v246, 16, v176
	v_and_b32_e32 v247, 0xffff0000, v176
	v_lshlrev_b32_e32 v248, 16, v177
	v_and_b32_e32 v249, 0xffff0000, v177
	v_fmac_f32_e32 v250, v246, v246
	v_fmac_f32_e32 v251, v247, v247
	v_fmac_f32_e32 v250, v248, v248
	v_fmac_f32_e32 v251, v249, v249
	v_lshlrev_b32_e32 v246, 16, v178
	v_and_b32_e32 v247, 0xffff0000, v178
	v_lshlrev_b32_e32 v248, 16, v179
	v_and_b32_e32 v249, 0xffff0000, v179
	v_fmac_f32_e32 v250, v246, v246
	v_fmac_f32_e32 v251, v247, v247
	v_fmac_f32_e32 v250, v248, v248
	v_fmac_f32_e32 v251, v249, v249
	v_lshlrev_b32_e32 v246, 16, v180
	v_and_b32_e32 v247, 0xffff0000, v180
	v_lshlrev_b32_e32 v248, 16, v181
	v_and_b32_e32 v249, 0xffff0000, v181
	v_fmac_f32_e32 v250, v246, v246
	v_fmac_f32_e32 v251, v247, v247
	v_fmac_f32_e32 v250, v248, v248
	v_fmac_f32_e32 v251, v249, v249
	v_add_f32_e32 v250, v250, v251
	s_nop 1
	v_add_f32_dpp v218, v250, v250 quad_perm:[1,0,3,2] row_mask:0xf bank_mask:0xf bound_ctrl:1
	s_nop 1
	v_add_f32_dpp v218, v218, v218 quad_perm:[2,3,0,1] row_mask:0xf bank_mask:0xf bound_ctrl:1
	s_nop 1
	v_add_f32_dpp v218, v218, v218 row_ror:4 row_mask:0xf bank_mask:0xf bound_ctrl:1
	s_nop 1
	v_add_f32_dpp v218, v218, v218 row_ror:8 row_mask:0xf bank_mask:0xf bound_ctrl:1
	s_nop 1
	v_readlane_b32 s8, v218, 0
	v_readlane_b32 s9, v218, 16
	v_readlane_b32 s10, v218, 32
	v_readlane_b32 s11, v218, 48
	s_nop 1
	v_mov_b32_e32 v218, s8
	v_add_f32_e32 v218, s9, v218
	v_mov_b32_e32 v219, s10
	v_add_f32_e32 v219, s11, v219
	v_add_f32_e32 v218, v218, v219
	v_mul_f32_e32 v218, 0x3a000000, v218
	v_add_f32_e32 v218, 0x358637bd, v218
	v_rsq_f32_e32 v218, v218
	s_nop 0
	v_lshlrev_b32_e32 v246, 16, v166
	v_and_b32_e32 v247, 0xffff0000, v166
	v_lshlrev_b32_e32 v248, 16, v167
	v_and_b32_e32 v249, 0xffff0000, v167
	v_mul_f32_e32 v246, v246, v218
	v_mul_f32_e32 v247, v247, v218
	v_mul_f32_e32 v248, v248, v218
	v_mul_f32_e32 v249, v249, v218
	v_lshlrev_b32_e32 v0, 16, v182
	v_and_b32_e32 v1, 0xffff0000, v182
	v_lshlrev_b32_e32 v2, 16, v183
	v_and_b32_e32 v3, 0xffff0000, v183
	v_fmac_f32_e32 v0, v246, v32
	v_fmac_f32_e32 v1, v247, v33
	v_fmac_f32_e32 v2, v248, v34
	v_fmac_f32_e32 v3, v249, v35
	v_lshlrev_b32_e32 v246, 16, v168
	v_and_b32_e32 v247, 0xffff0000, v168
	v_lshlrev_b32_e32 v248, 16, v169
	v_and_b32_e32 v249, 0xffff0000, v169
	v_mul_f32_e32 v246, v246, v218
	v_mul_f32_e32 v247, v247, v218
	v_mul_f32_e32 v248, v248, v218
	v_mul_f32_e32 v249, v249, v218
	v_lshlrev_b32_e32 v4, 16, v184
	v_and_b32_e32 v5, 0xffff0000, v184
	v_lshlrev_b32_e32 v6, 16, v185
	v_and_b32_e32 v7, 0xffff0000, v185
	v_fmac_f32_e32 v4, v246, v36
	v_fmac_f32_e32 v5, v247, v37
	v_fmac_f32_e32 v6, v248, v38
	v_fmac_f32_e32 v7, v249, v39
	v_lshlrev_b32_e32 v246, 16, v170
	v_and_b32_e32 v247, 0xffff0000, v170
	v_lshlrev_b32_e32 v248, 16, v171
	v_and_b32_e32 v249, 0xffff0000, v171
	v_mul_f32_e32 v246, v246, v218
	v_mul_f32_e32 v247, v247, v218
	v_mul_f32_e32 v248, v248, v218
	v_mul_f32_e32 v249, v249, v218
	v_lshlrev_b32_e32 v8, 16, v186
	v_and_b32_e32 v9, 0xffff0000, v186
	v_lshlrev_b32_e32 v10, 16, v187
	v_and_b32_e32 v11, 0xffff0000, v187
	v_fmac_f32_e32 v8, v246, v40
	v_fmac_f32_e32 v9, v247, v41
	v_fmac_f32_e32 v10, v248, v42
	v_fmac_f32_e32 v11, v249, v43
	v_lshlrev_b32_e32 v246, 16, v172
	v_and_b32_e32 v247, 0xffff0000, v172
	v_lshlrev_b32_e32 v248, 16, v173
	v_and_b32_e32 v249, 0xffff0000, v173
	v_mul_f32_e32 v246, v246, v218
	v_mul_f32_e32 v247, v247, v218
	v_mul_f32_e32 v248, v248, v218
	v_mul_f32_e32 v249, v249, v218
	v_lshlrev_b32_e32 v12, 16, v188
	v_and_b32_e32 v13, 0xffff0000, v188
	v_lshlrev_b32_e32 v14, 16, v189
	v_and_b32_e32 v15, 0xffff0000, v189
	v_fmac_f32_e32 v12, v246, v44
	v_fmac_f32_e32 v13, v247, v45
	v_fmac_f32_e32 v14, v248, v46
	v_fmac_f32_e32 v15, v249, v47
	v_lshlrev_b32_e32 v246, 16, v174
	v_and_b32_e32 v247, 0xffff0000, v174
	v_lshlrev_b32_e32 v248, 16, v175
	v_and_b32_e32 v249, 0xffff0000, v175
	v_mul_f32_e32 v246, v246, v218
	v_mul_f32_e32 v247, v247, v218
	v_mul_f32_e32 v248, v248, v218
	v_mul_f32_e32 v249, v249, v218
	v_lshlrev_b32_e32 v16, 16, v190
	v_and_b32_e32 v17, 0xffff0000, v190
	v_lshlrev_b32_e32 v18, 16, v191
	v_and_b32_e32 v19, 0xffff0000, v191
	v_fmac_f32_e32 v16, v246, v48
	v_fmac_f32_e32 v17, v247, v49
	v_fmac_f32_e32 v18, v248, v50
	v_fmac_f32_e32 v19, v249, v51
	v_lshlrev_b32_e32 v246, 16, v176
	v_and_b32_e32 v247, 0xffff0000, v176
	v_lshlrev_b32_e32 v248, 16, v177
	v_and_b32_e32 v249, 0xffff0000, v177
	v_mul_f32_e32 v246, v246, v218
	v_mul_f32_e32 v247, v247, v218
	v_mul_f32_e32 v248, v248, v218
	v_mul_f32_e32 v249, v249, v218
	v_lshlrev_b32_e32 v20, 16, v192
	v_and_b32_e32 v21, 0xffff0000, v192
	v_lshlrev_b32_e32 v22, 16, v193
	v_and_b32_e32 v23, 0xffff0000, v193
	v_fmac_f32_e32 v20, v246, v52
	v_fmac_f32_e32 v21, v247, v53
	v_fmac_f32_e32 v22, v248, v54
	v_fmac_f32_e32 v23, v249, v55
	v_lshlrev_b32_e32 v246, 16, v178
	v_and_b32_e32 v247, 0xffff0000, v178
	v_lshlrev_b32_e32 v248, 16, v179
	v_and_b32_e32 v249, 0xffff0000, v179
	v_mul_f32_e32 v246, v246, v218
	v_mul_f32_e32 v247, v247, v218
	v_mul_f32_e32 v248, v248, v218
	v_mul_f32_e32 v249, v249, v218
	v_lshlrev_b32_e32 v24, 16, v194
	v_and_b32_e32 v25, 0xffff0000, v194
	v_lshlrev_b32_e32 v26, 16, v195
	v_and_b32_e32 v27, 0xffff0000, v195
	v_fmac_f32_e32 v24, v246, v56
	v_fmac_f32_e32 v25, v247, v57
	v_fmac_f32_e32 v26, v248, v58
	v_fmac_f32_e32 v27, v249, v59
	v_lshlrev_b32_e32 v246, 16, v180
	v_and_b32_e32 v247, 0xffff0000, v180
	v_lshlrev_b32_e32 v248, 16, v181
	v_and_b32_e32 v249, 0xffff0000, v181
	v_mul_f32_e32 v246, v246, v218
	v_mul_f32_e32 v247, v247, v218
	v_mul_f32_e32 v248, v248, v218
	v_mul_f32_e32 v249, v249, v218
	v_lshlrev_b32_e32 v28, 16, v196
	v_and_b32_e32 v29, 0xffff0000, v196
	v_lshlrev_b32_e32 v30, 16, v197
	v_and_b32_e32 v31, 0xffff0000, v197
	v_fmac_f32_e32 v28, v246, v60
	v_fmac_f32_e32 v29, v247, v61
	v_fmac_f32_e32 v30, v248, v62
	v_fmac_f32_e32 v31, v249, v63
	global_load_dwordx4 v[166:169], v163, s[56:57]
	global_load_dwordx4 v[170:173], v163, s[56:57] offset:1024
	global_load_dwordx4 v[174:177], v163, s[56:57] offset:2048
	global_load_dwordx4 v[178:181], v163, s[56:57] offset:3072
	global_load_dwordx4 v[182:185], v163, s[58:59]
	global_load_dwordx4 v[186:189], v163, s[58:59] offset:1024
	global_load_dwordx4 v[190:193], v163, s[58:59] offset:2048
	global_load_dwordx4 v[194:197], v163, s[58:59] offset:3072
	s_add_u32 s58, s58, 0x8000
	s_addc_u32 s59, s59, 0
	s_add_u32 s56, s56, 0x8000
	s_addc_u32 s57, s57, 0
	global_store_dwordx4 v162, v[0:3], s[70:71]
	global_store_dwordx4 v162, v[4:7], s[70:71] offset:16
	global_store_dwordx4 v162, v[8:11], s[70:71] offset:2048
	global_store_dwordx4 v162, v[12:15], s[70:71] offset:2064
	s_add_u32 s10, s70, 0x1000
	s_addc_u32 s11, s71, 0
	global_store_dwordx4 v162, v[16:19], s[10:11]
	global_store_dwordx4 v162, v[20:23], s[10:11] offset:16
	global_store_dwordx4 v162, v[24:27], s[10:11] offset:2048
	global_store_dwordx4 v162, v[28:31], s[10:11] offset:2064
	s_add_u32 s70, s70, 0x10000
	s_addc_u32 s71, s71, 0
	s_add_u32 s76, s76, 1
	s_cmp_lt_u32 s76, 7
	s_cbranch_scc1 .Lmp_V3_loop
	s_waitcnt vmcnt(16)
	v_mov_b32_e32 v250, 0
	v_mov_b32_e32 v251, 0
	v_lshlrev_b32_e32 v246, 16, v128
	v_and_b32_e32 v247, 0xffff0000, v128
	v_lshlrev_b32_e32 v248, 16, v129
	v_and_b32_e32 v249, 0xffff0000, v129
	v_fmac_f32_e32 v250, v246, v246
	v_fmac_f32_e32 v251, v247, v247
	v_fmac_f32_e32 v250, v248, v248
	v_fmac_f32_e32 v251, v249, v249
	v_lshlrev_b32_e32 v246, 16, v130
	v_and_b32_e32 v247, 0xffff0000, v130
	v_lshlrev_b32_e32 v248, 16, v131
	v_and_b32_e32 v249, 0xffff0000, v131
	v_fmac_f32_e32 v250, v246, v246
	v_fmac_f32_e32 v251, v247, v247
	v_fmac_f32_e32 v250, v248, v248
	v_fmac_f32_e32 v251, v249, v249
	v_lshlrev_b32_e32 v246, 16, v132
	v_and_b32_e32 v247, 0xffff0000, v132
	v_lshlrev_b32_e32 v248, 16, v133
	v_and_b32_e32 v249, 0xffff0000, v133
	v_fmac_f32_e32 v250, v246, v246
	v_fmac_f32_e32 v251, v247, v247
	v_fmac_f32_e32 v250, v248, v248
	v_fmac_f32_e32 v251, v249, v249
	v_lshlrev_b32_e32 v246, 16, v134
	v_and_b32_e32 v247, 0xffff0000, v134
	v_lshlrev_b32_e32 v248, 16, v135
	v_and_b32_e32 v249, 0xffff0000, v135
	v_fmac_f32_e32 v250, v246, v246
	v_fmac_f32_e32 v251, v247, v247
	v_fmac_f32_e32 v250, v248, v248
	v_fmac_f32_e32 v251, v249, v249
	v_lshlrev_b32_e32 v246, 16, v136
	v_and_b32_e32 v247, 0xffff0000, v136
	v_lshlrev_b32_e32 v248, 16, v137
	v_and_b32_e32 v249, 0xffff0000, v137
	v_fmac_f32_e32 v250, v246, v246
	v_fmac_f32_e32 v251, v247, v247
	v_fmac_f32_e32 v250, v248, v248
	v_fmac_f32_e32 v251, v249, v249
	v_lshlrev_b32_e32 v246, 16, v138
	v_and_b32_e32 v247, 0xffff0000, v138
	v_lshlrev_b32_e32 v248, 16, v139
	v_and_b32_e32 v249, 0xffff0000, v139
	v_fmac_f32_e32 v250, v246, v246
	v_fmac_f32_e32 v251, v247, v247
	v_fmac_f32_e32 v250, v248, v248
	v_fmac_f32_e32 v251, v249, v249
	v_lshlrev_b32_e32 v246, 16, v140
	v_and_b32_e32 v247, 0xffff0000, v140
	v_lshlrev_b32_e32 v248, 16, v141
	v_and_b32_e32 v249, 0xffff0000, v141
	v_fmac_f32_e32 v250, v246, v246
	v_fmac_f32_e32 v251, v247, v247
	v_fmac_f32_e32 v250, v248, v248
	v_fmac_f32_e32 v251, v249, v249
	v_lshlrev_b32_e32 v246, 16, v142
	v_and_b32_e32 v247, 0xffff0000, v142
	v_lshlrev_b32_e32 v248, 16, v143
	v_and_b32_e32 v249, 0xffff0000, v143
	v_fmac_f32_e32 v250, v246, v246
	v_fmac_f32_e32 v251, v247, v247
	v_fmac_f32_e32 v250, v248, v248
	v_fmac_f32_e32 v251, v249, v249
	v_add_f32_e32 v250, v250, v251
	s_nop 1
	v_add_f32_dpp v218, v250, v250 quad_perm:[1,0,3,2] row_mask:0xf bank_mask:0xf bound_ctrl:1
	s_nop 1
	v_add_f32_dpp v218, v218, v218 quad_perm:[2,3,0,1] row_mask:0xf bank_mask:0xf bound_ctrl:1
	s_nop 1
	v_add_f32_dpp v218, v218, v218 row_ror:4 row_mask:0xf bank_mask:0xf bound_ctrl:1
	s_nop 1
	v_add_f32_dpp v218, v218, v218 row_ror:8 row_mask:0xf bank_mask:0xf bound_ctrl:1
	s_nop 1
	v_readlane_b32 s8, v218, 0
	v_readlane_b32 s9, v218, 16
	v_readlane_b32 s10, v218, 32
	v_readlane_b32 s11, v218, 48
	s_nop 1
	v_mov_b32_e32 v218, s8
	v_add_f32_e32 v218, s9, v218
	v_mov_b32_e32 v219, s10
	v_add_f32_e32 v219, s11, v219
	v_add_f32_e32 v218, v218, v219
	v_mul_f32_e32 v218, 0x3a000000, v218
	v_add_f32_e32 v218, 0x358637bd, v218
	v_rsq_f32_e32 v218, v218
	s_nop 0
	v_lshlrev_b32_e32 v246, 16, v128
	v_and_b32_e32 v247, 0xffff0000, v128
	v_lshlrev_b32_e32 v248, 16, v129
	v_and_b32_e32 v249, 0xffff0000, v129
	v_mul_f32_e32 v246, v246, v218
	v_mul_f32_e32 v247, v247, v218
	v_mul_f32_e32 v248, v248, v218
	v_mul_f32_e32 v249, v249, v218
	v_lshlrev_b32_e32 v0, 16, v144
	v_and_b32_e32 v1, 0xffff0000, v144
	v_lshlrev_b32_e32 v2, 16, v145
	v_and_b32_e32 v3, 0xffff0000, v145
	v_fmac_f32_e32 v0, v246, v32
	v_fmac_f32_e32 v1, v247, v33
	v_fmac_f32_e32 v2, v248, v34
	v_fmac_f32_e32 v3, v249, v35
	v_lshlrev_b32_e32 v246, 16, v130
	v_and_b32_e32 v247, 0xffff0000, v130
	v_lshlrev_b32_e32 v248, 16, v131
	v_and_b32_e32 v249, 0xffff0000, v131
	v_mul_f32_e32 v246, v246, v218
	v_mul_f32_e32 v247, v247, v218
	v_mul_f32_e32 v248, v248, v218
	v_mul_f32_e32 v249, v249, v218
	v_lshlrev_b32_e32 v4, 16, v146
	v_and_b32_e32 v5, 0xffff0000, v146
	v_lshlrev_b32_e32 v6, 16, v147
	v_and_b32_e32 v7, 0xffff0000, v147
	v_fmac_f32_e32 v4, v246, v36
	v_fmac_f32_e32 v5, v247, v37
	v_fmac_f32_e32 v6, v248, v38
	v_fmac_f32_e32 v7, v249, v39
	v_lshlrev_b32_e32 v246, 16, v132
	v_and_b32_e32 v247, 0xffff0000, v132
	v_lshlrev_b32_e32 v248, 16, v133
	v_and_b32_e32 v249, 0xffff0000, v133
	v_mul_f32_e32 v246, v246, v218
	v_mul_f32_e32 v247, v247, v218
	v_mul_f32_e32 v248, v248, v218
	v_mul_f32_e32 v249, v249, v218
	v_lshlrev_b32_e32 v8, 16, v148
	v_and_b32_e32 v9, 0xffff0000, v148
	v_lshlrev_b32_e32 v10, 16, v149
	v_and_b32_e32 v11, 0xffff0000, v149
	v_fmac_f32_e32 v8, v246, v40
	v_fmac_f32_e32 v9, v247, v41
	v_fmac_f32_e32 v10, v248, v42
	v_fmac_f32_e32 v11, v249, v43
	v_lshlrev_b32_e32 v246, 16, v134
	v_and_b32_e32 v247, 0xffff0000, v134
	v_lshlrev_b32_e32 v248, 16, v135
	v_and_b32_e32 v249, 0xffff0000, v135
	v_mul_f32_e32 v246, v246, v218
	v_mul_f32_e32 v247, v247, v218
	v_mul_f32_e32 v248, v248, v218
	v_mul_f32_e32 v249, v249, v218
	v_lshlrev_b32_e32 v12, 16, v150
	v_and_b32_e32 v13, 0xffff0000, v150
	v_lshlrev_b32_e32 v14, 16, v151
	v_and_b32_e32 v15, 0xffff0000, v151
	v_fmac_f32_e32 v12, v246, v44
	v_fmac_f32_e32 v13, v247, v45
	v_fmac_f32_e32 v14, v248, v46
	v_fmac_f32_e32 v15, v249, v47
	v_lshlrev_b32_e32 v246, 16, v136
	v_and_b32_e32 v247, 0xffff0000, v136
	v_lshlrev_b32_e32 v248, 16, v137
	v_and_b32_e32 v249, 0xffff0000, v137
	v_mul_f32_e32 v246, v246, v218
	v_mul_f32_e32 v247, v247, v218
	v_mul_f32_e32 v248, v248, v218
	v_mul_f32_e32 v249, v249, v218
	v_lshlrev_b32_e32 v16, 16, v152
	v_and_b32_e32 v17, 0xffff0000, v152
	v_lshlrev_b32_e32 v18, 16, v153
	v_and_b32_e32 v19, 0xffff0000, v153
	v_fmac_f32_e32 v16, v246, v48
	v_fmac_f32_e32 v17, v247, v49
	v_fmac_f32_e32 v18, v248, v50
	v_fmac_f32_e32 v19, v249, v51
	v_lshlrev_b32_e32 v246, 16, v138
	v_and_b32_e32 v247, 0xffff0000, v138
	v_lshlrev_b32_e32 v248, 16, v139
	v_and_b32_e32 v249, 0xffff0000, v139
	v_mul_f32_e32 v246, v246, v218
	v_mul_f32_e32 v247, v247, v218
	v_mul_f32_e32 v248, v248, v218
	v_mul_f32_e32 v249, v249, v218
	v_lshlrev_b32_e32 v20, 16, v154
	v_and_b32_e32 v21, 0xffff0000, v154
	v_lshlrev_b32_e32 v22, 16, v155
	v_and_b32_e32 v23, 0xffff0000, v155
	v_fmac_f32_e32 v20, v246, v52
	v_fmac_f32_e32 v21, v247, v53
	v_fmac_f32_e32 v22, v248, v54
	v_fmac_f32_e32 v23, v249, v55
	v_lshlrev_b32_e32 v246, 16, v140
	v_and_b32_e32 v247, 0xffff0000, v140
	v_lshlrev_b32_e32 v248, 16, v141
	v_and_b32_e32 v249, 0xffff0000, v141
	v_mul_f32_e32 v246, v246, v218
	v_mul_f32_e32 v247, v247, v218
	v_mul_f32_e32 v248, v248, v218
	v_mul_f32_e32 v249, v249, v218
	v_lshlrev_b32_e32 v24, 16, v156
	v_and_b32_e32 v25, 0xffff0000, v156
	v_lshlrev_b32_e32 v26, 16, v157
	v_and_b32_e32 v27, 0xffff0000, v157
	v_fmac_f32_e32 v24, v246, v56
	v_fmac_f32_e32 v25, v247, v57
	v_fmac_f32_e32 v26, v248, v58
	v_fmac_f32_e32 v27, v249, v59
	v_lshlrev_b32_e32 v246, 16, v142
	v_and_b32_e32 v247, 0xffff0000, v142
	v_lshlrev_b32_e32 v248, 16, v143
	v_and_b32_e32 v249, 0xffff0000, v143
	v_mul_f32_e32 v246, v246, v218
	v_mul_f32_e32 v247, v247, v218
	v_mul_f32_e32 v248, v248, v218
	v_mul_f32_e32 v249, v249, v218
	v_lshlrev_b32_e32 v28, 16, v158
	v_and_b32_e32 v29, 0xffff0000, v158
	v_lshlrev_b32_e32 v30, 16, v159
	v_and_b32_e32 v31, 0xffff0000, v159
	v_fmac_f32_e32 v28, v246, v60
	v_fmac_f32_e32 v29, v247, v61
	v_fmac_f32_e32 v30, v248, v62
	v_fmac_f32_e32 v31, v249, v63
	global_store_dwordx4 v162, v[0:3], s[70:71]
	global_store_dwordx4 v162, v[4:7], s[70:71] offset:16
	global_store_dwordx4 v162, v[8:11], s[70:71] offset:2048
	global_store_dwordx4 v162, v[12:15], s[70:71] offset:2064
	s_add_u32 s10, s70, 0x1000
	s_addc_u32 s11, s71, 0
	global_store_dwordx4 v162, v[16:19], s[10:11]
	global_store_dwordx4 v162, v[20:23], s[10:11] offset:16
	global_store_dwordx4 v162, v[24:27], s[10:11] offset:2048
	global_store_dwordx4 v162, v[28:31], s[10:11] offset:2064
	s_add_u32 s70, s70, 0x10000
	s_addc_u32 s71, s71, 0
	s_waitcnt vmcnt(16)
	v_mov_b32_e32 v250, 0
	v_mov_b32_e32 v251, 0
	v_lshlrev_b32_e32 v246, 16, v166
	v_and_b32_e32 v247, 0xffff0000, v166
	v_lshlrev_b32_e32 v248, 16, v167
	v_and_b32_e32 v249, 0xffff0000, v167
	v_fmac_f32_e32 v250, v246, v246
	v_fmac_f32_e32 v251, v247, v247
	v_fmac_f32_e32 v250, v248, v248
	v_fmac_f32_e32 v251, v249, v249
	v_lshlrev_b32_e32 v246, 16, v168
	v_and_b32_e32 v247, 0xffff0000, v168
	v_lshlrev_b32_e32 v248, 16, v169
	v_and_b32_e32 v249, 0xffff0000, v169
	v_fmac_f32_e32 v250, v246, v246
	v_fmac_f32_e32 v251, v247, v247
	v_fmac_f32_e32 v250, v248, v248
	v_fmac_f32_e32 v251, v249, v249
	v_lshlrev_b32_e32 v246, 16, v170
	v_and_b32_e32 v247, 0xffff0000, v170
	v_lshlrev_b32_e32 v248, 16, v171
	v_and_b32_e32 v249, 0xffff0000, v171
	v_fmac_f32_e32 v250, v246, v246
	v_fmac_f32_e32 v251, v247, v247
	v_fmac_f32_e32 v250, v248, v248
	v_fmac_f32_e32 v251, v249, v249
	v_lshlrev_b32_e32 v246, 16, v172
	v_and_b32_e32 v247, 0xffff0000, v172
	v_lshlrev_b32_e32 v248, 16, v173
	v_and_b32_e32 v249, 0xffff0000, v173
	v_fmac_f32_e32 v250, v246, v246
	v_fmac_f32_e32 v251, v247, v247
	v_fmac_f32_e32 v250, v248, v248
	v_fmac_f32_e32 v251, v249, v249
	v_lshlrev_b32_e32 v246, 16, v174
	v_and_b32_e32 v247, 0xffff0000, v174
	v_lshlrev_b32_e32 v248, 16, v175
	v_and_b32_e32 v249, 0xffff0000, v175
	v_fmac_f32_e32 v250, v246, v246
	v_fmac_f32_e32 v251, v247, v247
	v_fmac_f32_e32 v250, v248, v248
	v_fmac_f32_e32 v251, v249, v249
	v_lshlrev_b32_e32 v246, 16, v176
	v_and_b32_e32 v247, 0xffff0000, v176
	v_lshlrev_b32_e32 v248, 16, v177
	v_and_b32_e32 v249, 0xffff0000, v177
	v_fmac_f32_e32 v250, v246, v246
	v_fmac_f32_e32 v251, v247, v247
	v_fmac_f32_e32 v250, v248, v248
	v_fmac_f32_e32 v251, v249, v249
	v_lshlrev_b32_e32 v246, 16, v178
	v_and_b32_e32 v247, 0xffff0000, v178
	v_lshlrev_b32_e32 v248, 16, v179
	v_and_b32_e32 v249, 0xffff0000, v179
	v_fmac_f32_e32 v250, v246, v246
	v_fmac_f32_e32 v251, v247, v247
	v_fmac_f32_e32 v250, v248, v248
	v_fmac_f32_e32 v251, v249, v249
	v_lshlrev_b32_e32 v246, 16, v180
	v_and_b32_e32 v247, 0xffff0000, v180
	v_lshlrev_b32_e32 v248, 16, v181
	v_and_b32_e32 v249, 0xffff0000, v181
	v_fmac_f32_e32 v250, v246, v246
	v_fmac_f32_e32 v251, v247, v247
	v_fmac_f32_e32 v250, v248, v248
	v_fmac_f32_e32 v251, v249, v249
	v_add_f32_e32 v250, v250, v251
	s_nop 1
	v_add_f32_dpp v218, v250, v250 quad_perm:[1,0,3,2] row_mask:0xf bank_mask:0xf bound_ctrl:1
	s_nop 1
	v_add_f32_dpp v218, v218, v218 quad_perm:[2,3,0,1] row_mask:0xf bank_mask:0xf bound_ctrl:1
	s_nop 1
	v_add_f32_dpp v218, v218, v218 row_ror:4 row_mask:0xf bank_mask:0xf bound_ctrl:1
	s_nop 1
	v_add_f32_dpp v218, v218, v218 row_ror:8 row_mask:0xf bank_mask:0xf bound_ctrl:1
	s_nop 1
	v_readlane_b32 s8, v218, 0
	v_readlane_b32 s9, v218, 16
	v_readlane_b32 s10, v218, 32
	v_readlane_b32 s11, v218, 48
	s_nop 1
	v_mov_b32_e32 v218, s8
	v_add_f32_e32 v218, s9, v218
	v_mov_b32_e32 v219, s10
	v_add_f32_e32 v219, s11, v219
	v_add_f32_e32 v218, v218, v219
	v_mul_f32_e32 v218, 0x3a000000, v218
	v_add_f32_e32 v218, 0x358637bd, v218
	v_rsq_f32_e32 v218, v218
	s_nop 0
	v_lshlrev_b32_e32 v246, 16, v166
	v_and_b32_e32 v247, 0xffff0000, v166
	v_lshlrev_b32_e32 v248, 16, v167
	v_and_b32_e32 v249, 0xffff0000, v167
	v_mul_f32_e32 v246, v246, v218
	v_mul_f32_e32 v247, v247, v218
	v_mul_f32_e32 v248, v248, v218
	v_mul_f32_e32 v249, v249, v218
	v_lshlrev_b32_e32 v0, 16, v182
	v_and_b32_e32 v1, 0xffff0000, v182
	v_lshlrev_b32_e32 v2, 16, v183
	v_and_b32_e32 v3, 0xffff0000, v183
	v_fmac_f32_e32 v0, v246, v32
	v_fmac_f32_e32 v1, v247, v33
	v_fmac_f32_e32 v2, v248, v34
	v_fmac_f32_e32 v3, v249, v35
	v_lshlrev_b32_e32 v246, 16, v168
	v_and_b32_e32 v247, 0xffff0000, v168
	v_lshlrev_b32_e32 v248, 16, v169
	v_and_b32_e32 v249, 0xffff0000, v169
	v_mul_f32_e32 v246, v246, v218
	v_mul_f32_e32 v247, v247, v218
	v_mul_f32_e32 v248, v248, v218
	v_mul_f32_e32 v249, v249, v218
	v_lshlrev_b32_e32 v4, 16, v184
	v_and_b32_e32 v5, 0xffff0000, v184
	v_lshlrev_b32_e32 v6, 16, v185
	v_and_b32_e32 v7, 0xffff0000, v185
	v_fmac_f32_e32 v4, v246, v36
	v_fmac_f32_e32 v5, v247, v37
	v_fmac_f32_e32 v6, v248, v38
	v_fmac_f32_e32 v7, v249, v39
	v_lshlrev_b32_e32 v246, 16, v170
	v_and_b32_e32 v247, 0xffff0000, v170
	v_lshlrev_b32_e32 v248, 16, v171
	v_and_b32_e32 v249, 0xffff0000, v171
	v_mul_f32_e32 v246, v246, v218
	v_mul_f32_e32 v247, v247, v218
	v_mul_f32_e32 v248, v248, v218
	v_mul_f32_e32 v249, v249, v218
	v_lshlrev_b32_e32 v8, 16, v186
	v_and_b32_e32 v9, 0xffff0000, v186
	v_lshlrev_b32_e32 v10, 16, v187
	v_and_b32_e32 v11, 0xffff0000, v187
	v_fmac_f32_e32 v8, v246, v40
	v_fmac_f32_e32 v9, v247, v41
	v_fmac_f32_e32 v10, v248, v42
	v_fmac_f32_e32 v11, v249, v43
	v_lshlrev_b32_e32 v246, 16, v172
	v_and_b32_e32 v247, 0xffff0000, v172
	v_lshlrev_b32_e32 v248, 16, v173
	v_and_b32_e32 v249, 0xffff0000, v173
	v_mul_f32_e32 v246, v246, v218
	v_mul_f32_e32 v247, v247, v218
	v_mul_f32_e32 v248, v248, v218
	v_mul_f32_e32 v249, v249, v218
	v_lshlrev_b32_e32 v12, 16, v188
	v_and_b32_e32 v13, 0xffff0000, v188
	v_lshlrev_b32_e32 v14, 16, v189
	v_and_b32_e32 v15, 0xffff0000, v189
	v_fmac_f32_e32 v12, v246, v44
	v_fmac_f32_e32 v13, v247, v45
	v_fmac_f32_e32 v14, v248, v46
	v_fmac_f32_e32 v15, v249, v47
	v_lshlrev_b32_e32 v246, 16, v174
	v_and_b32_e32 v247, 0xffff0000, v174
	v_lshlrev_b32_e32 v248, 16, v175
	v_and_b32_e32 v249, 0xffff0000, v175
	v_mul_f32_e32 v246, v246, v218
	v_mul_f32_e32 v247, v247, v218
	v_mul_f32_e32 v248, v248, v218
	v_mul_f32_e32 v249, v249, v218
	v_lshlrev_b32_e32 v16, 16, v190
	v_and_b32_e32 v17, 0xffff0000, v190
	v_lshlrev_b32_e32 v18, 16, v191
	v_and_b32_e32 v19, 0xffff0000, v191
	v_fmac_f32_e32 v16, v246, v48
	v_fmac_f32_e32 v17, v247, v49
	v_fmac_f32_e32 v18, v248, v50
	v_fmac_f32_e32 v19, v249, v51
	v_lshlrev_b32_e32 v246, 16, v176
	v_and_b32_e32 v247, 0xffff0000, v176
	v_lshlrev_b32_e32 v248, 16, v177
	v_and_b32_e32 v249, 0xffff0000, v177
	v_mul_f32_e32 v246, v246, v218
	v_mul_f32_e32 v247, v247, v218
	v_mul_f32_e32 v248, v248, v218
	v_mul_f32_e32 v249, v249, v218
	v_lshlrev_b32_e32 v20, 16, v192
	v_and_b32_e32 v21, 0xffff0000, v192
	v_lshlrev_b32_e32 v22, 16, v193
	v_and_b32_e32 v23, 0xffff0000, v193
	v_fmac_f32_e32 v20, v246, v52
	v_fmac_f32_e32 v21, v247, v53
	v_fmac_f32_e32 v22, v248, v54
	v_fmac_f32_e32 v23, v249, v55
	v_lshlrev_b32_e32 v246, 16, v178
	v_and_b32_e32 v247, 0xffff0000, v178
	v_lshlrev_b32_e32 v248, 16, v179
	v_and_b32_e32 v249, 0xffff0000, v179
	v_mul_f32_e32 v246, v246, v218
	v_mul_f32_e32 v247, v247, v218
	v_mul_f32_e32 v248, v248, v218
	v_mul_f32_e32 v249, v249, v218
	v_lshlrev_b32_e32 v24, 16, v194
	v_and_b32_e32 v25, 0xffff0000, v194
	v_lshlrev_b32_e32 v26, 16, v195
	v_and_b32_e32 v27, 0xffff0000, v195
	v_fmac_f32_e32 v24, v246, v56
	v_fmac_f32_e32 v25, v247, v57
	v_fmac_f32_e32 v26, v248, v58
	v_fmac_f32_e32 v27, v249, v59
	v_lshlrev_b32_e32 v246, 16, v180
	v_and_b32_e32 v247, 0xffff0000, v180
	v_lshlrev_b32_e32 v248, 16, v181
	v_and_b32_e32 v249, 0xffff0000, v181
	v_mul_f32_e32 v246, v246, v218
	v_mul_f32_e32 v247, v247, v218
	v_mul_f32_e32 v248, v248, v218
	v_mul_f32_e32 v249, v249, v218
	v_lshlrev_b32_e32 v28, 16, v196
	v_and_b32_e32 v29, 0xffff0000, v196
	v_lshlrev_b32_e32 v30, 16, v197
	v_and_b32_e32 v31, 0xffff0000, v197
	v_fmac_f32_e32 v28, v246, v60
	v_fmac_f32_e32 v29, v247, v61
	v_fmac_f32_e32 v30, v248, v62
	v_fmac_f32_e32 v31, v249, v63
	global_store_dwordx4 v162, v[0:3], s[70:71]
	global_store_dwordx4 v162, v[4:7], s[70:71] offset:16
	global_store_dwordx4 v162, v[8:11], s[70:71] offset:2048
	global_store_dwordx4 v162, v[12:15], s[70:71] offset:2064
	s_add_u32 s10, s70, 0x1000
	s_addc_u32 s11, s71, 0
	global_store_dwordx4 v162, v[16:19], s[10:11]
	global_store_dwordx4 v162, v[20:23], s[10:11] offset:16
	global_store_dwordx4 v162, v[24:27], s[10:11] offset:2048
	global_store_dwordx4 v162, v[28:31], s[10:11] offset:2064
	s_add_u32 s70, s70, 0x10000
	s_addc_u32 s71, s71, 0
	s_branch .Lmp_done
